# expert-weight conversion stream: the once-read f32 weight loads marked non-temporal (nt) so they do not displace the attention K/V working set from L2/Infinity Cache; on top of packed-SwiGLU stack
# baseline (speedup 1.0000x reference)
; #define LAS __attribute__((address_space(3)))
; #define CV_LOAD(qi, Q, D) do { _Pragma("unroll") for (int s_ = 0; s_ < 2; ++s_) _Pragma("unroll") for (int r_ = 0; r_ < 4; ++r_) Q.v[s_][r_] = *(const f32x4*)(D.src + (size_t)(16 * (2 * (qi) + s_) + r_) * D.N); asm volatile("" ::: "memory"); } while (0)
; #define CV_PROC(qi, Q) do { _Pragma("unroll") for (int s_ = 0; s_ < 2; ++s_) _Pragma("unroll") for (int c_ = 0; c_ < 4; ++c_) \
;         *(LAS unsigned*)(scr + (4 * nl + c_) * 132 + 16 * (2 * (qi) + s_) + 4 * kg) = pg8::pk4_fp8c(Q.v[s_][0][c_] * FP8_WSC, Q.v[s_][1][c_] * FP8_WSC, Q.v[s_][2][c_] * FP8_WSC, Q.v[s_][3][c_] * FP8_WSC); asm volatile("" ::: "memory"); } while (0)
; __device__ __forceinline__ void moe_conv_stream(const Args& a, ARGAS unsigned char* ws, LAS unsigned char* scr, int first, int cnt, int lane) {
;     const int nl = lane & 15, kg = lane >> 4, c8 = lane & 7;
;     struct Qt { f32x4 v[2][4]; };
;     ...
;     Qt A, B, C, D4;
;     ConvItem cur = moe_conv_desc(a, ws, first, lane);
;     CV_LOAD(0, A, cur); CV_LOAD(1, B, cur); CV_LOAD(2, C, cur);
; #pragma unroll 1
;     for (int i = 0; i < cnt; ++i) {
;         const ConvItem nxt = moe_conv_desc(a, ws, first + 8 * ((i + 1 < cnt) ? i + 1 : i), lane);
;         CV_LOAD(3, D4, cur); CV_PROC(0, A);
;         CV_LOAD(0, A, nxt);  CV_PROC(1, B);
;         CV_LOAD(1, B, nxt);  CV_PROC(2, C);
;         CV_LOAD(2, C, nxt);  CV_PROC(3, D4);
.LBB0_585:
	v_lshl_add_u64 v[96:97], v[0:1], 0, v[128:129]
	s_lshl_b32 s6, s11, 2
	v_lshl_add_u64 v[0:1], v[96:97], 0, s[6:7]
	s_lshl_b32 s6, s11, 3
	v_lshl_add_u64 v[2:3], v[96:97], 0, s[6:7]
	s_mul_i32 s6, s11, 12
	s_waitcnt vmcnt(26)
	v_lshl_add_u64 v[4:5], v[96:97], 0, s[6:7]
	s_lshl_b32 s6, s11, 6
	v_lshl_add_u64 v[6:7], v[96:97], 0, s[6:7]
	s_mul_i32 s6, s11, 0x44
	s_waitcnt vmcnt(24)
	v_lshl_add_u64 v[12:13], v[96:97], 0, s[6:7]
	s_mul_i32 s6, s11, 0x48
	v_lshl_add_u64 v[14:15], v[96:97], 0, s[6:7]
	s_mul_i32 s6, s11, 0x4c
	s_waitcnt vmcnt(19)
	v_lshl_add_u64 v[32:33], v[96:97], 0, s[6:7]
	s_lshl_b32 s6, s11, 7
	global_load_dwordx4 v[16:19], v[0:1], off nt
	global_load_dwordx4 v[20:23], v[2:3], off nt
	global_load_dwordx4 v[24:27], v[4:5], off nt
	s_nop 0
	global_load_dwordx4 v[0:3], v[6:7], off nt
	s_nop 0
	global_load_dwordx4 v[4:7], v[12:13], off nt
	global_load_dwordx4 v[8:11], v[14:15], off nt
	global_load_dwordx4 v[28:31], v[96:97], off nt
	s_nop 0
	global_load_dwordx4 v[12:15], v[32:33], off nt
	v_lshl_add_u64 v[32:33], v[96:97], 0, s[6:7]
	s_mul_i32 s6, s11, 0x84
	v_lshl_add_u64 v[34:35], v[96:97], 0, s[6:7]
	s_mul_i32 s6, s11, 0x88
	global_load_dwordx4 v[40:43], v[32:33], off nt
	global_load_dwordx4 v[48:51], v[34:35], off nt
	v_lshl_add_u64 v[32:33], v[96:97], 0, s[6:7]
	s_mul_i32 s6, s11, 0x8c
	v_lshl_add_u64 v[34:35], v[96:97], 0, s[6:7]
	s_mul_i32 s6, s11, 0xc0
	s_waitcnt vmcnt(26)
	v_lshl_add_u64 v[44:45], v[96:97], 0, s[6:7]
	s_mul_i32 s6, s11, 0xc4
	v_lshl_add_u64 v[46:47], v[96:97], 0, s[6:7]
	s_mul_i32 s6, s11, 0xc8
	s_waitcnt vmcnt(21)
	v_lshl_add_u64 v[64:65], v[96:97], 0, s[6:7]
	s_mul_i32 s6, s11, 0xcc
	v_lshl_add_u64 v[66:67], v[96:97], 0, s[6:7]
	s_lshl_b32 s6, s11, 8
	global_load_dwordx4 v[60:63], v[32:33], off nt
	global_load_dwordx4 v[56:59], v[34:35], off nt
	s_nop 0
	global_load_dwordx4 v[32:35], v[44:45], off nt
	global_load_dwordx4 v[36:39], v[46:47], off nt
	global_load_dwordx4 v[52:55], v[64:65], off nt
	s_nop 0
	global_load_dwordx4 v[44:47], v[66:67], off nt
	v_lshl_add_u64 v[64:65], v[96:97], 0, s[6:7]
	s_mul_i32 s6, s11, 0x104
	v_lshl_add_u64 v[66:67], v[96:97], 0, s[6:7]
	s_mul_i32 s6, s11, 0x108
	global_load_dwordx4 v[72:75], v[64:65], off nt
	global_load_dwordx4 v[80:83], v[66:67], off nt
	v_lshl_add_u64 v[64:65], v[96:97], 0, s[6:7]
	s_mul_i32 s6, s11, 0x10c
	v_lshl_add_u64 v[66:67], v[96:97], 0, s[6:7]
	s_mul_i32 s6, s11, 0x140
	s_waitcnt vmcnt(26)
	v_lshl_add_u64 v[76:77], v[96:97], 0, s[6:7]
	s_mul_i32 s6, s11, 0x144
	v_lshl_add_u64 v[78:79], v[96:97], 0, s[6:7]
	s_mul_i32 s6, s11, 0x148
	v_lshl_add_u64 v[98:99], v[96:97], 0, s[6:7]
	s_mul_i32 s6, s11, 0x14c
	global_load_dwordx4 v[92:95], v[64:65], off nt
	global_load_dwordx4 v[88:91], v[66:67], off nt
	s_nop 0
	global_load_dwordx4 v[64:67], v[76:77], off nt
	global_load_dwordx4 v[68:71], v[78:79], off nt
	v_lshl_add_u64 v[100:101], v[96:97], 0, s[6:7]
	global_load_dwordx4 v[84:87], v[98:99], off nt
	global_load_dwordx4 v[76:79], v[100:101], off nt
	s_mov_b32 s40, 8
	s_mov_b32 s6, s11
	s_branch .LBB0_587
.LBB0_586:
	s_waitcnt vmcnt(17)
	v_mul_f32_e32 v28, 0x43000000, v28
	v_mul_f32_e32 v16, 0x43000000, v16
	v_med3_f32 v28, v28, s36, v149
	v_med3_f32 v16, v16, s36, v149
	v_mov_b32_e32 v150, v129
	v_cvt_pk_fp8_f32 v150, v28, v16
	v_mul_f32_e32 v20, 0x43000000, v20
	v_mul_f32_e32 v16, 0x43000000, v24
	v_med3_f32 v20, v20, s36, v149
	v_med3_f32 v16, v16, s36, v149
	v_cvt_pk_fp8_f32 v150, v20, v16 op_sel:[0,0,1]
	v_mul_f32_e32 v16, 0x43000000, v29
	v_mul_f32_e32 v17, 0x43000000, v17
	v_mul_f32_e32 v20, 0x43000000, v21
	v_med3_f32 v16, v16, s36, v149
	v_med3_f32 v17, v17, s36, v149
	v_mov_b32_e32 v21, v129
	v_cvt_pk_fp8_f32 v21, v16, v17
	v_mul_f32_e32 v16, 0x43000000, v25
	v_med3_f32 v17, v20, s36, v149
	v_med3_f32 v16, v16, s36, v149
	v_cvt_pk_fp8_f32 v21, v17, v16 op_sel:[0,0,1]
	v_mul_f32_e32 v16, 0x43000000, v30
	v_mul_f32_e32 v17, 0x43000000, v18
	v_med3_f32 v16, v16, s36, v149
	v_med3_f32 v17, v17, s36, v149
	v_mov_b32_e32 v20, v129
	v_cvt_pk_fp8_f32 v20, v16, v17
	v_mul_f32_e32 v18, 0x43000000, v22
	v_mul_f32_e32 v16, 0x43000000, v26
	v_med3_f32 v17, v18, s36, v149
	v_med3_f32 v16, v16, s36, v149
	v_cvt_pk_fp8_f32 v20, v17, v16 op_sel:[0,0,1]
	v_mul_f32_e32 v16, 0x43000000, v31
	v_mul_f32_e32 v17, 0x43000000, v19
	v_med3_f32 v16, v16, s36, v149
	v_med3_f32 v17, v17, s36, v149
	v_mov_b32_e32 v19, v129
	v_cvt_pk_fp8_f32 v19, v16, v17
	v_mul_f32_e32 v18, 0x43000000, v23
	v_mul_f32_e32 v16, 0x43000000, v27
	v_med3_f32 v17, v18, s36, v149
	v_med3_f32 v16, v16, s36, v149
	v_mul_f32_e32 v0, 0x43000000, v0
	v_mul_f32_e32 v4, 0x43000000, v4
	v_cvt_pk_fp8_f32 v19, v17, v16 op_sel:[0,0,1]
	v_med3_f32 v0, v0, s36, v149
	v_med3_f32 v4, v4, s36, v149
	v_mov_b32_e32 v16, v129
	v_cvt_pk_fp8_f32 v16, v0, v4
	v_mul_f32_e32 v8, 0x43000000, v8
	s_waitcnt vmcnt(16)
; #define CV_LOAD(qi, Q, D) do { _Pragma("unroll") for (int s_ = 0; s_ < 2; ++s_) _Pragma("unroll") for (int r_ = 0; r_ < 4; ++r_) Q.v[s_][r_] = *(const f32x4*)(D.src + (size_t)(16 * (2 * (qi) + s_) + r_) * D.N); asm volatile("" ::: "memory"); } while (0)
; #define CV_PROC(qi, Q) do { _Pragma("unroll") for (int s_ = 0; s_ < 2; ++s_) _Pragma("unroll") for (int c_ = 0; c_ < 4; ++c_) \
;         *(LAS unsigned*)(scr + (4 * nl + c_) * 132 + 16 * (2 * (qi) + s_) + 4 * kg) = pg8::pk4_fp8c(Q.v[s_][0][c_] * FP8_WSC, Q.v[s_][1][c_] * FP8_WSC, Q.v[s_][2][c_] * FP8_WSC, Q.v[s_][3][c_] * FP8_WSC); asm volatile("" ::: "memory"); } while (0)
; __device__ __forceinline__ void moe_conv_stream(const Args& a, ARGAS unsigned char* ws, LAS unsigned char* scr, int first, int cnt, int lane) {
;     ...
;     Qt A, B, C, D4;
;     ConvItem cur = moe_conv_desc(a, ws, first, lane);
;     CV_LOAD(0, A, cur); CV_LOAD(1, B, cur); CV_LOAD(2, C, cur);
; #pragma unroll 1
;     for (int i = 0; i < cnt; ++i) {
;         const ConvItem nxt = moe_conv_desc(a, ws, first + 8 * ((i + 1 < cnt) ? i + 1 : i), lane);
;         CV_LOAD(3, D4, cur); CV_PROC(0, A);
;         CV_LOAD(0, A, nxt);  CV_PROC(1, B);
;         CV_LOAD(1, B, nxt);  CV_PROC(2, C);
;         CV_LOAD(2, C, nxt);  CV_PROC(3, D4);
	v_mul_f32_e32 v0, 0x43000000, v12
	v_med3_f32 v4, v8, s36, v149
	v_med3_f32 v0, v0, s36, v149
	v_cvt_pk_fp8_f32 v16, v4, v0 op_sel:[0,0,1]
	v_mul_f32_e32 v0, 0x43000000, v1
	v_mul_f32_e32 v1, 0x43000000, v5
	v_med3_f32 v0, v0, s36, v149
	v_med3_f32 v1, v1, s36, v149
	v_mov_b32_e32 v5, v129
	v_cvt_pk_fp8_f32 v5, v0, v1
	v_mul_f32_e32 v4, 0x43000000, v9
	v_mul_f32_e32 v0, 0x43000000, v13
	v_med3_f32 v1, v4, s36, v149
	v_med3_f32 v0, v0, s36, v149
	v_cvt_pk_fp8_f32 v5, v1, v0 op_sel:[0,0,1]
	v_mul_f32_e32 v0, 0x43000000, v2
	v_mul_f32_e32 v1, 0x43000000, v6
	v_med3_f32 v0, v0, s36, v149
	v_med3_f32 v1, v1, s36, v149
	v_mov_b32_e32 v4, v129
	v_cvt_pk_fp8_f32 v4, v0, v1
	v_mad_u64_u32 v[96:97], s[14:15], s6, v148, v[96:97]
	v_mul_f32_e32 v2, 0x43000000, v10
	v_mul_f32_e32 v0, 0x43000000, v14
	s_lshl_b64 s[14:15], s[6:7], 2
	v_med3_f32 v1, v2, s36, v149
	v_med3_f32 v0, v0, s36, v149
	v_lshl_add_u64 v[132:133], v[98:99], 0, v[128:129]
	v_lshl_add_u64 v[98:99], v[96:97], 0, s[14:15]
	v_cvt_pk_fp8_f32 v4, v1, v0 op_sel:[0,0,1]
	v_mul_f32_e32 v0, 0x43000000, v3
	v_mul_f32_e32 v1, 0x43000000, v7
	global_load_dwordx4 v[116:119], v[96:97], off nt
	global_load_dwordx4 v[120:123], v[98:99], off nt
	v_lshl_add_u64 v[96:97], v[98:99], 0, s[14:15]
	v_med3_f32 v0, v0, s36, v149
	v_med3_f32 v1, v1, s36, v149
	v_mov_b32_e32 v3, v129
	v_lshl_add_u64 v[98:99], v[96:97], 0, s[14:15]
	v_cvt_pk_fp8_f32 v3, v0, v1
	global_load_dwordx4 v[124:127], v[96:97], off nt
	global_load_dwordx4 v[112:115], v[98:99], off nt
	v_mad_u64_u32 v[96:97], s[42:43], s6, 52, v[98:99]
	v_lshl_add_u64 v[98:99], v[96:97], 0, s[14:15]
	v_mul_f32_e32 v2, 0x43000000, v11
	v_mul_f32_e32 v0, 0x43000000, v15
	global_load_dwordx4 v[100:103], v[96:97], off nt
	global_load_dwordx4 v[104:107], v[98:99], off nt
	v_lshl_add_u64 v[96:97], v[98:99], 0, s[14:15]
	v_med3_f32 v1, v2, s36, v149
	v_med3_f32 v0, v0, s36, v149
	v_lshl_add_u64 v[98:99], v[96:97], 0, s[14:15]
	v_cvt_pk_fp8_f32 v3, v1, v0 op_sel:[0,0,1]
	s_waitcnt vmcnt(21)
	v_mul_f32_e32 v40, 0x43000000, v40
	s_waitcnt vmcnt(20)
	v_mul_f32_e32 v48, 0x43000000, v48
	global_load_dwordx4 v[108:111], v[96:97], off nt
	s_nop 0
	global_load_dwordx4 v[96:99], v[98:99], off nt
	ds_write2_b32 v145, v150, v16 offset1:4
	ds_write2_b32 v145, v21, v5 offset0:33 offset1:37
	ds_write2_b32 v145, v20, v4 offset0:66 offset1:70
	ds_write2_b32 v145, v19, v3 offset0:99 offset1:103
	v_med3_f32 v40, v40, s36, v149
	v_med3_f32 v48, v48, s36, v149
	v_mov_b32_e32 v150, v129
	v_cvt_pk_fp8_f32 v150, v40, v48
	s_waitcnt vmcnt(21)
	v_mul_f32_e32 v60, 0x43000000, v60
	s_waitcnt vmcnt(20)
	v_mul_f32_e32 v40, 0x43000000, v56
	v_med3_f32 v48, v60, s36, v149
	v_med3_f32 v40, v40, s36, v149
	v_cvt_pk_fp8_f32 v150, v48, v40 op_sel:[0,0,1]
	v_mul_f32_e32 v40, 0x43000000, v41
	v_mul_f32_e32 v41, 0x43000000, v49
	v_med3_f32 v40, v40, s36, v149
	v_med3_f32 v41, v41, s36, v149
	v_mov_b32_e32 v49, v129
	v_cvt_pk_fp8_f32 v49, v40, v41
	v_mul_f32_e32 v48, 0x43000000, v61
	v_mul_f32_e32 v40, 0x43000000, v57
	v_med3_f32 v41, v48, s36, v149
	v_med3_f32 v40, v40, s36, v149
	v_cvt_pk_fp8_f32 v49, v41, v40 op_sel:[0,0,1]
	v_mul_f32_e32 v40, 0x43000000, v42
	v_mul_f32_e32 v41, 0x43000000, v50
	v_med3_f32 v40, v40, s36, v149
	v_med3_f32 v41, v41, s36, v149
	v_mov_b32_e32 v48, v129
	v_cvt_pk_fp8_f32 v48, v40, v41
	v_mul_f32_e32 v42, 0x43000000, v62
	v_mul_f32_e32 v40, 0x43000000, v58
	v_med3_f32 v41, v42, s36, v149
	v_med3_f32 v40, v40, s36, v149
	v_cvt_pk_fp8_f32 v48, v41, v40 op_sel:[0,0,1]
	v_mul_f32_e32 v40, 0x43000000, v43
	v_mul_f32_e32 v41, 0x43000000, v51
	v_med3_f32 v40, v40, s36, v149
	v_med3_f32 v41, v41, s36, v149
	v_mov_b32_e32 v43, v129
	v_cvt_pk_fp8_f32 v43, v40, v41
	v_mul_f32_e32 v42, 0x43000000, v63
	v_mul_f32_e32 v40, 0x43000000, v59
	v_med3_f32 v41, v42, s36, v149
	v_med3_f32 v40, v40, s36, v149
	s_waitcnt vmcnt(19)
	v_mul_f32_e32 v32, 0x43000000, v32
	s_waitcnt vmcnt(18)
	v_mul_f32_e32 v36, 0x43000000, v36
	v_cvt_pk_fp8_f32 v43, v41, v40 op_sel:[0,0,1]
	v_med3_f32 v32, v32, s36, v149
	v_med3_f32 v36, v36, s36, v149
	v_mov_b32_e32 v41, v129
	v_cvt_pk_fp8_f32 v41, v32, v36
	s_waitcnt vmcnt(17)
	v_mul_f32_e32 v40, 0x43000000, v52
	s_waitcnt vmcnt(16)
	v_mul_f32_e32 v32, 0x43000000, v44
	v_med3_f32 v36, v40, s36, v149
	v_med3_f32 v32, v32, s36, v149
	v_cvt_pk_fp8_f32 v41, v36, v32 op_sel:[0,0,1]
	v_mul_f32_e32 v32, 0x43000000, v33
	v_mul_f32_e32 v33, 0x43000000, v37
	v_med3_f32 v32, v32, s36, v149
	v_med3_f32 v33, v33, s36, v149
	v_mov_b32_e32 v37, v129
	v_cvt_pk_fp8_f32 v37, v32, v33
	v_mul_f32_e32 v36, 0x43000000, v53
	v_mul_f32_e32 v32, 0x43000000, v45
	v_med3_f32 v33, v36, s36, v149
	v_med3_f32 v32, v32, s36, v149
	v_cvt_pk_fp8_f32 v37, v33, v32 op_sel:[0,0,1]
	v_mul_f32_e32 v32, 0x43000000, v34
	v_mul_f32_e32 v33, 0x43000000, v38
	v_med3_f32 v32, v32, s36, v149
	v_med3_f32 v33, v33, s36, v149
	v_mov_b32_e32 v36, v129
	v_cvt_pk_fp8_f32 v36, v32, v33
	v_mul_f32_e32 v34, 0x43000000, v54
	v_mul_f32_e32 v32, 0x43000000, v46
	s_lshl_b32 s6, s13, 2
	v_med3_f32 v33, v34, s36, v149
	v_med3_f32 v32, v32, s36, v149
	v_lshl_add_u64 v[0:1], v[132:133], 0, s[6:7]
	s_lshl_b32 s6, s13, 3
	v_cvt_pk_fp8_f32 v36, v33, v32 op_sel:[0,0,1]
	v_mul_f32_e32 v32, 0x43000000, v35
	v_mul_f32_e32 v33, 0x43000000, v39
	global_load_dwordx4 v[28:31], v[132:133], off nt
	global_load_dwordx4 v[16:19], v[0:1], off nt
	v_lshl_add_u64 v[0:1], v[132:133], 0, s[6:7]
	s_mul_i32 s6, s13, 12
	v_med3_f32 v32, v32, s36, v149
	v_med3_f32 v33, v33, s36, v149
	v_mov_b32_e32 v35, v129
	v_lshl_add_u64 v[2:3], v[132:133], 0, s[6:7]
	s_lshl_b32 s6, s13, 6
	v_cvt_pk_fp8_f32 v35, v32, v33
	global_load_dwordx4 v[20:23], v[0:1], off nt
	global_load_dwordx4 v[24:27], v[2:3], off nt
	v_lshl_add_u64 v[0:1], v[132:133], 0, s[6:7]
	s_mul_i32 s6, s13, 0x44
	v_lshl_add_u64 v[4:5], v[132:133], 0, s[6:7]
	s_mul_i32 s6, s13, 0x48
	v_mul_f32_e32 v34, 0x43000000, v55
	v_mul_f32_e32 v32, 0x43000000, v47
	v_lshl_add_u64 v[8:9], v[132:133], 0, s[6:7]
	s_mul_i32 s6, s13, 0x4c
	v_med3_f32 v33, v34, s36, v149
	v_med3_f32 v32, v32, s36, v149
	v_lshl_add_u64 v[12:13], v[132:133], 0, s[6:7]
	v_cvt_pk_fp8_f32 v35, v33, v32 op_sel:[0,0,1]
	s_waitcnt vmcnt(19)
; #define CV_LOAD(qi, Q, D) do { _Pragma("unroll") for (int s_ = 0; s_ < 2; ++s_) _Pragma("unroll") for (int r_ = 0; r_ < 4; ++r_) Q.v[s_][r_] = *(const f32x4*)(D.src + (size_t)(16 * (2 * (qi) + s_) + r_) * D.N); asm volatile("" ::: "memory"); } while (0)
; #define CV_PROC(qi, Q) do { _Pragma("unroll") for (int s_ = 0; s_ < 2; ++s_) _Pragma("unroll") for (int c_ = 0; c_ < 4; ++c_) \
;         *(LAS unsigned*)(scr + (4 * nl + c_) * 132 + 16 * (2 * (qi) + s_) + 4 * kg) = pg8::pk4_fp8c(Q.v[s_][0][c_] * FP8_WSC, Q.v[s_][1][c_] * FP8_WSC, Q.v[s_][2][c_] * FP8_WSC, Q.v[s_][3][c_] * FP8_WSC); asm volatile("" ::: "memory"); } while (0)
; __device__ __forceinline__ void moe_conv_stream(const Args& a, ARGAS unsigned char* ws, LAS unsigned char* scr, int first, int cnt, int lane) {
;     ...
;     Qt A, B, C, D4;
;     ConvItem cur = moe_conv_desc(a, ws, first, lane);
;     CV_LOAD(0, A, cur); CV_LOAD(1, B, cur); CV_LOAD(2, C, cur);
; #pragma unroll 1
;     for (int i = 0; i < cnt; ++i) {
;         const ConvItem nxt = moe_conv_desc(a, ws, first + 8 * ((i + 1 < cnt) ? i + 1 : i), lane);
;         CV_LOAD(3, D4, cur); CV_PROC(0, A);
;         CV_LOAD(0, A, nxt);  CV_PROC(1, B);
;         CV_LOAD(1, B, nxt);  CV_PROC(2, C);
;         CV_LOAD(2, C, nxt);  CV_PROC(3, D4);
	v_mul_f32_e32 v72, 0x43000000, v72
	s_waitcnt vmcnt(18)
	v_mul_f32_e32 v80, 0x43000000, v80
	global_load_dwordx4 v[0:3], v[0:1], off nt
	s_nop 0
	global_load_dwordx4 v[4:7], v[4:5], off nt
	s_nop 0
	global_load_dwordx4 v[8:11], v[8:9], off nt
	s_nop 0
	global_load_dwordx4 v[12:15], v[12:13], off nt
	ds_write2_b32 v146, v150, v41 offset0:8 offset1:12
	ds_write2_b32 v146, v49, v37 offset0:41 offset1:45
	ds_write2_b32 v146, v48, v36 offset0:74 offset1:78
	ds_write2_b32 v146, v43, v35 offset0:107 offset1:111
	v_med3_f32 v72, v72, s36, v149
	v_med3_f32 v80, v80, s36, v149
	v_mov_b32_e32 v150, v129
	v_cvt_pk_fp8_f32 v150, v72, v80
	s_waitcnt vmcnt(21)
	v_mul_f32_e32 v92, 0x43000000, v92
	s_waitcnt vmcnt(20)
	v_mul_f32_e32 v72, 0x43000000, v88
	v_med3_f32 v80, v92, s36, v149
	v_med3_f32 v72, v72, s36, v149
	v_cvt_pk_fp8_f32 v150, v80, v72 op_sel:[0,0,1]
	v_mul_f32_e32 v72, 0x43000000, v73
	v_mul_f32_e32 v73, 0x43000000, v81
	v_med3_f32 v72, v72, s36, v149
	v_med3_f32 v73, v73, s36, v149
	v_mov_b32_e32 v81, v129
	v_cvt_pk_fp8_f32 v81, v72, v73
	v_mul_f32_e32 v80, 0x43000000, v93
	v_mul_f32_e32 v72, 0x43000000, v89
	v_med3_f32 v73, v80, s36, v149
	v_med3_f32 v72, v72, s36, v149
	v_cvt_pk_fp8_f32 v81, v73, v72 op_sel:[0,0,1]
	v_mul_f32_e32 v72, 0x43000000, v74
	v_mul_f32_e32 v73, 0x43000000, v82
	v_med3_f32 v72, v72, s36, v149
	v_med3_f32 v73, v73, s36, v149
	v_mov_b32_e32 v80, v129
	v_cvt_pk_fp8_f32 v80, v72, v73
	v_mul_f32_e32 v74, 0x43000000, v94
	v_mul_f32_e32 v72, 0x43000000, v90
	v_med3_f32 v73, v74, s36, v149
	v_med3_f32 v72, v72, s36, v149
	v_cvt_pk_fp8_f32 v80, v73, v72 op_sel:[0,0,1]
	v_mul_f32_e32 v72, 0x43000000, v75
	v_mul_f32_e32 v73, 0x43000000, v83
	v_med3_f32 v72, v72, s36, v149
	v_med3_f32 v73, v73, s36, v149
	v_mov_b32_e32 v75, v129
	v_cvt_pk_fp8_f32 v75, v72, v73
	v_mul_f32_e32 v74, 0x43000000, v95
	v_mul_f32_e32 v72, 0x43000000, v91
	v_med3_f32 v73, v74, s36, v149
	v_med3_f32 v72, v72, s36, v149
	s_waitcnt vmcnt(19)
	v_mul_f32_e32 v64, 0x43000000, v64
	s_waitcnt vmcnt(18)
	v_mul_f32_e32 v68, 0x43000000, v68
	v_cvt_pk_fp8_f32 v75, v73, v72 op_sel:[0,0,1]
	v_med3_f32 v64, v64, s36, v149
	v_med3_f32 v68, v68, s36, v149
	v_mov_b32_e32 v73, v129
	v_cvt_pk_fp8_f32 v73, v64, v68
	s_waitcnt vmcnt(17)
	v_mul_f32_e32 v72, 0x43000000, v84
	s_waitcnt vmcnt(16)
	v_mul_f32_e32 v64, 0x43000000, v76
	v_med3_f32 v68, v72, s36, v149
	v_med3_f32 v64, v64, s36, v149
	v_cvt_pk_fp8_f32 v73, v68, v64 op_sel:[0,0,1]
	v_mul_f32_e32 v64, 0x43000000, v65
	v_mul_f32_e32 v65, 0x43000000, v69
	v_med3_f32 v64, v64, s36, v149
	v_med3_f32 v65, v65, s36, v149
	v_mov_b32_e32 v69, v129
	v_cvt_pk_fp8_f32 v69, v64, v65
	v_mul_f32_e32 v68, 0x43000000, v85
	v_mul_f32_e32 v64, 0x43000000, v77
	v_med3_f32 v65, v68, s36, v149
	v_med3_f32 v64, v64, s36, v149
	v_cvt_pk_fp8_f32 v69, v65, v64 op_sel:[0,0,1]
	v_mul_f32_e32 v64, 0x43000000, v66
	v_mul_f32_e32 v65, 0x43000000, v70
	v_med3_f32 v64, v64, s36, v149
	v_med3_f32 v65, v65, s36, v149
	v_mov_b32_e32 v68, v129
	v_cvt_pk_fp8_f32 v68, v64, v65
	s_lshl_b32 s6, s13, 7
	v_mul_f32_e32 v66, 0x43000000, v86
	v_mul_f32_e32 v64, 0x43000000, v78
	v_lshl_add_u64 v[32:33], v[132:133], 0, s[6:7]
	s_mul_i32 s6, s13, 0x84
	v_med3_f32 v65, v66, s36, v149
	v_med3_f32 v64, v64, s36, v149
	v_lshl_add_u64 v[34:35], v[132:133], 0, s[6:7]
	s_mul_i32 s6, s13, 0x88
	v_cvt_pk_fp8_f32 v68, v65, v64 op_sel:[0,0,1]
	v_mul_f32_e32 v64, 0x43000000, v67
	v_mul_f32_e32 v65, 0x43000000, v71
	global_load_dwordx4 v[40:43], v[32:33], off nt
	global_load_dwordx4 v[48:51], v[34:35], off nt
	v_lshl_add_u64 v[32:33], v[132:133], 0, s[6:7]
	s_mul_i32 s6, s13, 0x8c
	v_med3_f32 v64, v64, s36, v149
	v_med3_f32 v65, v65, s36, v149
	v_mov_b32_e32 v67, v129
	v_lshl_add_u64 v[34:35], v[132:133], 0, s[6:7]
	s_mul_i32 s6, s13, 0xc0
	v_cvt_pk_fp8_f32 v67, v64, v65
	global_load_dwordx4 v[60:63], v[32:33], off nt
	global_load_dwordx4 v[56:59], v[34:35], off nt
	v_lshl_add_u64 v[32:33], v[132:133], 0, s[6:7]
	s_mul_i32 s6, s13, 0xc4
	v_lshl_add_u64 v[36:37], v[132:133], 0, s[6:7]
	s_mul_i32 s6, s13, 0xc8
	v_mul_f32_e32 v66, 0x43000000, v87
	v_mul_f32_e32 v64, 0x43000000, v79
	v_lshl_add_u64 v[44:45], v[132:133], 0, s[6:7]
	s_mul_i32 s6, s13, 0xcc
	v_med3_f32 v65, v66, s36, v149
	v_med3_f32 v64, v64, s36, v149
	v_lshl_add_u64 v[46:47], v[132:133], 0, s[6:7]
	v_cvt_pk_fp8_f32 v67, v65, v64 op_sel:[0,0,1]
	s_waitcnt vmcnt(19)
	v_mul_f32_e32 v116, 0x43000000, v116
	s_waitcnt vmcnt(18)
	v_mul_f32_e32 v120, 0x43000000, v120
	global_load_dwordx4 v[32:35], v[32:33], off nt
	s_nop 0
	global_load_dwordx4 v[36:39], v[36:37], off nt
	s_nop 0
	global_load_dwordx4 v[52:55], v[44:45], off nt
	s_nop 0
	global_load_dwordx4 v[44:47], v[46:47], off nt
	ds_write2_b32 v146, v150, v73 offset0:16 offset1:20
	ds_write2_b32 v146, v81, v69 offset0:49 offset1:53
	ds_write2_b32 v146, v80, v68 offset0:82 offset1:86
	ds_write2_b32 v146, v75, v67 offset0:115 offset1:119
	v_med3_f32 v116, v116, s36, v149
	v_med3_f32 v120, v120, s36, v149
	v_mov_b32_e32 v150, v129
	v_cvt_pk_fp8_f32 v150, v116, v120
	s_waitcnt vmcnt(21)
	v_mul_f32_e32 v124, 0x43000000, v124
	s_waitcnt vmcnt(20)
; #define LAS __attribute__((address_space(3)))
; #define LDS_WAIT() asm volatile("s_waitcnt lgkmcnt(0)" ::: "memory")
; #define CV_LOAD(qi, Q, D) do { _Pragma("unroll") for (int s_ = 0; s_ < 2; ++s_) _Pragma("unroll") for (int r_ = 0; r_ < 4; ++r_) Q.v[s_][r_] = *(const f32x4*)(D.src + (size_t)(16 * (2 * (qi) + s_) + r_) * D.N); asm volatile("" ::: "memory"); } while (0)
; #define CV_PROC(qi, Q) do { _Pragma("unroll") for (int s_ = 0; s_ < 2; ++s_) _Pragma("unroll") for (int c_ = 0; c_ < 4; ++c_) \
;         *(LAS unsigned*)(scr + (4 * nl + c_) * 132 + 16 * (2 * (qi) + s_) + 4 * kg) = pg8::pk4_fp8c(Q.v[s_][0][c_] * FP8_WSC, Q.v[s_][1][c_] * FP8_WSC, Q.v[s_][2][c_] * FP8_WSC, Q.v[s_][3][c_] * FP8_WSC); asm volatile("" ::: "memory"); } while (0)
; __device__ __forceinline__ void moe_conv_stream(const Args& a, ARGAS unsigned char* ws, LAS unsigned char* scr, int first, int cnt, int lane) {
;     ...
;     Qt A, B, C, D4;
;     ConvItem cur = moe_conv_desc(a, ws, first, lane);
;     CV_LOAD(0, A, cur); CV_LOAD(1, B, cur); CV_LOAD(2, C, cur);
; #pragma unroll 1
;     for (int i = 0; i < cnt; ++i) {
;         const ConvItem nxt = moe_conv_desc(a, ws, first + 8 * ((i + 1 < cnt) ? i + 1 : i), lane);
;         CV_LOAD(3, D4, cur); CV_PROC(0, A);
;         CV_LOAD(0, A, nxt);  CV_PROC(1, B);
;         CV_LOAD(1, B, nxt);  CV_PROC(2, C);
;         CV_LOAD(2, C, nxt);  CV_PROC(3, D4);
;         LDS_WAIT(); asm volatile("" ::: "memory");
;         const int n0 = cur.gu > 0 ? cur.gu - 1 : -cur.gu - 1;
; #pragma unroll
;         for (int j = 0; j < 8; ++j) { const int row = (lane >> 3) + 8 * j; const LAS unsigned* s = (const LAS unsigned*)(scr + row * 132 + 16 * c8);
;             u32x4 o; o.x = s[0]; o.y = s[1]; o.z = s[2]; o.w = s[3];
;             const int n = n0 + row, wr_ = cur.gu > 0 ? RmGu()(n) : n;
;             *(u32x4*)(cur.dst + (size_t)wr_ * cur.ldk + 16 * c8) = o; }
	v_mul_f32_e32 v112, 0x43000000, v112
	v_med3_f32 v116, v124, s36, v149
	v_med3_f32 v112, v112, s36, v149
	v_cvt_pk_fp8_f32 v150, v116, v112 op_sel:[0,0,1]
	v_mul_f32_e32 v112, 0x43000000, v117
	v_mul_f32_e32 v116, 0x43000000, v121
	v_med3_f32 v112, v112, s36, v149
	v_med3_f32 v116, v116, s36, v149
	v_mov_b32_e32 v120, v129
	v_cvt_pk_fp8_f32 v120, v112, v116
	v_mul_f32_e32 v117, 0x43000000, v125
	v_mul_f32_e32 v112, 0x43000000, v113
	v_med3_f32 v113, v117, s36, v149
	v_med3_f32 v112, v112, s36, v149
	v_cvt_pk_fp8_f32 v120, v113, v112 op_sel:[0,0,1]
	v_mul_f32_e32 v112, 0x43000000, v118
	v_mul_f32_e32 v113, 0x43000000, v122
	v_med3_f32 v112, v112, s36, v149
	v_med3_f32 v113, v113, s36, v149
	v_mov_b32_e32 v117, v129
	v_cvt_pk_fp8_f32 v117, v112, v113
	v_mul_f32_e32 v116, 0x43000000, v126
	v_mul_f32_e32 v112, 0x43000000, v114
	v_med3_f32 v113, v116, s36, v149
	v_med3_f32 v112, v112, s36, v149
	v_cvt_pk_fp8_f32 v117, v113, v112 op_sel:[0,0,1]
	v_mul_f32_e32 v112, 0x43000000, v119
	v_mul_f32_e32 v113, 0x43000000, v123
	v_med3_f32 v112, v112, s36, v149
	v_med3_f32 v113, v113, s36, v149
	v_mov_b32_e32 v116, v129
	v_cvt_pk_fp8_f32 v116, v112, v113
	v_mul_f32_e32 v114, 0x43000000, v127
	v_mul_f32_e32 v112, 0x43000000, v115
	v_med3_f32 v113, v114, s36, v149
	v_med3_f32 v112, v112, s36, v149
	s_waitcnt vmcnt(19)
	v_mul_f32_e32 v100, 0x43000000, v100
	s_waitcnt vmcnt(18)
	v_mul_f32_e32 v104, 0x43000000, v104
	v_cvt_pk_fp8_f32 v116, v113, v112 op_sel:[0,0,1]
	v_med3_f32 v100, v100, s36, v149
	v_med3_f32 v104, v104, s36, v149
	v_mov_b32_e32 v112, v129
	v_cvt_pk_fp8_f32 v112, v100, v104
	s_waitcnt vmcnt(17)
	v_mul_f32_e32 v108, 0x43000000, v108
	s_waitcnt vmcnt(16)
	v_mul_f32_e32 v96, 0x43000000, v96
	v_med3_f32 v100, v108, s36, v149
	v_med3_f32 v96, v96, s36, v149
	v_cvt_pk_fp8_f32 v112, v100, v96 op_sel:[0,0,1]
	v_mul_f32_e32 v96, 0x43000000, v101
	v_mul_f32_e32 v100, 0x43000000, v105
	v_med3_f32 v96, v96, s36, v149
	v_med3_f32 v100, v100, s36, v149
	v_mov_b32_e32 v104, v129
	v_cvt_pk_fp8_f32 v104, v96, v100
	v_mul_f32_e32 v101, 0x43000000, v109
	v_mul_f32_e32 v96, 0x43000000, v97
	v_med3_f32 v97, v101, s36, v149
	v_med3_f32 v96, v96, s36, v149
	s_lshl_b32 s6, s13, 8
	v_cvt_pk_fp8_f32 v104, v97, v96 op_sel:[0,0,1]
	v_mul_f32_e32 v96, 0x43000000, v102
	v_mul_f32_e32 v97, 0x43000000, v106
	v_lshl_add_u64 v[64:65], v[132:133], 0, s[6:7]
	s_mul_i32 s6, s13, 0x104
	v_med3_f32 v96, v96, s36, v149
	v_med3_f32 v97, v97, s36, v149
	v_mov_b32_e32 v101, v129
	v_lshl_add_u64 v[66:67], v[132:133], 0, s[6:7]
	s_mul_i32 s6, s13, 0x108
	v_cvt_pk_fp8_f32 v101, v96, v97
	global_load_dwordx4 v[72:75], v[64:65], off nt
	global_load_dwordx4 v[80:83], v[66:67], off nt
	v_lshl_add_u64 v[64:65], v[132:133], 0, s[6:7]
	s_mul_i32 s6, s13, 0x10c
	v_lshl_add_u64 v[66:67], v[132:133], 0, s[6:7]
	s_mul_i32 s6, s13, 0x140
	v_mul_f32_e32 v100, 0x43000000, v110
	v_mul_f32_e32 v96, 0x43000000, v98
	global_load_dwordx4 v[92:95], v[64:65], off nt
	global_load_dwordx4 v[88:91], v[66:67], off nt
	v_lshl_add_u64 v[64:65], v[132:133], 0, s[6:7]
	s_mul_i32 s6, s13, 0x144
	v_med3_f32 v97, v100, s36, v149
	v_med3_f32 v96, v96, s36, v149
	v_lshl_add_u64 v[68:69], v[132:133], 0, s[6:7]
	s_mul_i32 s6, s13, 0x148
	v_cvt_pk_fp8_f32 v101, v97, v96 op_sel:[0,0,1]
	v_mul_f32_e32 v96, 0x43000000, v103
	v_mul_f32_e32 v97, 0x43000000, v107
	v_lshl_add_u64 v[76:77], v[132:133], 0, s[6:7]
	s_mul_i32 s6, s13, 0x14c
	v_med3_f32 v96, v96, s36, v149
	v_med3_f32 v97, v97, s36, v149
	v_mov_b32_e32 v100, v129
	v_lshl_add_u64 v[78:79], v[132:133], 0, s[6:7]
	v_cvt_pk_fp8_f32 v100, v96, v97
	s_add_i32 s6, s39, -1
	s_not_b32 s12, s39
	s_cmp_gt_i32 s39, 0
	global_load_dwordx4 v[64:67], v[64:65], off nt
	s_nop 0
	global_load_dwordx4 v[68:71], v[68:69], off nt
	s_nop 0
	global_load_dwordx4 v[84:87], v[76:77], off nt
	s_nop 0
	global_load_dwordx4 v[76:79], v[78:79], off nt
	v_mul_f32_e32 v98, 0x43000000, v111
	v_mul_f32_e32 v96, 0x43000000, v99
	s_cselect_b64 vcc, -1, 0
	v_med3_f32 v97, v98, s36, v149
	v_med3_f32 v96, v96, s36, v149
	s_and_b64 s[14:15], vcc, exec
	v_cvt_pk_fp8_f32 v100, v97, v96 op_sel:[0,0,1]
	s_cselect_b32 s6, s6, s12
	ds_write2_b32 v146, v150, v112 offset0:24 offset1:28
	ds_write2_b32 v146, v120, v104 offset0:57 offset1:61
	ds_write2_b32 v146, v117, v101 offset0:90 offset1:94
	ds_write2_b32 v146, v116, v100 offset0:123 offset1:127
	v_add_u32_e32 v100, s6, v194
	v_lshlrev_b32_e32 v101, 1, v100
	v_ashrrev_i32_e32 v102, 3, v100
	s_waitcnt lgkmcnt(0)
; #define LAS __attribute__((address_space(3)))
; #define LDS_WAIT() asm volatile("s_waitcnt lgkmcnt(0)" ::: "memory")
; __device__ __forceinline__ void moe_conv_stream(const Args& a, ARGAS unsigned char* ws, LAS unsigned char* scr, int first, int cnt, int lane) {
;     ...
;         LDS_WAIT(); asm volatile("" ::: "memory");
;         const int n0 = cur.gu > 0 ? cur.gu - 1 : -cur.gu - 1;
; #pragma unroll
;         for (int j = 0; j < 8; ++j) { const int row = (lane >> 3) + 8 * j; const LAS unsigned* s = (const LAS unsigned*)(scr + row * 132 + 16 * c8);
;             u32x4 o; o.x = s[0]; o.y = s[1]; o.z = s[2]; o.w = s[3];
;             const int n = n0 + row, wr_ = cur.gu > 0 ? RmGu()(n) : n;
;             *(u32x4*)(cur.dst + (size_t)wr_ * cur.ldk + 16 * c8) = o; }
;         LDS_WAIT(); asm volatile("" ::: "memory");
;         cur = nxt;
	v_and_b32_e32 v101, 0x700, v101
	v_and_b32_e32 v102, 0xffffff80, v102
	v_add_u32_e32 v101, v101, v102
	ds_read2_b32 v[96:97], v147 offset1:1
	ds_read2_b32 v[98:99], v147 offset0:2 offset1:3
	v_and_or_b32 v101, v100, s37, v101
	v_cndmask_b32_e32 v100, v100, v101, vcc
	v_ashrrev_i32_e32 v101, 31, v100
	v_lshl_add_u64 v[104:105], s[8:9], 0, v[130:131]
	v_lshlrev_b64 v[100:101], 10, v[100:101]
	v_lshl_add_u64 v[106:107], v[104:105], 0, v[100:101]
	v_add_u32_e32 v100, 0x420, v147
	v_add_u32_e32 v102, 0x428, v147
	ds_read2_b32 v[100:101], v100 offset1:1
	ds_read2_b32 v[102:103], v102 offset1:1
	s_waitcnt lgkmcnt(2)
	global_store_dwordx4 v[106:107], v[96:99], off
	s_add_i32 s40, s40, 8
	s_cmpk_eq_i32 s40, 0x88
	v_add_u32_e32 v96, s6, v137
	v_lshlrev_b32_e32 v97, 1, v96
	v_ashrrev_i32_e32 v98, 3, v96
	v_and_b32_e32 v97, 0x700, v97
	v_and_b32_e32 v98, 0xffffff80, v98
	v_add_u32_e32 v97, v97, v98
	v_and_or_b32 v97, v96, s37, v97
	v_cndmask_b32_e32 v96, v96, v97, vcc
	v_ashrrev_i32_e32 v97, 31, v96
	v_lshlrev_b64 v[96:97], 10, v[96:97]
	v_lshl_add_u64 v[96:97], v[104:105], 0, v[96:97]
	s_waitcnt lgkmcnt(0)
	global_store_dwordx4 v[96:97], v[100:103], off
	v_add_u32_e32 v96, 0x840, v147
	v_add_u32_e32 v98, 0x848, v147
	v_add_u32_e32 v100, s6, v138
	v_lshlrev_b32_e32 v101, 1, v100
	v_ashrrev_i32_e32 v102, 3, v100
	v_and_b32_e32 v101, 0x700, v101
	v_and_b32_e32 v102, 0xffffff80, v102
	v_add_u32_e32 v101, v101, v102
	ds_read2_b32 v[96:97], v96 offset1:1
	ds_read2_b32 v[98:99], v98 offset1:1
	v_and_or_b32 v101, v100, s37, v101
	v_cndmask_b32_e32 v100, v100, v101, vcc
	v_ashrrev_i32_e32 v101, 31, v100
	v_lshlrev_b64 v[100:101], 10, v[100:101]
	v_lshl_add_u64 v[106:107], v[104:105], 0, v[100:101]
	v_add_u32_e32 v100, 0xc60, v147
	v_add_u32_e32 v102, 0xc68, v147
	ds_read2_b32 v[100:101], v100 offset1:1
	ds_read2_b32 v[102:103], v102 offset1:1
	s_waitcnt lgkmcnt(2)
	global_store_dwordx4 v[106:107], v[96:99], off
	s_mov_b32 s39, s41
	s_mov_b64 s[8:9], s[10:11]
	v_add_u32_e32 v96, s6, v139
	v_lshlrev_b32_e32 v97, 1, v96
	v_ashrrev_i32_e32 v98, 3, v96
	v_and_b32_e32 v97, 0x700, v97
	v_and_b32_e32 v98, 0xffffff80, v98
	v_add_u32_e32 v97, v97, v98
	v_and_or_b32 v97, v96, s37, v97
	v_cndmask_b32_e32 v96, v96, v97, vcc
	v_ashrrev_i32_e32 v97, 31, v96
	v_lshlrev_b64 v[96:97], 10, v[96:97]
	v_lshl_add_u64 v[96:97], v[104:105], 0, v[96:97]
	s_waitcnt lgkmcnt(0)
	global_store_dwordx4 v[96:97], v[100:103], off
	v_add_u32_e32 v96, 0x1080, v147
	v_add_u32_e32 v98, 0x1088, v147
	v_add_u32_e32 v100, s6, v140
	v_lshlrev_b32_e32 v101, 1, v100
	v_ashrrev_i32_e32 v102, 3, v100
	v_and_b32_e32 v101, 0x700, v101
	v_and_b32_e32 v102, 0xffffff80, v102
	v_add_u32_e32 v101, v101, v102
	ds_read2_b32 v[96:97], v96 offset1:1
	ds_read2_b32 v[98:99], v98 offset1:1
	v_and_or_b32 v101, v100, s37, v101
	v_cndmask_b32_e32 v100, v100, v101, vcc
	v_ashrrev_i32_e32 v101, 31, v100
	v_lshlrev_b64 v[100:101], 10, v[100:101]
	v_lshl_add_u64 v[106:107], v[104:105], 0, v[100:101]
	v_add_u32_e32 v100, 0x14a0, v147
	v_add_u32_e32 v102, 0x14a8, v147
	ds_read2_b32 v[100:101], v100 offset1:1
	ds_read2_b32 v[102:103], v102 offset1:1
	s_waitcnt lgkmcnt(2)
	global_store_dwordx4 v[106:107], v[96:99], off
	s_nop 1
	v_add_u32_e32 v96, s6, v141
	v_lshlrev_b32_e32 v97, 1, v96
	v_ashrrev_i32_e32 v98, 3, v96
	v_and_b32_e32 v97, 0x700, v97
	v_and_b32_e32 v98, 0xffffff80, v98
	v_add_u32_e32 v97, v97, v98
	v_and_or_b32 v97, v96, s37, v97
	v_cndmask_b32_e32 v96, v96, v97, vcc
	v_ashrrev_i32_e32 v97, 31, v96
	v_lshlrev_b64 v[96:97], 10, v[96:97]
	v_lshl_add_u64 v[96:97], v[104:105], 0, v[96:97]
	s_waitcnt lgkmcnt(0)
	global_store_dwordx4 v[96:97], v[100:103], off
	v_add_u32_e32 v96, 0x18c0, v147
	v_add_u32_e32 v98, 0x18c8, v147
	v_add_u32_e32 v100, s6, v142
	v_lshlrev_b32_e32 v101, 1, v100
	v_ashrrev_i32_e32 v102, 3, v100
	v_and_b32_e32 v101, 0x700, v101
	v_and_b32_e32 v102, 0xffffff80, v102
	v_add_u32_e32 v101, v101, v102
	ds_read2_b32 v[96:97], v96 offset1:1
	ds_read2_b32 v[98:99], v98 offset1:1
	v_and_or_b32 v101, v100, s37, v101
	v_cndmask_b32_e32 v100, v100, v101, vcc
	v_ashrrev_i32_e32 v101, 31, v100
	v_lshlrev_b64 v[100:101], 10, v[100:101]
	v_lshl_add_u64 v[106:107], v[104:105], 0, v[100:101]
	v_add_u32_e32 v100, 0x1ce0, v147
	v_add_u32_e32 v102, 0x1ce8, v147
	ds_read2_b32 v[100:101], v100 offset1:1
	ds_read2_b32 v[102:103], v102 offset1:1
	s_waitcnt lgkmcnt(2)
	global_store_dwordx4 v[106:107], v[96:99], off
	s_nop 1
	v_add_u32_e32 v96, s6, v143
	v_lshlrev_b32_e32 v97, 1, v96
	v_ashrrev_i32_e32 v98, 3, v96
	v_and_b32_e32 v97, 0x700, v97
	v_and_b32_e32 v98, 0xffffff80, v98
	v_add_u32_e32 v97, v97, v98
	v_and_or_b32 v97, v96, s37, v97
	v_cndmask_b32_e32 v96, v96, v97, vcc
	v_ashrrev_i32_e32 v97, 31, v96
	v_lshlrev_b64 v[96:97], 10, v[96:97]
	v_lshl_add_u64 v[96:97], v[104:105], 0, v[96:97]
	s_waitcnt lgkmcnt(0)
	global_store_dwordx4 v[96:97], v[100:103], off
	s_waitcnt lgkmcnt(0)
	s_mov_b32 s6, s13
	v_mov_b64_e32 v[96:97], v[132:133]
	s_cbranch_scc1 .LBB0_574

; #define LAS __attribute__((address_space(3)))
; #define CV_LOAD(qi, Q, D) do { _Pragma("unroll") for (int s_ = 0; s_ < 2; ++s_) _Pragma("unroll") for (int r_ = 0; r_ < 4; ++r_) Q.v[s_][r_] = *(const f32x4*)(D.src + (size_t)(16 * (2 * (qi) + s_) + r_) * D.N); asm volatile("" ::: "memory"); } while (0)
; #define CV_PROC(qi, Q) do { _Pragma("unroll") for (int s_ = 0; s_ < 2; ++s_) _Pragma("unroll") for (int c_ = 0; c_ < 4; ++c_) \
;         *(LAS unsigned*)(scr + (4 * nl + c_) * 132 + 16 * (2 * (qi) + s_) + 4 * kg) = pg8::pk4_fp8c(Q.v[s_][0][c_] * FP8_WSC, Q.v[s_][1][c_] * FP8_WSC, Q.v[s_][2][c_] * FP8_WSC, Q.v[s_][3][c_] * FP8_WSC); asm volatile("" ::: "memory"); } while (0)
; __device__ __forceinline__ void moe_conv_stream(const Args& a, ARGAS unsigned char* ws, LAS unsigned char* scr, int first, int cnt, int lane) {
;     const int nl = lane & 15, kg = lane >> 4, c8 = lane & 7;
;     struct Qt { f32x4 v[2][4]; };
;     ...
;     Qt A, B, C, D4;
;     ConvItem cur = moe_conv_desc(a, ws, first, lane);
;     CV_LOAD(0, A, cur); CV_LOAD(1, B, cur); CV_LOAD(2, C, cur);
; #pragma unroll 1
;     for (int i = 0; i < cnt; ++i) {
;         const ConvItem nxt = moe_conv_desc(a, ws, first + 8 * ((i + 1 < cnt) ? i + 1 : i), lane);
;         CV_LOAD(3, D4, cur); CV_PROC(0, A);
;         CV_LOAD(0, A, nxt);  CV_PROC(1, B);
;         CV_LOAD(1, B, nxt);  CV_PROC(2, C);
;         CV_LOAD(2, C, nxt);  CV_PROC(3, D4);
.LBB0_665:
	v_lshl_add_u64 v[96:97], v[0:1], 0, v[128:129]
	s_lshl_b32 s6, s11, 2
	v_lshl_add_u64 v[0:1], v[96:97], 0, s[6:7]
	s_lshl_b32 s6, s11, 3
	v_lshl_add_u64 v[2:3], v[96:97], 0, s[6:7]
	s_mul_i32 s6, s11, 12
	s_waitcnt vmcnt(26)
	v_lshl_add_u64 v[4:5], v[96:97], 0, s[6:7]
	s_lshl_b32 s6, s11, 6
	v_lshl_add_u64 v[6:7], v[96:97], 0, s[6:7]
	s_mul_i32 s6, s11, 0x44
	s_waitcnt vmcnt(24)
	v_lshl_add_u64 v[12:13], v[96:97], 0, s[6:7]
	s_mul_i32 s6, s11, 0x48
	v_lshl_add_u64 v[14:15], v[96:97], 0, s[6:7]
	s_mul_i32 s6, s11, 0x4c
	s_waitcnt vmcnt(19)
	v_lshl_add_u64 v[32:33], v[96:97], 0, s[6:7]
	s_lshl_b32 s6, s11, 7
	global_load_dwordx4 v[16:19], v[0:1], off nt
	global_load_dwordx4 v[20:23], v[2:3], off nt
	global_load_dwordx4 v[24:27], v[4:5], off nt
	s_nop 0
	global_load_dwordx4 v[0:3], v[6:7], off nt
	s_nop 0
	global_load_dwordx4 v[4:7], v[12:13], off nt
	global_load_dwordx4 v[8:11], v[14:15], off nt
	global_load_dwordx4 v[28:31], v[96:97], off nt
	s_nop 0
	global_load_dwordx4 v[12:15], v[32:33], off nt
	v_lshl_add_u64 v[32:33], v[96:97], 0, s[6:7]
	s_mul_i32 s6, s11, 0x84
	v_lshl_add_u64 v[34:35], v[96:97], 0, s[6:7]
	s_mul_i32 s6, s11, 0x88
	global_load_dwordx4 v[40:43], v[32:33], off nt
	global_load_dwordx4 v[48:51], v[34:35], off nt
	v_lshl_add_u64 v[32:33], v[96:97], 0, s[6:7]
	s_mul_i32 s6, s11, 0x8c
	v_lshl_add_u64 v[34:35], v[96:97], 0, s[6:7]
	s_mul_i32 s6, s11, 0xc0
	s_waitcnt vmcnt(26)
	v_lshl_add_u64 v[44:45], v[96:97], 0, s[6:7]
	s_mul_i32 s6, s11, 0xc4
	v_lshl_add_u64 v[46:47], v[96:97], 0, s[6:7]
	s_mul_i32 s6, s11, 0xc8
	s_waitcnt vmcnt(21)
	v_lshl_add_u64 v[64:65], v[96:97], 0, s[6:7]
	s_mul_i32 s6, s11, 0xcc
	v_lshl_add_u64 v[66:67], v[96:97], 0, s[6:7]
	s_lshl_b32 s6, s11, 8
	global_load_dwordx4 v[60:63], v[32:33], off nt
	global_load_dwordx4 v[56:59], v[34:35], off nt
	s_nop 0
	global_load_dwordx4 v[32:35], v[44:45], off nt
	global_load_dwordx4 v[36:39], v[46:47], off nt
	global_load_dwordx4 v[52:55], v[64:65], off nt
	s_nop 0
	global_load_dwordx4 v[44:47], v[66:67], off nt
	v_lshl_add_u64 v[64:65], v[96:97], 0, s[6:7]
	s_mul_i32 s6, s11, 0x104
	v_lshl_add_u64 v[66:67], v[96:97], 0, s[6:7]
	s_mul_i32 s6, s11, 0x108
	global_load_dwordx4 v[72:75], v[64:65], off nt
	global_load_dwordx4 v[80:83], v[66:67], off nt
	v_lshl_add_u64 v[64:65], v[96:97], 0, s[6:7]
	s_mul_i32 s6, s11, 0x10c
	v_lshl_add_u64 v[66:67], v[96:97], 0, s[6:7]
	s_mul_i32 s6, s11, 0x140
	s_waitcnt vmcnt(26)
	v_lshl_add_u64 v[76:77], v[96:97], 0, s[6:7]
	s_mul_i32 s6, s11, 0x144
	v_lshl_add_u64 v[78:79], v[96:97], 0, s[6:7]
	s_mul_i32 s6, s11, 0x148
	v_lshl_add_u64 v[98:99], v[96:97], 0, s[6:7]
	s_mul_i32 s6, s11, 0x14c
	global_load_dwordx4 v[92:95], v[64:65], off nt
	global_load_dwordx4 v[88:91], v[66:67], off nt
	s_nop 0
	global_load_dwordx4 v[64:67], v[76:77], off nt
	global_load_dwordx4 v[68:71], v[78:79], off nt
	v_lshl_add_u64 v[100:101], v[96:97], 0, s[6:7]
	global_load_dwordx4 v[84:87], v[98:99], off nt
	global_load_dwordx4 v[76:79], v[100:101], off nt
	s_mov_b32 s38, 8
	s_mov_b32 s6, s11
	s_branch .LBB0_667
.LBB0_666:
	s_waitcnt vmcnt(17)
	v_mul_f32_e32 v28, 0x43000000, v28
	v_mul_f32_e32 v16, 0x43000000, v16
	v_med3_f32 v28, v28, s26, v147
	v_med3_f32 v16, v16, s26, v147
	v_mov_b32_e32 v148, v129
	v_cvt_pk_fp8_f32 v148, v28, v16
	v_mul_f32_e32 v20, 0x43000000, v20
	v_mul_f32_e32 v16, 0x43000000, v24
	v_med3_f32 v20, v20, s26, v147
	v_med3_f32 v16, v16, s26, v147
	v_cvt_pk_fp8_f32 v148, v20, v16 op_sel:[0,0,1]
	v_mul_f32_e32 v16, 0x43000000, v29
	v_mul_f32_e32 v17, 0x43000000, v17
	v_mul_f32_e32 v20, 0x43000000, v21
	v_med3_f32 v16, v16, s26, v147
	v_med3_f32 v17, v17, s26, v147
	v_mov_b32_e32 v21, v129
	v_cvt_pk_fp8_f32 v21, v16, v17
	v_mul_f32_e32 v16, 0x43000000, v25
	v_med3_f32 v17, v20, s26, v147
	v_med3_f32 v16, v16, s26, v147
	v_cvt_pk_fp8_f32 v21, v17, v16 op_sel:[0,0,1]
	v_mul_f32_e32 v16, 0x43000000, v30
	v_mul_f32_e32 v17, 0x43000000, v18
	v_med3_f32 v16, v16, s26, v147
	v_med3_f32 v17, v17, s26, v147
	v_mov_b32_e32 v20, v129
	v_cvt_pk_fp8_f32 v20, v16, v17
	v_mul_f32_e32 v18, 0x43000000, v22
	v_mul_f32_e32 v16, 0x43000000, v26
	v_med3_f32 v17, v18, s26, v147
	v_med3_f32 v16, v16, s26, v147
	v_cvt_pk_fp8_f32 v20, v17, v16 op_sel:[0,0,1]
	v_mul_f32_e32 v16, 0x43000000, v31
	v_mul_f32_e32 v17, 0x43000000, v19
	v_med3_f32 v16, v16, s26, v147
	v_med3_f32 v17, v17, s26, v147
	v_mov_b32_e32 v19, v129
	v_cvt_pk_fp8_f32 v19, v16, v17
	v_mul_f32_e32 v18, 0x43000000, v23
	v_mul_f32_e32 v16, 0x43000000, v27
	v_med3_f32 v17, v18, s26, v147
	v_med3_f32 v16, v16, s26, v147
	v_mul_f32_e32 v0, 0x43000000, v0
	v_mul_f32_e32 v4, 0x43000000, v4
	v_cvt_pk_fp8_f32 v19, v17, v16 op_sel:[0,0,1]
	v_med3_f32 v0, v0, s26, v147
	v_med3_f32 v4, v4, s26, v147
	v_mov_b32_e32 v16, v129
	v_cvt_pk_fp8_f32 v16, v0, v4
	v_mul_f32_e32 v8, 0x43000000, v8
	s_waitcnt vmcnt(16)
; #define CV_LOAD(qi, Q, D) do { _Pragma("unroll") for (int s_ = 0; s_ < 2; ++s_) _Pragma("unroll") for (int r_ = 0; r_ < 4; ++r_) Q.v[s_][r_] = *(const f32x4*)(D.src + (size_t)(16 * (2 * (qi) + s_) + r_) * D.N); asm volatile("" ::: "memory"); } while (0)
; #define CV_PROC(qi, Q) do { _Pragma("unroll") for (int s_ = 0; s_ < 2; ++s_) _Pragma("unroll") for (int c_ = 0; c_ < 4; ++c_) \
;         *(LAS unsigned*)(scr + (4 * nl + c_) * 132 + 16 * (2 * (qi) + s_) + 4 * kg) = pg8::pk4_fp8c(Q.v[s_][0][c_] * FP8_WSC, Q.v[s_][1][c_] * FP8_WSC, Q.v[s_][2][c_] * FP8_WSC, Q.v[s_][3][c_] * FP8_WSC); asm volatile("" ::: "memory"); } while (0)
; __device__ __forceinline__ void moe_conv_stream(const Args& a, ARGAS unsigned char* ws, LAS unsigned char* scr, int first, int cnt, int lane) {
;     ...
;     Qt A, B, C, D4;
;     ConvItem cur = moe_conv_desc(a, ws, first, lane);
;     CV_LOAD(0, A, cur); CV_LOAD(1, B, cur); CV_LOAD(2, C, cur);
; #pragma unroll 1
;     for (int i = 0; i < cnt; ++i) {
;         const ConvItem nxt = moe_conv_desc(a, ws, first + 8 * ((i + 1 < cnt) ? i + 1 : i), lane);
;         CV_LOAD(3, D4, cur); CV_PROC(0, A);
;         CV_LOAD(0, A, nxt);  CV_PROC(1, B);
;         CV_LOAD(1, B, nxt);  CV_PROC(2, C);
;         CV_LOAD(2, C, nxt);  CV_PROC(3, D4);
	v_mul_f32_e32 v0, 0x43000000, v12
	v_med3_f32 v4, v8, s26, v147
	v_med3_f32 v0, v0, s26, v147
	v_cvt_pk_fp8_f32 v16, v4, v0 op_sel:[0,0,1]
	v_mul_f32_e32 v0, 0x43000000, v1
	v_mul_f32_e32 v1, 0x43000000, v5
	v_med3_f32 v0, v0, s26, v147
	v_med3_f32 v1, v1, s26, v147
	v_mov_b32_e32 v5, v129
	v_cvt_pk_fp8_f32 v5, v0, v1
	v_mul_f32_e32 v4, 0x43000000, v9
	v_mul_f32_e32 v0, 0x43000000, v13
	v_med3_f32 v1, v4, s26, v147
	v_med3_f32 v0, v0, s26, v147
	v_cvt_pk_fp8_f32 v5, v1, v0 op_sel:[0,0,1]
	v_mul_f32_e32 v0, 0x43000000, v2
	v_mul_f32_e32 v1, 0x43000000, v6
	v_med3_f32 v0, v0, s26, v147
	v_med3_f32 v1, v1, s26, v147
	v_mov_b32_e32 v4, v129
	v_cvt_pk_fp8_f32 v4, v0, v1
	v_mad_u64_u32 v[96:97], s[14:15], s6, v146, v[96:97]
	v_mul_f32_e32 v2, 0x43000000, v10
	v_mul_f32_e32 v0, 0x43000000, v14
	s_lshl_b64 s[14:15], s[6:7], 2
	v_med3_f32 v1, v2, s26, v147
	v_med3_f32 v0, v0, s26, v147
	v_lshl_add_u64 v[132:133], v[98:99], 0, v[128:129]
	v_lshl_add_u64 v[98:99], v[96:97], 0, s[14:15]
	v_cvt_pk_fp8_f32 v4, v1, v0 op_sel:[0,0,1]
	v_mul_f32_e32 v0, 0x43000000, v3
	v_mul_f32_e32 v1, 0x43000000, v7
	global_load_dwordx4 v[116:119], v[96:97], off nt
	global_load_dwordx4 v[120:123], v[98:99], off nt
	v_lshl_add_u64 v[96:97], v[98:99], 0, s[14:15]
	v_med3_f32 v0, v0, s26, v147
	v_med3_f32 v1, v1, s26, v147
	v_mov_b32_e32 v3, v129
	v_lshl_add_u64 v[98:99], v[96:97], 0, s[14:15]
	v_cvt_pk_fp8_f32 v3, v0, v1
	global_load_dwordx4 v[124:127], v[96:97], off nt
	global_load_dwordx4 v[112:115], v[98:99], off nt
	v_mad_u64_u32 v[96:97], s[40:41], s6, 52, v[98:99]
	v_lshl_add_u64 v[98:99], v[96:97], 0, s[14:15]
	v_mul_f32_e32 v2, 0x43000000, v11
	v_mul_f32_e32 v0, 0x43000000, v15
	global_load_dwordx4 v[100:103], v[96:97], off nt
	global_load_dwordx4 v[104:107], v[98:99], off nt
	v_lshl_add_u64 v[96:97], v[98:99], 0, s[14:15]
	v_med3_f32 v1, v2, s26, v147
	v_med3_f32 v0, v0, s26, v147
	v_lshl_add_u64 v[98:99], v[96:97], 0, s[14:15]
	v_cvt_pk_fp8_f32 v3, v1, v0 op_sel:[0,0,1]
	s_waitcnt vmcnt(21)
	v_mul_f32_e32 v40, 0x43000000, v40
	s_waitcnt vmcnt(20)
	v_mul_f32_e32 v48, 0x43000000, v48
	global_load_dwordx4 v[108:111], v[96:97], off nt
	s_nop 0
	global_load_dwordx4 v[96:99], v[98:99], off nt
	ds_write2_b32 v143, v148, v16 offset1:4
	ds_write2_b32 v143, v21, v5 offset0:33 offset1:37
	ds_write2_b32 v143, v20, v4 offset0:66 offset1:70
	ds_write2_b32 v143, v19, v3 offset0:99 offset1:103
	v_med3_f32 v40, v40, s26, v147
	v_med3_f32 v48, v48, s26, v147
	v_mov_b32_e32 v148, v129
	v_cvt_pk_fp8_f32 v148, v40, v48
	s_waitcnt vmcnt(21)
	v_mul_f32_e32 v60, 0x43000000, v60
	s_waitcnt vmcnt(20)
	v_mul_f32_e32 v40, 0x43000000, v56
	v_med3_f32 v48, v60, s26, v147
	v_med3_f32 v40, v40, s26, v147
	v_cvt_pk_fp8_f32 v148, v48, v40 op_sel:[0,0,1]
	v_mul_f32_e32 v40, 0x43000000, v41
	v_mul_f32_e32 v41, 0x43000000, v49
	v_med3_f32 v40, v40, s26, v147
	v_med3_f32 v41, v41, s26, v147
	v_mov_b32_e32 v49, v129
	v_cvt_pk_fp8_f32 v49, v40, v41
	v_mul_f32_e32 v48, 0x43000000, v61
	v_mul_f32_e32 v40, 0x43000000, v57
	v_med3_f32 v41, v48, s26, v147
	v_med3_f32 v40, v40, s26, v147
	v_cvt_pk_fp8_f32 v49, v41, v40 op_sel:[0,0,1]
	v_mul_f32_e32 v40, 0x43000000, v42
	v_mul_f32_e32 v41, 0x43000000, v50
	v_med3_f32 v40, v40, s26, v147
	v_med3_f32 v41, v41, s26, v147
	v_mov_b32_e32 v48, v129
	v_cvt_pk_fp8_f32 v48, v40, v41
	v_mul_f32_e32 v42, 0x43000000, v62
	v_mul_f32_e32 v40, 0x43000000, v58
	v_med3_f32 v41, v42, s26, v147
	v_med3_f32 v40, v40, s26, v147
	v_cvt_pk_fp8_f32 v48, v41, v40 op_sel:[0,0,1]
	v_mul_f32_e32 v40, 0x43000000, v43
	v_mul_f32_e32 v41, 0x43000000, v51
	v_med3_f32 v40, v40, s26, v147
	v_med3_f32 v41, v41, s26, v147
	v_mov_b32_e32 v43, v129
	v_cvt_pk_fp8_f32 v43, v40, v41
	v_mul_f32_e32 v42, 0x43000000, v63
	v_mul_f32_e32 v40, 0x43000000, v59
	v_med3_f32 v41, v42, s26, v147
	v_med3_f32 v40, v40, s26, v147
	s_waitcnt vmcnt(19)
	v_mul_f32_e32 v32, 0x43000000, v32
	s_waitcnt vmcnt(18)
	v_mul_f32_e32 v36, 0x43000000, v36
	v_cvt_pk_fp8_f32 v43, v41, v40 op_sel:[0,0,1]
	v_med3_f32 v32, v32, s26, v147
	v_med3_f32 v36, v36, s26, v147
	v_mov_b32_e32 v41, v129
	v_cvt_pk_fp8_f32 v41, v32, v36
	s_waitcnt vmcnt(17)
	v_mul_f32_e32 v40, 0x43000000, v52
	s_waitcnt vmcnt(16)
	v_mul_f32_e32 v32, 0x43000000, v44
	v_med3_f32 v36, v40, s26, v147
	v_med3_f32 v32, v32, s26, v147
	v_cvt_pk_fp8_f32 v41, v36, v32 op_sel:[0,0,1]
	v_mul_f32_e32 v32, 0x43000000, v33
	v_mul_f32_e32 v33, 0x43000000, v37
	v_med3_f32 v32, v32, s26, v147
	v_med3_f32 v33, v33, s26, v147
	v_mov_b32_e32 v37, v129
	v_cvt_pk_fp8_f32 v37, v32, v33
	v_mul_f32_e32 v36, 0x43000000, v53
	v_mul_f32_e32 v32, 0x43000000, v45
	v_med3_f32 v33, v36, s26, v147
	v_med3_f32 v32, v32, s26, v147
	v_cvt_pk_fp8_f32 v37, v33, v32 op_sel:[0,0,1]
	v_mul_f32_e32 v32, 0x43000000, v34
	v_mul_f32_e32 v33, 0x43000000, v38
	v_med3_f32 v32, v32, s26, v147
	v_med3_f32 v33, v33, s26, v147
	v_mov_b32_e32 v36, v129
	v_cvt_pk_fp8_f32 v36, v32, v33
	v_mul_f32_e32 v34, 0x43000000, v54
	v_mul_f32_e32 v32, 0x43000000, v46
	s_lshl_b32 s6, s13, 2
	v_med3_f32 v33, v34, s26, v147
	v_med3_f32 v32, v32, s26, v147
	v_lshl_add_u64 v[0:1], v[132:133], 0, s[6:7]
	s_lshl_b32 s6, s13, 3
	v_cvt_pk_fp8_f32 v36, v33, v32 op_sel:[0,0,1]
	v_mul_f32_e32 v32, 0x43000000, v35
	v_mul_f32_e32 v33, 0x43000000, v39
	global_load_dwordx4 v[28:31], v[132:133], off nt
	global_load_dwordx4 v[16:19], v[0:1], off nt
	v_lshl_add_u64 v[0:1], v[132:133], 0, s[6:7]
	s_mul_i32 s6, s13, 12
	v_med3_f32 v32, v32, s26, v147
	v_med3_f32 v33, v33, s26, v147
	v_mov_b32_e32 v35, v129
	v_lshl_add_u64 v[2:3], v[132:133], 0, s[6:7]
	s_lshl_b32 s6, s13, 6
	v_cvt_pk_fp8_f32 v35, v32, v33
	global_load_dwordx4 v[20:23], v[0:1], off nt
	global_load_dwordx4 v[24:27], v[2:3], off nt
	v_lshl_add_u64 v[0:1], v[132:133], 0, s[6:7]
	s_mul_i32 s6, s13, 0x44
	v_lshl_add_u64 v[4:5], v[132:133], 0, s[6:7]
	s_mul_i32 s6, s13, 0x48
	v_mul_f32_e32 v34, 0x43000000, v55
	v_mul_f32_e32 v32, 0x43000000, v47
	v_lshl_add_u64 v[8:9], v[132:133], 0, s[6:7]
	s_mul_i32 s6, s13, 0x4c
	v_med3_f32 v33, v34, s26, v147
	v_med3_f32 v32, v32, s26, v147
	v_lshl_add_u64 v[12:13], v[132:133], 0, s[6:7]
	v_cvt_pk_fp8_f32 v35, v33, v32 op_sel:[0,0,1]
	s_waitcnt vmcnt(19)
; #define CV_LOAD(qi, Q, D) do { _Pragma("unroll") for (int s_ = 0; s_ < 2; ++s_) _Pragma("unroll") for (int r_ = 0; r_ < 4; ++r_) Q.v[s_][r_] = *(const f32x4*)(D.src + (size_t)(16 * (2 * (qi) + s_) + r_) * D.N); asm volatile("" ::: "memory"); } while (0)
; #define CV_PROC(qi, Q) do { _Pragma("unroll") for (int s_ = 0; s_ < 2; ++s_) _Pragma("unroll") for (int c_ = 0; c_ < 4; ++c_) \
;         *(LAS unsigned*)(scr + (4 * nl + c_) * 132 + 16 * (2 * (qi) + s_) + 4 * kg) = pg8::pk4_fp8c(Q.v[s_][0][c_] * FP8_WSC, Q.v[s_][1][c_] * FP8_WSC, Q.v[s_][2][c_] * FP8_WSC, Q.v[s_][3][c_] * FP8_WSC); asm volatile("" ::: "memory"); } while (0)
; __device__ __forceinline__ void moe_conv_stream(const Args& a, ARGAS unsigned char* ws, LAS unsigned char* scr, int first, int cnt, int lane) {
;     ...
;     Qt A, B, C, D4;
;     ConvItem cur = moe_conv_desc(a, ws, first, lane);
;     CV_LOAD(0, A, cur); CV_LOAD(1, B, cur); CV_LOAD(2, C, cur);
; #pragma unroll 1
;     for (int i = 0; i < cnt; ++i) {
;         const ConvItem nxt = moe_conv_desc(a, ws, first + 8 * ((i + 1 < cnt) ? i + 1 : i), lane);
;         CV_LOAD(3, D4, cur); CV_PROC(0, A);
;         CV_LOAD(0, A, nxt);  CV_PROC(1, B);
;         CV_LOAD(1, B, nxt);  CV_PROC(2, C);
;         CV_LOAD(2, C, nxt);  CV_PROC(3, D4);
	v_mul_f32_e32 v72, 0x43000000, v72
	s_waitcnt vmcnt(18)
	v_mul_f32_e32 v80, 0x43000000, v80
	global_load_dwordx4 v[0:3], v[0:1], off nt
	s_nop 0
	global_load_dwordx4 v[4:7], v[4:5], off nt
	s_nop 0
	global_load_dwordx4 v[8:11], v[8:9], off nt
	s_nop 0
	global_load_dwordx4 v[12:15], v[12:13], off nt
	ds_write2_b32 v144, v148, v41 offset0:8 offset1:12
	ds_write2_b32 v144, v49, v37 offset0:41 offset1:45
	ds_write2_b32 v144, v48, v36 offset0:74 offset1:78
	ds_write2_b32 v144, v43, v35 offset0:107 offset1:111
	v_med3_f32 v72, v72, s26, v147
	v_med3_f32 v80, v80, s26, v147
	v_mov_b32_e32 v148, v129
	v_cvt_pk_fp8_f32 v148, v72, v80
	s_waitcnt vmcnt(21)
	v_mul_f32_e32 v92, 0x43000000, v92
	s_waitcnt vmcnt(20)
	v_mul_f32_e32 v72, 0x43000000, v88
	v_med3_f32 v80, v92, s26, v147
	v_med3_f32 v72, v72, s26, v147
	v_cvt_pk_fp8_f32 v148, v80, v72 op_sel:[0,0,1]
	v_mul_f32_e32 v72, 0x43000000, v73
	v_mul_f32_e32 v73, 0x43000000, v81
	v_med3_f32 v72, v72, s26, v147
	v_med3_f32 v73, v73, s26, v147
	v_mov_b32_e32 v81, v129
	v_cvt_pk_fp8_f32 v81, v72, v73
	v_mul_f32_e32 v80, 0x43000000, v93
	v_mul_f32_e32 v72, 0x43000000, v89
	v_med3_f32 v73, v80, s26, v147
	v_med3_f32 v72, v72, s26, v147
	v_cvt_pk_fp8_f32 v81, v73, v72 op_sel:[0,0,1]
	v_mul_f32_e32 v72, 0x43000000, v74
	v_mul_f32_e32 v73, 0x43000000, v82
	v_med3_f32 v72, v72, s26, v147
	v_med3_f32 v73, v73, s26, v147
	v_mov_b32_e32 v80, v129
	v_cvt_pk_fp8_f32 v80, v72, v73
	v_mul_f32_e32 v74, 0x43000000, v94
	v_mul_f32_e32 v72, 0x43000000, v90
	v_med3_f32 v73, v74, s26, v147
	v_med3_f32 v72, v72, s26, v147
	v_cvt_pk_fp8_f32 v80, v73, v72 op_sel:[0,0,1]
	v_mul_f32_e32 v72, 0x43000000, v75
	v_mul_f32_e32 v73, 0x43000000, v83
	v_med3_f32 v72, v72, s26, v147
	v_med3_f32 v73, v73, s26, v147
	v_mov_b32_e32 v75, v129
	v_cvt_pk_fp8_f32 v75, v72, v73
	v_mul_f32_e32 v74, 0x43000000, v95
	v_mul_f32_e32 v72, 0x43000000, v91
	v_med3_f32 v73, v74, s26, v147
	v_med3_f32 v72, v72, s26, v147
	s_waitcnt vmcnt(19)
	v_mul_f32_e32 v64, 0x43000000, v64
	s_waitcnt vmcnt(18)
	v_mul_f32_e32 v68, 0x43000000, v68
	v_cvt_pk_fp8_f32 v75, v73, v72 op_sel:[0,0,1]
	v_med3_f32 v64, v64, s26, v147
	v_med3_f32 v68, v68, s26, v147
	v_mov_b32_e32 v73, v129
	v_cvt_pk_fp8_f32 v73, v64, v68
	s_waitcnt vmcnt(17)
	v_mul_f32_e32 v72, 0x43000000, v84
	s_waitcnt vmcnt(16)
	v_mul_f32_e32 v64, 0x43000000, v76
	v_med3_f32 v68, v72, s26, v147
	v_med3_f32 v64, v64, s26, v147
	v_cvt_pk_fp8_f32 v73, v68, v64 op_sel:[0,0,1]
	v_mul_f32_e32 v64, 0x43000000, v65
	v_mul_f32_e32 v65, 0x43000000, v69
	v_med3_f32 v64, v64, s26, v147
	v_med3_f32 v65, v65, s26, v147
	v_mov_b32_e32 v69, v129
	v_cvt_pk_fp8_f32 v69, v64, v65
	v_mul_f32_e32 v68, 0x43000000, v85
	v_mul_f32_e32 v64, 0x43000000, v77
	v_med3_f32 v65, v68, s26, v147
	v_med3_f32 v64, v64, s26, v147
	v_cvt_pk_fp8_f32 v69, v65, v64 op_sel:[0,0,1]
	v_mul_f32_e32 v64, 0x43000000, v66
	v_mul_f32_e32 v65, 0x43000000, v70
	v_med3_f32 v64, v64, s26, v147
	v_med3_f32 v65, v65, s26, v147
	v_mov_b32_e32 v68, v129
	v_cvt_pk_fp8_f32 v68, v64, v65
	s_lshl_b32 s6, s13, 7
	v_mul_f32_e32 v66, 0x43000000, v86
	v_mul_f32_e32 v64, 0x43000000, v78
	v_lshl_add_u64 v[32:33], v[132:133], 0, s[6:7]
	s_mul_i32 s6, s13, 0x84
	v_med3_f32 v65, v66, s26, v147
	v_med3_f32 v64, v64, s26, v147
	v_lshl_add_u64 v[34:35], v[132:133], 0, s[6:7]
	s_mul_i32 s6, s13, 0x88
	v_cvt_pk_fp8_f32 v68, v65, v64 op_sel:[0,0,1]
	v_mul_f32_e32 v64, 0x43000000, v67
	v_mul_f32_e32 v65, 0x43000000, v71
	global_load_dwordx4 v[40:43], v[32:33], off nt
	global_load_dwordx4 v[48:51], v[34:35], off nt
	v_lshl_add_u64 v[32:33], v[132:133], 0, s[6:7]
	s_mul_i32 s6, s13, 0x8c
	v_med3_f32 v64, v64, s26, v147
	v_med3_f32 v65, v65, s26, v147
	v_mov_b32_e32 v67, v129
	v_lshl_add_u64 v[34:35], v[132:133], 0, s[6:7]
	s_mul_i32 s6, s13, 0xc0
	v_cvt_pk_fp8_f32 v67, v64, v65
	global_load_dwordx4 v[60:63], v[32:33], off nt
	global_load_dwordx4 v[56:59], v[34:35], off nt
	v_lshl_add_u64 v[32:33], v[132:133], 0, s[6:7]
	s_mul_i32 s6, s13, 0xc4
	v_lshl_add_u64 v[36:37], v[132:133], 0, s[6:7]
	s_mul_i32 s6, s13, 0xc8
	v_mul_f32_e32 v66, 0x43000000, v87
	v_mul_f32_e32 v64, 0x43000000, v79
	v_lshl_add_u64 v[44:45], v[132:133], 0, s[6:7]
	s_mul_i32 s6, s13, 0xcc
	v_med3_f32 v65, v66, s26, v147
	v_med3_f32 v64, v64, s26, v147
	v_lshl_add_u64 v[46:47], v[132:133], 0, s[6:7]
	v_cvt_pk_fp8_f32 v67, v65, v64 op_sel:[0,0,1]
	s_waitcnt vmcnt(19)
	v_mul_f32_e32 v116, 0x43000000, v116
	s_waitcnt vmcnt(18)
	v_mul_f32_e32 v120, 0x43000000, v120
	global_load_dwordx4 v[32:35], v[32:33], off nt
	s_nop 0
	global_load_dwordx4 v[36:39], v[36:37], off nt
	s_nop 0
	global_load_dwordx4 v[52:55], v[44:45], off nt
	s_nop 0
	global_load_dwordx4 v[44:47], v[46:47], off nt
	ds_write2_b32 v144, v148, v73 offset0:16 offset1:20
	ds_write2_b32 v144, v81, v69 offset0:49 offset1:53
	ds_write2_b32 v144, v80, v68 offset0:82 offset1:86
	ds_write2_b32 v144, v75, v67 offset0:115 offset1:119
	v_med3_f32 v116, v116, s26, v147
	v_med3_f32 v120, v120, s26, v147
	v_mov_b32_e32 v148, v129
	v_cvt_pk_fp8_f32 v148, v116, v120
	s_waitcnt vmcnt(21)
	v_mul_f32_e32 v124, 0x43000000, v124
	s_waitcnt vmcnt(20)
; #define LAS __attribute__((address_space(3)))
; #define LDS_WAIT() asm volatile("s_waitcnt lgkmcnt(0)" ::: "memory")
; #define CV_LOAD(qi, Q, D) do { _Pragma("unroll") for (int s_ = 0; s_ < 2; ++s_) _Pragma("unroll") for (int r_ = 0; r_ < 4; ++r_) Q.v[s_][r_] = *(const f32x4*)(D.src + (size_t)(16 * (2 * (qi) + s_) + r_) * D.N); asm volatile("" ::: "memory"); } while (0)
; #define CV_PROC(qi, Q) do { _Pragma("unroll") for (int s_ = 0; s_ < 2; ++s_) _Pragma("unroll") for (int c_ = 0; c_ < 4; ++c_) \
;         *(LAS unsigned*)(scr + (4 * nl + c_) * 132 + 16 * (2 * (qi) + s_) + 4 * kg) = pg8::pk4_fp8c(Q.v[s_][0][c_] * FP8_WSC, Q.v[s_][1][c_] * FP8_WSC, Q.v[s_][2][c_] * FP8_WSC, Q.v[s_][3][c_] * FP8_WSC); asm volatile("" ::: "memory"); } while (0)
; __device__ __forceinline__ void moe_conv_stream(const Args& a, ARGAS unsigned char* ws, LAS unsigned char* scr, int first, int cnt, int lane) {
;     ...
;     Qt A, B, C, D4;
;     ConvItem cur = moe_conv_desc(a, ws, first, lane);
;     CV_LOAD(0, A, cur); CV_LOAD(1, B, cur); CV_LOAD(2, C, cur);
; #pragma unroll 1
;     for (int i = 0; i < cnt; ++i) {
;         const ConvItem nxt = moe_conv_desc(a, ws, first + 8 * ((i + 1 < cnt) ? i + 1 : i), lane);
;         CV_LOAD(3, D4, cur); CV_PROC(0, A);
;         CV_LOAD(0, A, nxt);  CV_PROC(1, B);
;         CV_LOAD(1, B, nxt);  CV_PROC(2, C);
;         CV_LOAD(2, C, nxt);  CV_PROC(3, D4);
;         LDS_WAIT(); asm volatile("" ::: "memory");
;         const int n0 = cur.gu > 0 ? cur.gu - 1 : -cur.gu - 1;
; #pragma unroll
;         for (int j = 0; j < 8; ++j) { const int row = (lane >> 3) + 8 * j; const LAS unsigned* s = (const LAS unsigned*)(scr + row * 132 + 16 * c8);
;             u32x4 o; o.x = s[0]; o.y = s[1]; o.z = s[2]; o.w = s[3];
;             const int n = n0 + row, wr_ = cur.gu > 0 ? RmGu()(n) : n;
;             *(u32x4*)(cur.dst + (size_t)wr_ * cur.ldk + 16 * c8) = o; }
	v_mul_f32_e32 v112, 0x43000000, v112
	v_med3_f32 v116, v124, s26, v147
	v_med3_f32 v112, v112, s26, v147
	v_cvt_pk_fp8_f32 v148, v116, v112 op_sel:[0,0,1]
	v_mul_f32_e32 v112, 0x43000000, v117
	v_mul_f32_e32 v116, 0x43000000, v121
	v_med3_f32 v112, v112, s26, v147
	v_med3_f32 v116, v116, s26, v147
	v_mov_b32_e32 v120, v129
	v_cvt_pk_fp8_f32 v120, v112, v116
	v_mul_f32_e32 v117, 0x43000000, v125
	v_mul_f32_e32 v112, 0x43000000, v113
	v_med3_f32 v113, v117, s26, v147
	v_med3_f32 v112, v112, s26, v147
	v_cvt_pk_fp8_f32 v120, v113, v112 op_sel:[0,0,1]
	v_mul_f32_e32 v112, 0x43000000, v118
	v_mul_f32_e32 v113, 0x43000000, v122
	v_med3_f32 v112, v112, s26, v147
	v_med3_f32 v113, v113, s26, v147
	v_mov_b32_e32 v117, v129
	v_cvt_pk_fp8_f32 v117, v112, v113
	v_mul_f32_e32 v116, 0x43000000, v126
	v_mul_f32_e32 v112, 0x43000000, v114
	v_med3_f32 v113, v116, s26, v147
	v_med3_f32 v112, v112, s26, v147
	v_cvt_pk_fp8_f32 v117, v113, v112 op_sel:[0,0,1]
	v_mul_f32_e32 v112, 0x43000000, v119
	v_mul_f32_e32 v113, 0x43000000, v123
	v_med3_f32 v112, v112, s26, v147
	v_med3_f32 v113, v113, s26, v147
	v_mov_b32_e32 v116, v129
	v_cvt_pk_fp8_f32 v116, v112, v113
	v_mul_f32_e32 v114, 0x43000000, v127
	v_mul_f32_e32 v112, 0x43000000, v115
	v_med3_f32 v113, v114, s26, v147
	v_med3_f32 v112, v112, s26, v147
	s_waitcnt vmcnt(19)
	v_mul_f32_e32 v100, 0x43000000, v100
	s_waitcnt vmcnt(18)
	v_mul_f32_e32 v104, 0x43000000, v104
	v_cvt_pk_fp8_f32 v116, v113, v112 op_sel:[0,0,1]
	v_med3_f32 v100, v100, s26, v147
	v_med3_f32 v104, v104, s26, v147
	v_mov_b32_e32 v112, v129
	v_cvt_pk_fp8_f32 v112, v100, v104
	s_waitcnt vmcnt(17)
	v_mul_f32_e32 v108, 0x43000000, v108
	s_waitcnt vmcnt(16)
	v_mul_f32_e32 v96, 0x43000000, v96
	v_med3_f32 v100, v108, s26, v147
	v_med3_f32 v96, v96, s26, v147
	v_cvt_pk_fp8_f32 v112, v100, v96 op_sel:[0,0,1]
	v_mul_f32_e32 v96, 0x43000000, v101
	v_mul_f32_e32 v100, 0x43000000, v105
	v_med3_f32 v96, v96, s26, v147
	v_med3_f32 v100, v100, s26, v147
	v_mov_b32_e32 v104, v129
	v_cvt_pk_fp8_f32 v104, v96, v100
	v_mul_f32_e32 v101, 0x43000000, v109
	v_mul_f32_e32 v96, 0x43000000, v97
	v_med3_f32 v97, v101, s26, v147
	v_med3_f32 v96, v96, s26, v147
	s_lshl_b32 s6, s13, 8
	v_cvt_pk_fp8_f32 v104, v97, v96 op_sel:[0,0,1]
	v_mul_f32_e32 v96, 0x43000000, v102
	v_mul_f32_e32 v97, 0x43000000, v106
	v_lshl_add_u64 v[64:65], v[132:133], 0, s[6:7]
	s_mul_i32 s6, s13, 0x104
	v_med3_f32 v96, v96, s26, v147
	v_med3_f32 v97, v97, s26, v147
	v_mov_b32_e32 v101, v129
	v_lshl_add_u64 v[66:67], v[132:133], 0, s[6:7]
	s_mul_i32 s6, s13, 0x108
	v_cvt_pk_fp8_f32 v101, v96, v97
	global_load_dwordx4 v[72:75], v[64:65], off nt
	global_load_dwordx4 v[80:83], v[66:67], off nt
	v_lshl_add_u64 v[64:65], v[132:133], 0, s[6:7]
	s_mul_i32 s6, s13, 0x10c
	v_lshl_add_u64 v[66:67], v[132:133], 0, s[6:7]
	s_mul_i32 s6, s13, 0x140
	v_mul_f32_e32 v100, 0x43000000, v110
	v_mul_f32_e32 v96, 0x43000000, v98
	global_load_dwordx4 v[92:95], v[64:65], off nt
	global_load_dwordx4 v[88:91], v[66:67], off nt
	v_lshl_add_u64 v[64:65], v[132:133], 0, s[6:7]
	s_mul_i32 s6, s13, 0x144
	v_med3_f32 v97, v100, s26, v147
	v_med3_f32 v96, v96, s26, v147
	v_lshl_add_u64 v[68:69], v[132:133], 0, s[6:7]
	s_mul_i32 s6, s13, 0x148
	v_cvt_pk_fp8_f32 v101, v97, v96 op_sel:[0,0,1]
	v_mul_f32_e32 v96, 0x43000000, v103
	v_mul_f32_e32 v97, 0x43000000, v107
	v_lshl_add_u64 v[76:77], v[132:133], 0, s[6:7]
	s_mul_i32 s6, s13, 0x14c
	v_med3_f32 v96, v96, s26, v147
	v_med3_f32 v97, v97, s26, v147
	v_mov_b32_e32 v100, v129
	v_lshl_add_u64 v[78:79], v[132:133], 0, s[6:7]
	v_cvt_pk_fp8_f32 v100, v96, v97
	s_add_i32 s6, s37, -1
	s_not_b32 s12, s37
	s_cmp_gt_i32 s37, 0
	global_load_dwordx4 v[64:67], v[64:65], off nt
	s_nop 0
	global_load_dwordx4 v[68:71], v[68:69], off nt
	s_nop 0
	global_load_dwordx4 v[84:87], v[76:77], off nt
	s_nop 0
	global_load_dwordx4 v[76:79], v[78:79], off nt
	v_mul_f32_e32 v98, 0x43000000, v111
	v_mul_f32_e32 v96, 0x43000000, v99
	s_cselect_b64 vcc, -1, 0
	v_med3_f32 v97, v98, s26, v147
	v_med3_f32 v96, v96, s26, v147
	s_and_b64 s[14:15], vcc, exec
	v_cvt_pk_fp8_f32 v100, v97, v96 op_sel:[0,0,1]
	s_cselect_b32 s6, s6, s12
	ds_write2_b32 v144, v148, v112 offset0:24 offset1:28
	ds_write2_b32 v144, v120, v104 offset0:57 offset1:61
	ds_write2_b32 v144, v117, v101 offset0:90 offset1:94
	ds_write2_b32 v144, v116, v100 offset0:123 offset1:127
	v_add_u32_e32 v100, s6, v194
	v_lshlrev_b32_e32 v101, 1, v100
	v_ashrrev_i32_e32 v102, 3, v100
	s_waitcnt lgkmcnt(0)
; #define LAS __attribute__((address_space(3)))
; #define LDS_WAIT() asm volatile("s_waitcnt lgkmcnt(0)" ::: "memory")
; __device__ __forceinline__ void moe_conv_stream(const Args& a, ARGAS unsigned char* ws, LAS unsigned char* scr, int first, int cnt, int lane) {
;     ...
;         LDS_WAIT(); asm volatile("" ::: "memory");
;         const int n0 = cur.gu > 0 ? cur.gu - 1 : -cur.gu - 1;
; #pragma unroll
;         for (int j = 0; j < 8; ++j) { const int row = (lane >> 3) + 8 * j; const LAS unsigned* s = (const LAS unsigned*)(scr + row * 132 + 16 * c8);
;             u32x4 o; o.x = s[0]; o.y = s[1]; o.z = s[2]; o.w = s[3];
;             const int n = n0 + row, wr_ = cur.gu > 0 ? RmGu()(n) : n;
;             *(u32x4*)(cur.dst + (size_t)wr_ * cur.ldk + 16 * c8) = o; }
;         LDS_WAIT(); asm volatile("" ::: "memory");
;         cur = nxt;
	v_and_b32_e32 v101, 0x700, v101
	v_and_b32_e32 v102, 0xffffff80, v102
	v_add_u32_e32 v101, v101, v102
	ds_read2_b32 v[96:97], v145 offset1:1
	ds_read2_b32 v[98:99], v145 offset0:2 offset1:3
	v_and_or_b32 v101, v100, s27, v101
	v_cndmask_b32_e32 v100, v100, v101, vcc
	v_ashrrev_i32_e32 v101, 31, v100
	v_lshl_add_u64 v[104:105], s[8:9], 0, v[130:131]
	v_lshlrev_b64 v[100:101], 10, v[100:101]
	v_lshl_add_u64 v[106:107], v[104:105], 0, v[100:101]
	v_add_u32_e32 v100, 0x420, v145
	v_add_u32_e32 v102, 0x428, v145
	ds_read2_b32 v[100:101], v100 offset1:1
	ds_read2_b32 v[102:103], v102 offset1:1
	s_waitcnt lgkmcnt(2)
	global_store_dwordx4 v[106:107], v[96:99], off
	s_add_i32 s38, s38, 8
	s_cmpk_eq_i32 s38, 0x88
	v_add_u32_e32 v96, s6, v135
	v_lshlrev_b32_e32 v97, 1, v96
	v_ashrrev_i32_e32 v98, 3, v96
	v_and_b32_e32 v97, 0x700, v97
	v_and_b32_e32 v98, 0xffffff80, v98
	v_add_u32_e32 v97, v97, v98
	v_and_or_b32 v97, v96, s27, v97
	v_cndmask_b32_e32 v96, v96, v97, vcc
	v_ashrrev_i32_e32 v97, 31, v96
	v_lshlrev_b64 v[96:97], 10, v[96:97]
	v_lshl_add_u64 v[96:97], v[104:105], 0, v[96:97]
	s_waitcnt lgkmcnt(0)
	global_store_dwordx4 v[96:97], v[100:103], off
	v_add_u32_e32 v96, 0x840, v145
	v_add_u32_e32 v98, 0x848, v145
	v_add_u32_e32 v100, s6, v136
	v_lshlrev_b32_e32 v101, 1, v100
	v_ashrrev_i32_e32 v102, 3, v100
	v_and_b32_e32 v101, 0x700, v101
	v_and_b32_e32 v102, 0xffffff80, v102
	v_add_u32_e32 v101, v101, v102
	ds_read2_b32 v[96:97], v96 offset1:1
	ds_read2_b32 v[98:99], v98 offset1:1
	v_and_or_b32 v101, v100, s27, v101
	v_cndmask_b32_e32 v100, v100, v101, vcc
	v_ashrrev_i32_e32 v101, 31, v100
	v_lshlrev_b64 v[100:101], 10, v[100:101]
	v_lshl_add_u64 v[106:107], v[104:105], 0, v[100:101]
	v_add_u32_e32 v100, 0xc60, v145
	v_add_u32_e32 v102, 0xc68, v145
	ds_read2_b32 v[100:101], v100 offset1:1
	ds_read2_b32 v[102:103], v102 offset1:1
	s_waitcnt lgkmcnt(2)
	global_store_dwordx4 v[106:107], v[96:99], off
	s_mov_b32 s37, s39
	s_mov_b64 s[8:9], s[10:11]
	v_add_u32_e32 v96, s6, v137
	v_lshlrev_b32_e32 v97, 1, v96
	v_ashrrev_i32_e32 v98, 3, v96
	v_and_b32_e32 v97, 0x700, v97
	v_and_b32_e32 v98, 0xffffff80, v98
	v_add_u32_e32 v97, v97, v98
	v_and_or_b32 v97, v96, s27, v97
	v_cndmask_b32_e32 v96, v96, v97, vcc
	v_ashrrev_i32_e32 v97, 31, v96
	v_lshlrev_b64 v[96:97], 10, v[96:97]
	v_lshl_add_u64 v[96:97], v[104:105], 0, v[96:97]
	s_waitcnt lgkmcnt(0)
	global_store_dwordx4 v[96:97], v[100:103], off
	v_add_u32_e32 v96, 0x1080, v145
	v_add_u32_e32 v98, 0x1088, v145
	v_add_u32_e32 v100, s6, v138
	v_lshlrev_b32_e32 v101, 1, v100
	v_ashrrev_i32_e32 v102, 3, v100
	v_and_b32_e32 v101, 0x700, v101
	v_and_b32_e32 v102, 0xffffff80, v102
	v_add_u32_e32 v101, v101, v102
	ds_read2_b32 v[96:97], v96 offset1:1
	ds_read2_b32 v[98:99], v98 offset1:1
	v_and_or_b32 v101, v100, s27, v101
	v_cndmask_b32_e32 v100, v100, v101, vcc
	v_ashrrev_i32_e32 v101, 31, v100
	v_lshlrev_b64 v[100:101], 10, v[100:101]
	v_lshl_add_u64 v[106:107], v[104:105], 0, v[100:101]
	v_add_u32_e32 v100, 0x14a0, v145
	v_add_u32_e32 v102, 0x14a8, v145
	ds_read2_b32 v[100:101], v100 offset1:1
	ds_read2_b32 v[102:103], v102 offset1:1
	s_waitcnt lgkmcnt(2)
	global_store_dwordx4 v[106:107], v[96:99], off
	s_nop 1
	v_add_u32_e32 v96, s6, v139
	v_lshlrev_b32_e32 v97, 1, v96
	v_ashrrev_i32_e32 v98, 3, v96
	v_and_b32_e32 v97, 0x700, v97
	v_and_b32_e32 v98, 0xffffff80, v98
	v_add_u32_e32 v97, v97, v98
	v_and_or_b32 v97, v96, s27, v97
	v_cndmask_b32_e32 v96, v96, v97, vcc
	v_ashrrev_i32_e32 v97, 31, v96
	v_lshlrev_b64 v[96:97], 10, v[96:97]
	v_lshl_add_u64 v[96:97], v[104:105], 0, v[96:97]
	s_waitcnt lgkmcnt(0)
	global_store_dwordx4 v[96:97], v[100:103], off
	v_add_u32_e32 v96, 0x18c0, v145
	v_add_u32_e32 v98, 0x18c8, v145
	v_add_u32_e32 v100, s6, v140
	v_lshlrev_b32_e32 v101, 1, v100
	v_ashrrev_i32_e32 v102, 3, v100
	v_and_b32_e32 v101, 0x700, v101
	v_and_b32_e32 v102, 0xffffff80, v102
	v_add_u32_e32 v101, v101, v102
	ds_read2_b32 v[96:97], v96 offset1:1
	ds_read2_b32 v[98:99], v98 offset1:1
	v_and_or_b32 v101, v100, s27, v101
	v_cndmask_b32_e32 v100, v100, v101, vcc
	v_ashrrev_i32_e32 v101, 31, v100
	v_lshlrev_b64 v[100:101], 10, v[100:101]
	v_lshl_add_u64 v[106:107], v[104:105], 0, v[100:101]
	v_add_u32_e32 v100, 0x1ce0, v145
	v_add_u32_e32 v102, 0x1ce8, v145
	ds_read2_b32 v[100:101], v100 offset1:1
	ds_read2_b32 v[102:103], v102 offset1:1
	s_waitcnt lgkmcnt(2)
	global_store_dwordx4 v[106:107], v[96:99], off
	s_nop 1
	v_add_u32_e32 v96, s6, v141
	v_lshlrev_b32_e32 v97, 1, v96
	v_ashrrev_i32_e32 v98, 3, v96
	v_and_b32_e32 v97, 0x700, v97
	v_and_b32_e32 v98, 0xffffff80, v98
	v_add_u32_e32 v97, v97, v98
	v_and_or_b32 v97, v96, s27, v97
	v_cndmask_b32_e32 v96, v96, v97, vcc
	v_ashrrev_i32_e32 v97, 31, v96
	v_lshlrev_b64 v[96:97], 10, v[96:97]
	v_lshl_add_u64 v[96:97], v[104:105], 0, v[96:97]
	s_waitcnt lgkmcnt(0)
	global_store_dwordx4 v[96:97], v[100:103], off
	s_waitcnt lgkmcnt(0)
	s_mov_b32 s6, s13
	v_mov_b64_e32 v[96:97], v[132:133]
	s_cbranch_scc1 .LBB0_654

; #define LAS __attribute__((address_space(3)))
; #define CV_LOAD(qi, Q, D) do { _Pragma("unroll") for (int s_ = 0; s_ < 2; ++s_) _Pragma("unroll") for (int r_ = 0; r_ < 4; ++r_) Q.v[s_][r_] = *(const f32x4*)(D.src + (size_t)(16 * (2 * (qi) + s_) + r_) * D.N); asm volatile("" ::: "memory"); } while (0)
; #define CV_PROC(qi, Q) do { _Pragma("unroll") for (int s_ = 0; s_ < 2; ++s_) _Pragma("unroll") for (int c_ = 0; c_ < 4; ++c_) \
;         *(LAS unsigned*)(scr + (4 * nl + c_) * 132 + 16 * (2 * (qi) + s_) + 4 * kg) = pg8::pk4_fp8c(Q.v[s_][0][c_] * FP8_WSC, Q.v[s_][1][c_] * FP8_WSC, Q.v[s_][2][c_] * FP8_WSC, Q.v[s_][3][c_] * FP8_WSC); asm volatile("" ::: "memory"); } while (0)
; __device__ __forceinline__ void moe_conv_stream(const Args& a, ARGAS unsigned char* ws, LAS unsigned char* scr, int first, int cnt, int lane) {
;     const int nl = lane & 15, kg = lane >> 4, c8 = lane & 7;
;     struct Qt { f32x4 v[2][4]; };
;     ...
;     Qt A, B, C, D4;
;     ConvItem cur = moe_conv_desc(a, ws, first, lane);
;     CV_LOAD(0, A, cur); CV_LOAD(1, B, cur); CV_LOAD(2, C, cur);
; #pragma unroll 1
;     for (int i = 0; i < cnt; ++i) {
;         const ConvItem nxt = moe_conv_desc(a, ws, first + 8 * ((i + 1 < cnt) ? i + 1 : i), lane);
;         CV_LOAD(3, D4, cur); CV_PROC(0, A);
;         CV_LOAD(0, A, nxt);  CV_PROC(1, B);
;         CV_LOAD(1, B, nxt);  CV_PROC(2, C);
;         CV_LOAD(2, C, nxt);  CV_PROC(3, D4);
.LBB0_3126:
	v_lshl_add_u64 v[96:97], v[0:1], 0, v[128:129]
	s_lshl_b32 s6, s11, 2
	v_lshl_add_u64 v[0:1], v[96:97], 0, s[6:7]
	s_lshl_b32 s6, s11, 3
	v_lshl_add_u64 v[2:3], v[96:97], 0, s[6:7]
	s_mul_i32 s6, s11, 12
	s_waitcnt vmcnt(26)
	v_lshl_add_u64 v[4:5], v[96:97], 0, s[6:7]
	s_lshl_b32 s6, s11, 6
	v_lshl_add_u64 v[6:7], v[96:97], 0, s[6:7]
	s_mul_i32 s6, s11, 0x44
	s_waitcnt vmcnt(24)
	v_lshl_add_u64 v[12:13], v[96:97], 0, s[6:7]
	s_mul_i32 s6, s11, 0x48
	v_lshl_add_u64 v[14:15], v[96:97], 0, s[6:7]
	s_mul_i32 s6, s11, 0x4c
	s_waitcnt vmcnt(19)
	v_lshl_add_u64 v[32:33], v[96:97], 0, s[6:7]
	s_lshl_b32 s6, s11, 7
	global_load_dwordx4 v[16:19], v[0:1], off nt
	global_load_dwordx4 v[20:23], v[2:3], off nt
	global_load_dwordx4 v[24:27], v[4:5], off nt
	s_nop 0
	global_load_dwordx4 v[0:3], v[6:7], off nt
	s_nop 0
	global_load_dwordx4 v[4:7], v[12:13], off nt
	global_load_dwordx4 v[8:11], v[14:15], off nt
	global_load_dwordx4 v[28:31], v[96:97], off nt
	s_nop 0
	global_load_dwordx4 v[12:15], v[32:33], off nt
	v_lshl_add_u64 v[32:33], v[96:97], 0, s[6:7]
	s_mul_i32 s6, s11, 0x84
	v_lshl_add_u64 v[34:35], v[96:97], 0, s[6:7]
	s_mul_i32 s6, s11, 0x88
	global_load_dwordx4 v[40:43], v[32:33], off nt
	global_load_dwordx4 v[48:51], v[34:35], off nt
	v_lshl_add_u64 v[32:33], v[96:97], 0, s[6:7]
	s_mul_i32 s6, s11, 0x8c
	v_lshl_add_u64 v[34:35], v[96:97], 0, s[6:7]
	s_mul_i32 s6, s11, 0xc0
	s_waitcnt vmcnt(26)
	v_lshl_add_u64 v[44:45], v[96:97], 0, s[6:7]
	s_mul_i32 s6, s11, 0xc4
	v_lshl_add_u64 v[46:47], v[96:97], 0, s[6:7]
	s_mul_i32 s6, s11, 0xc8
	s_waitcnt vmcnt(21)
	v_lshl_add_u64 v[64:65], v[96:97], 0, s[6:7]
	s_mul_i32 s6, s11, 0xcc
	v_lshl_add_u64 v[66:67], v[96:97], 0, s[6:7]
	s_lshl_b32 s6, s11, 8
	global_load_dwordx4 v[60:63], v[32:33], off nt
	global_load_dwordx4 v[56:59], v[34:35], off nt
	s_nop 0
	global_load_dwordx4 v[32:35], v[44:45], off nt
	global_load_dwordx4 v[36:39], v[46:47], off nt
	global_load_dwordx4 v[52:55], v[64:65], off nt
	s_nop 0
	global_load_dwordx4 v[44:47], v[66:67], off nt
	v_lshl_add_u64 v[64:65], v[96:97], 0, s[6:7]
	s_mul_i32 s6, s11, 0x104
	v_lshl_add_u64 v[66:67], v[96:97], 0, s[6:7]
	s_mul_i32 s6, s11, 0x108
	global_load_dwordx4 v[72:75], v[64:65], off nt
	global_load_dwordx4 v[80:83], v[66:67], off nt
	v_lshl_add_u64 v[64:65], v[96:97], 0, s[6:7]
	s_mul_i32 s6, s11, 0x10c
	v_lshl_add_u64 v[66:67], v[96:97], 0, s[6:7]
	s_mul_i32 s6, s11, 0x140
	s_waitcnt vmcnt(26)
	v_lshl_add_u64 v[76:77], v[96:97], 0, s[6:7]
	s_mul_i32 s6, s11, 0x144
	v_lshl_add_u64 v[78:79], v[96:97], 0, s[6:7]
	s_mul_i32 s6, s11, 0x148
	v_lshl_add_u64 v[98:99], v[96:97], 0, s[6:7]
	s_mul_i32 s6, s11, 0x14c
	global_load_dwordx4 v[92:95], v[64:65], off nt
	global_load_dwordx4 v[88:91], v[66:67], off nt
	s_nop 0
	global_load_dwordx4 v[64:67], v[76:77], off nt
	global_load_dwordx4 v[68:71], v[78:79], off nt
	v_lshl_add_u64 v[100:101], v[96:97], 0, s[6:7]
	global_load_dwordx4 v[84:87], v[98:99], off nt
	global_load_dwordx4 v[76:79], v[100:101], off nt
	s_mov_b32 s41, 8
	s_mov_b32 s6, s11
	s_branch .LBB0_3128
.LBB0_3127:
	s_waitcnt vmcnt(17)
	v_mul_f32_e32 v28, 0x43000000, v28
	v_mul_f32_e32 v16, 0x43000000, v16
	v_med3_f32 v28, v28, s37, v149
	v_med3_f32 v16, v16, s37, v149
	v_mov_b32_e32 v150, v129
	v_cvt_pk_fp8_f32 v150, v28, v16
	v_mul_f32_e32 v20, 0x43000000, v20
	v_mul_f32_e32 v16, 0x43000000, v24
	v_med3_f32 v20, v20, s37, v149
	v_med3_f32 v16, v16, s37, v149
	v_cvt_pk_fp8_f32 v150, v20, v16 op_sel:[0,0,1]
	v_mul_f32_e32 v16, 0x43000000, v29
	v_mul_f32_e32 v17, 0x43000000, v17
	v_mul_f32_e32 v20, 0x43000000, v21
	v_med3_f32 v16, v16, s37, v149
	v_med3_f32 v17, v17, s37, v149
	v_mov_b32_e32 v21, v129
	v_cvt_pk_fp8_f32 v21, v16, v17
	v_mul_f32_e32 v16, 0x43000000, v25
	v_med3_f32 v17, v20, s37, v149
	v_med3_f32 v16, v16, s37, v149
	v_cvt_pk_fp8_f32 v21, v17, v16 op_sel:[0,0,1]
	v_mul_f32_e32 v16, 0x43000000, v30
	v_mul_f32_e32 v17, 0x43000000, v18
	v_med3_f32 v16, v16, s37, v149
	v_med3_f32 v17, v17, s37, v149
	v_mov_b32_e32 v20, v129
	v_cvt_pk_fp8_f32 v20, v16, v17
	v_mul_f32_e32 v18, 0x43000000, v22
	v_mul_f32_e32 v16, 0x43000000, v26
	v_med3_f32 v17, v18, s37, v149
	v_med3_f32 v16, v16, s37, v149
	v_cvt_pk_fp8_f32 v20, v17, v16 op_sel:[0,0,1]
	v_mul_f32_e32 v16, 0x43000000, v31
	v_mul_f32_e32 v17, 0x43000000, v19
	v_med3_f32 v16, v16, s37, v149
	v_med3_f32 v17, v17, s37, v149
	v_mov_b32_e32 v19, v129
	v_cvt_pk_fp8_f32 v19, v16, v17
	v_mul_f32_e32 v18, 0x43000000, v23
	v_mul_f32_e32 v16, 0x43000000, v27
	v_med3_f32 v17, v18, s37, v149
	v_med3_f32 v16, v16, s37, v149
	v_mul_f32_e32 v0, 0x43000000, v0
	v_mul_f32_e32 v4, 0x43000000, v4
	v_cvt_pk_fp8_f32 v19, v17, v16 op_sel:[0,0,1]
	v_med3_f32 v0, v0, s37, v149
	v_med3_f32 v4, v4, s37, v149
	v_mov_b32_e32 v16, v129
	v_cvt_pk_fp8_f32 v16, v0, v4
	v_mul_f32_e32 v8, 0x43000000, v8
	s_waitcnt vmcnt(16)
; #define CV_LOAD(qi, Q, D) do { _Pragma("unroll") for (int s_ = 0; s_ < 2; ++s_) _Pragma("unroll") for (int r_ = 0; r_ < 4; ++r_) Q.v[s_][r_] = *(const f32x4*)(D.src + (size_t)(16 * (2 * (qi) + s_) + r_) * D.N); asm volatile("" ::: "memory"); } while (0)
; #define CV_PROC(qi, Q) do { _Pragma("unroll") for (int s_ = 0; s_ < 2; ++s_) _Pragma("unroll") for (int c_ = 0; c_ < 4; ++c_) \
;         *(LAS unsigned*)(scr + (4 * nl + c_) * 132 + 16 * (2 * (qi) + s_) + 4 * kg) = pg8::pk4_fp8c(Q.v[s_][0][c_] * FP8_WSC, Q.v[s_][1][c_] * FP8_WSC, Q.v[s_][2][c_] * FP8_WSC, Q.v[s_][3][c_] * FP8_WSC); asm volatile("" ::: "memory"); } while (0)
; __device__ __forceinline__ void moe_conv_stream(const Args& a, ARGAS unsigned char* ws, LAS unsigned char* scr, int first, int cnt, int lane) {
;     ...
;     Qt A, B, C, D4;
;     ConvItem cur = moe_conv_desc(a, ws, first, lane);
;     CV_LOAD(0, A, cur); CV_LOAD(1, B, cur); CV_LOAD(2, C, cur);
; #pragma unroll 1
;     for (int i = 0; i < cnt; ++i) {
;         const ConvItem nxt = moe_conv_desc(a, ws, first + 8 * ((i + 1 < cnt) ? i + 1 : i), lane);
;         CV_LOAD(3, D4, cur); CV_PROC(0, A);
;         CV_LOAD(0, A, nxt);  CV_PROC(1, B);
;         CV_LOAD(1, B, nxt);  CV_PROC(2, C);
;         CV_LOAD(2, C, nxt);  CV_PROC(3, D4);
	v_mul_f32_e32 v0, 0x43000000, v12
	v_med3_f32 v4, v8, s37, v149
	v_med3_f32 v0, v0, s37, v149
	v_cvt_pk_fp8_f32 v16, v4, v0 op_sel:[0,0,1]
	v_mul_f32_e32 v0, 0x43000000, v1
	v_mul_f32_e32 v1, 0x43000000, v5
	v_med3_f32 v0, v0, s37, v149
	v_med3_f32 v1, v1, s37, v149
	v_mov_b32_e32 v5, v129
	v_cvt_pk_fp8_f32 v5, v0, v1
	v_mul_f32_e32 v4, 0x43000000, v9
	v_mul_f32_e32 v0, 0x43000000, v13
	v_med3_f32 v1, v4, s37, v149
	v_med3_f32 v0, v0, s37, v149
	v_cvt_pk_fp8_f32 v5, v1, v0 op_sel:[0,0,1]
	v_mul_f32_e32 v0, 0x43000000, v2
	v_mul_f32_e32 v1, 0x43000000, v6
	v_med3_f32 v0, v0, s37, v149
	v_med3_f32 v1, v1, s37, v149
	v_mov_b32_e32 v4, v129
	v_cvt_pk_fp8_f32 v4, v0, v1
	v_mad_u64_u32 v[96:97], s[14:15], s6, v148, v[96:97]
	v_mul_f32_e32 v2, 0x43000000, v10
	v_mul_f32_e32 v0, 0x43000000, v14
	s_lshl_b64 s[14:15], s[6:7], 2
	v_med3_f32 v1, v2, s37, v149
	v_med3_f32 v0, v0, s37, v149
	v_lshl_add_u64 v[132:133], v[98:99], 0, v[128:129]
	v_lshl_add_u64 v[98:99], v[96:97], 0, s[14:15]
	v_cvt_pk_fp8_f32 v4, v1, v0 op_sel:[0,0,1]
	v_mul_f32_e32 v0, 0x43000000, v3
	v_mul_f32_e32 v1, 0x43000000, v7
	global_load_dwordx4 v[116:119], v[96:97], off nt
	global_load_dwordx4 v[120:123], v[98:99], off nt
	v_lshl_add_u64 v[96:97], v[98:99], 0, s[14:15]
	v_med3_f32 v0, v0, s37, v149
	v_med3_f32 v1, v1, s37, v149
	v_mov_b32_e32 v3, v129
	v_lshl_add_u64 v[98:99], v[96:97], 0, s[14:15]
	v_cvt_pk_fp8_f32 v3, v0, v1
	global_load_dwordx4 v[124:127], v[96:97], off nt
	global_load_dwordx4 v[112:115], v[98:99], off nt
	v_mad_u64_u32 v[96:97], s[48:49], s6, 52, v[98:99]
	v_lshl_add_u64 v[98:99], v[96:97], 0, s[14:15]
	v_mul_f32_e32 v2, 0x43000000, v11
	v_mul_f32_e32 v0, 0x43000000, v15
	global_load_dwordx4 v[100:103], v[96:97], off nt
	global_load_dwordx4 v[104:107], v[98:99], off nt
	v_lshl_add_u64 v[96:97], v[98:99], 0, s[14:15]
	v_med3_f32 v1, v2, s37, v149
	v_med3_f32 v0, v0, s37, v149
	v_lshl_add_u64 v[98:99], v[96:97], 0, s[14:15]
	v_cvt_pk_fp8_f32 v3, v1, v0 op_sel:[0,0,1]
	s_waitcnt vmcnt(21)
	v_mul_f32_e32 v40, 0x43000000, v40
	s_waitcnt vmcnt(20)
	v_mul_f32_e32 v48, 0x43000000, v48
	global_load_dwordx4 v[108:111], v[96:97], off nt
	s_nop 0
	global_load_dwordx4 v[96:99], v[98:99], off nt
	ds_write2_b32 v145, v150, v16 offset1:4
	ds_write2_b32 v145, v21, v5 offset0:33 offset1:37
	ds_write2_b32 v145, v20, v4 offset0:66 offset1:70
	ds_write2_b32 v145, v19, v3 offset0:99 offset1:103
	v_med3_f32 v40, v40, s37, v149
	v_med3_f32 v48, v48, s37, v149
	v_mov_b32_e32 v150, v129
	v_cvt_pk_fp8_f32 v150, v40, v48
	s_waitcnt vmcnt(21)
	v_mul_f32_e32 v60, 0x43000000, v60
	s_waitcnt vmcnt(20)
	v_mul_f32_e32 v40, 0x43000000, v56
	v_med3_f32 v48, v60, s37, v149
	v_med3_f32 v40, v40, s37, v149
	v_cvt_pk_fp8_f32 v150, v48, v40 op_sel:[0,0,1]
	v_mul_f32_e32 v40, 0x43000000, v41
	v_mul_f32_e32 v41, 0x43000000, v49
	v_med3_f32 v40, v40, s37, v149
	v_med3_f32 v41, v41, s37, v149
	v_mov_b32_e32 v49, v129
	v_cvt_pk_fp8_f32 v49, v40, v41
	v_mul_f32_e32 v48, 0x43000000, v61
	v_mul_f32_e32 v40, 0x43000000, v57
	v_med3_f32 v41, v48, s37, v149
	v_med3_f32 v40, v40, s37, v149
	v_cvt_pk_fp8_f32 v49, v41, v40 op_sel:[0,0,1]
	v_mul_f32_e32 v40, 0x43000000, v42
	v_mul_f32_e32 v41, 0x43000000, v50
	v_med3_f32 v40, v40, s37, v149
	v_med3_f32 v41, v41, s37, v149
	v_mov_b32_e32 v48, v129
	v_cvt_pk_fp8_f32 v48, v40, v41
	v_mul_f32_e32 v42, 0x43000000, v62
	v_mul_f32_e32 v40, 0x43000000, v58
	v_med3_f32 v41, v42, s37, v149
	v_med3_f32 v40, v40, s37, v149
	v_cvt_pk_fp8_f32 v48, v41, v40 op_sel:[0,0,1]
	v_mul_f32_e32 v40, 0x43000000, v43
	v_mul_f32_e32 v41, 0x43000000, v51
	v_med3_f32 v40, v40, s37, v149
	v_med3_f32 v41, v41, s37, v149
	v_mov_b32_e32 v43, v129
	v_cvt_pk_fp8_f32 v43, v40, v41
	v_mul_f32_e32 v42, 0x43000000, v63
	v_mul_f32_e32 v40, 0x43000000, v59
	v_med3_f32 v41, v42, s37, v149
	v_med3_f32 v40, v40, s37, v149
	s_waitcnt vmcnt(19)
	v_mul_f32_e32 v32, 0x43000000, v32
	s_waitcnt vmcnt(18)
	v_mul_f32_e32 v36, 0x43000000, v36
	v_cvt_pk_fp8_f32 v43, v41, v40 op_sel:[0,0,1]
	v_med3_f32 v32, v32, s37, v149
	v_med3_f32 v36, v36, s37, v149
	v_mov_b32_e32 v41, v129
	v_cvt_pk_fp8_f32 v41, v32, v36
	s_waitcnt vmcnt(17)
	v_mul_f32_e32 v40, 0x43000000, v52
	s_waitcnt vmcnt(16)
	v_mul_f32_e32 v32, 0x43000000, v44
	v_med3_f32 v36, v40, s37, v149
	v_med3_f32 v32, v32, s37, v149
	v_cvt_pk_fp8_f32 v41, v36, v32 op_sel:[0,0,1]
	v_mul_f32_e32 v32, 0x43000000, v33
	v_mul_f32_e32 v33, 0x43000000, v37
	v_med3_f32 v32, v32, s37, v149
	v_med3_f32 v33, v33, s37, v149
	v_mov_b32_e32 v37, v129
	v_cvt_pk_fp8_f32 v37, v32, v33
	v_mul_f32_e32 v36, 0x43000000, v53
	v_mul_f32_e32 v32, 0x43000000, v45
	v_med3_f32 v33, v36, s37, v149
	v_med3_f32 v32, v32, s37, v149
	v_cvt_pk_fp8_f32 v37, v33, v32 op_sel:[0,0,1]
	v_mul_f32_e32 v32, 0x43000000, v34
	v_mul_f32_e32 v33, 0x43000000, v38
	v_med3_f32 v32, v32, s37, v149
	v_med3_f32 v33, v33, s37, v149
	v_mov_b32_e32 v36, v129
	v_cvt_pk_fp8_f32 v36, v32, v33
	v_mul_f32_e32 v34, 0x43000000, v54
	v_mul_f32_e32 v32, 0x43000000, v46
	s_lshl_b32 s6, s13, 2
	v_med3_f32 v33, v34, s37, v149
	v_med3_f32 v32, v32, s37, v149
	v_lshl_add_u64 v[0:1], v[132:133], 0, s[6:7]
	s_lshl_b32 s6, s13, 3
	v_cvt_pk_fp8_f32 v36, v33, v32 op_sel:[0,0,1]
	v_mul_f32_e32 v32, 0x43000000, v35
	v_mul_f32_e32 v33, 0x43000000, v39
	global_load_dwordx4 v[28:31], v[132:133], off nt
	global_load_dwordx4 v[16:19], v[0:1], off nt
	v_lshl_add_u64 v[0:1], v[132:133], 0, s[6:7]
	s_mul_i32 s6, s13, 12
	v_med3_f32 v32, v32, s37, v149
	v_med3_f32 v33, v33, s37, v149
	v_mov_b32_e32 v35, v129
	v_lshl_add_u64 v[2:3], v[132:133], 0, s[6:7]
	s_lshl_b32 s6, s13, 6
	v_cvt_pk_fp8_f32 v35, v32, v33
	global_load_dwordx4 v[20:23], v[0:1], off nt
	global_load_dwordx4 v[24:27], v[2:3], off nt
	v_lshl_add_u64 v[0:1], v[132:133], 0, s[6:7]
	s_mul_i32 s6, s13, 0x44
	v_lshl_add_u64 v[4:5], v[132:133], 0, s[6:7]
	s_mul_i32 s6, s13, 0x48
	v_mul_f32_e32 v34, 0x43000000, v55
	v_mul_f32_e32 v32, 0x43000000, v47
	v_lshl_add_u64 v[8:9], v[132:133], 0, s[6:7]
	s_mul_i32 s6, s13, 0x4c
	v_med3_f32 v33, v34, s37, v149
	v_med3_f32 v32, v32, s37, v149
	v_lshl_add_u64 v[12:13], v[132:133], 0, s[6:7]
	v_cvt_pk_fp8_f32 v35, v33, v32 op_sel:[0,0,1]
	s_waitcnt vmcnt(19)
; #define CV_LOAD(qi, Q, D) do { _Pragma("unroll") for (int s_ = 0; s_ < 2; ++s_) _Pragma("unroll") for (int r_ = 0; r_ < 4; ++r_) Q.v[s_][r_] = *(const f32x4*)(D.src + (size_t)(16 * (2 * (qi) + s_) + r_) * D.N); asm volatile("" ::: "memory"); } while (0)
; #define CV_PROC(qi, Q) do { _Pragma("unroll") for (int s_ = 0; s_ < 2; ++s_) _Pragma("unroll") for (int c_ = 0; c_ < 4; ++c_) \
;         *(LAS unsigned*)(scr + (4 * nl + c_) * 132 + 16 * (2 * (qi) + s_) + 4 * kg) = pg8::pk4_fp8c(Q.v[s_][0][c_] * FP8_WSC, Q.v[s_][1][c_] * FP8_WSC, Q.v[s_][2][c_] * FP8_WSC, Q.v[s_][3][c_] * FP8_WSC); asm volatile("" ::: "memory"); } while (0)
; __device__ __forceinline__ void moe_conv_stream(const Args& a, ARGAS unsigned char* ws, LAS unsigned char* scr, int first, int cnt, int lane) {
;     ...
;     Qt A, B, C, D4;
;     ConvItem cur = moe_conv_desc(a, ws, first, lane);
;     CV_LOAD(0, A, cur); CV_LOAD(1, B, cur); CV_LOAD(2, C, cur);
; #pragma unroll 1
;     for (int i = 0; i < cnt; ++i) {
;         const ConvItem nxt = moe_conv_desc(a, ws, first + 8 * ((i + 1 < cnt) ? i + 1 : i), lane);
;         CV_LOAD(3, D4, cur); CV_PROC(0, A);
;         CV_LOAD(0, A, nxt);  CV_PROC(1, B);
;         CV_LOAD(1, B, nxt);  CV_PROC(2, C);
;         CV_LOAD(2, C, nxt);  CV_PROC(3, D4);
	v_mul_f32_e32 v72, 0x43000000, v72
	s_waitcnt vmcnt(18)
	v_mul_f32_e32 v80, 0x43000000, v80
	global_load_dwordx4 v[0:3], v[0:1], off nt
	s_nop 0
	global_load_dwordx4 v[4:7], v[4:5], off nt
	s_nop 0
	global_load_dwordx4 v[8:11], v[8:9], off nt
	s_nop 0
	global_load_dwordx4 v[12:15], v[12:13], off nt
	ds_write2_b32 v146, v150, v41 offset0:8 offset1:12
	ds_write2_b32 v146, v49, v37 offset0:41 offset1:45
	ds_write2_b32 v146, v48, v36 offset0:74 offset1:78
	ds_write2_b32 v146, v43, v35 offset0:107 offset1:111
	v_med3_f32 v72, v72, s37, v149
	v_med3_f32 v80, v80, s37, v149
	v_mov_b32_e32 v150, v129
	v_cvt_pk_fp8_f32 v150, v72, v80
	s_waitcnt vmcnt(21)
	v_mul_f32_e32 v92, 0x43000000, v92
	s_waitcnt vmcnt(20)
	v_mul_f32_e32 v72, 0x43000000, v88
	v_med3_f32 v80, v92, s37, v149
	v_med3_f32 v72, v72, s37, v149
	v_cvt_pk_fp8_f32 v150, v80, v72 op_sel:[0,0,1]
	v_mul_f32_e32 v72, 0x43000000, v73
	v_mul_f32_e32 v73, 0x43000000, v81
	v_med3_f32 v72, v72, s37, v149
	v_med3_f32 v73, v73, s37, v149
	v_mov_b32_e32 v81, v129
	v_cvt_pk_fp8_f32 v81, v72, v73
	v_mul_f32_e32 v80, 0x43000000, v93
	v_mul_f32_e32 v72, 0x43000000, v89
	v_med3_f32 v73, v80, s37, v149
	v_med3_f32 v72, v72, s37, v149
	v_cvt_pk_fp8_f32 v81, v73, v72 op_sel:[0,0,1]
	v_mul_f32_e32 v72, 0x43000000, v74
	v_mul_f32_e32 v73, 0x43000000, v82
	v_med3_f32 v72, v72, s37, v149
	v_med3_f32 v73, v73, s37, v149
	v_mov_b32_e32 v80, v129
	v_cvt_pk_fp8_f32 v80, v72, v73
	v_mul_f32_e32 v74, 0x43000000, v94
	v_mul_f32_e32 v72, 0x43000000, v90
	v_med3_f32 v73, v74, s37, v149
	v_med3_f32 v72, v72, s37, v149
	v_cvt_pk_fp8_f32 v80, v73, v72 op_sel:[0,0,1]
	v_mul_f32_e32 v72, 0x43000000, v75
	v_mul_f32_e32 v73, 0x43000000, v83
	v_med3_f32 v72, v72, s37, v149
	v_med3_f32 v73, v73, s37, v149
	v_mov_b32_e32 v75, v129
	v_cvt_pk_fp8_f32 v75, v72, v73
	v_mul_f32_e32 v74, 0x43000000, v95
	v_mul_f32_e32 v72, 0x43000000, v91
	v_med3_f32 v73, v74, s37, v149
	v_med3_f32 v72, v72, s37, v149
	s_waitcnt vmcnt(19)
	v_mul_f32_e32 v64, 0x43000000, v64
	s_waitcnt vmcnt(18)
	v_mul_f32_e32 v68, 0x43000000, v68
	v_cvt_pk_fp8_f32 v75, v73, v72 op_sel:[0,0,1]
	v_med3_f32 v64, v64, s37, v149
	v_med3_f32 v68, v68, s37, v149
	v_mov_b32_e32 v73, v129
	v_cvt_pk_fp8_f32 v73, v64, v68
	s_waitcnt vmcnt(17)
	v_mul_f32_e32 v72, 0x43000000, v84
	s_waitcnt vmcnt(16)
	v_mul_f32_e32 v64, 0x43000000, v76
	v_med3_f32 v68, v72, s37, v149
	v_med3_f32 v64, v64, s37, v149
	v_cvt_pk_fp8_f32 v73, v68, v64 op_sel:[0,0,1]
	v_mul_f32_e32 v64, 0x43000000, v65
	v_mul_f32_e32 v65, 0x43000000, v69
	v_med3_f32 v64, v64, s37, v149
	v_med3_f32 v65, v65, s37, v149
	v_mov_b32_e32 v69, v129
	v_cvt_pk_fp8_f32 v69, v64, v65
	v_mul_f32_e32 v68, 0x43000000, v85
	v_mul_f32_e32 v64, 0x43000000, v77
	v_med3_f32 v65, v68, s37, v149
	v_med3_f32 v64, v64, s37, v149
	v_cvt_pk_fp8_f32 v69, v65, v64 op_sel:[0,0,1]
	v_mul_f32_e32 v64, 0x43000000, v66
	v_mul_f32_e32 v65, 0x43000000, v70
	v_med3_f32 v64, v64, s37, v149
	v_med3_f32 v65, v65, s37, v149
	v_mov_b32_e32 v68, v129
	v_cvt_pk_fp8_f32 v68, v64, v65
	s_lshl_b32 s6, s13, 7
	v_mul_f32_e32 v66, 0x43000000, v86
	v_mul_f32_e32 v64, 0x43000000, v78
	v_lshl_add_u64 v[32:33], v[132:133], 0, s[6:7]
	s_mul_i32 s6, s13, 0x84
	v_med3_f32 v65, v66, s37, v149
	v_med3_f32 v64, v64, s37, v149
	v_lshl_add_u64 v[34:35], v[132:133], 0, s[6:7]
	s_mul_i32 s6, s13, 0x88
	v_cvt_pk_fp8_f32 v68, v65, v64 op_sel:[0,0,1]
	v_mul_f32_e32 v64, 0x43000000, v67
	v_mul_f32_e32 v65, 0x43000000, v71
	global_load_dwordx4 v[40:43], v[32:33], off nt
	global_load_dwordx4 v[48:51], v[34:35], off nt
	v_lshl_add_u64 v[32:33], v[132:133], 0, s[6:7]
	s_mul_i32 s6, s13, 0x8c
	v_med3_f32 v64, v64, s37, v149
	v_med3_f32 v65, v65, s37, v149
	v_mov_b32_e32 v67, v129
	v_lshl_add_u64 v[34:35], v[132:133], 0, s[6:7]
	s_mul_i32 s6, s13, 0xc0
	v_cvt_pk_fp8_f32 v67, v64, v65
	global_load_dwordx4 v[60:63], v[32:33], off nt
	global_load_dwordx4 v[56:59], v[34:35], off nt
	v_lshl_add_u64 v[32:33], v[132:133], 0, s[6:7]
	s_mul_i32 s6, s13, 0xc4
	v_lshl_add_u64 v[36:37], v[132:133], 0, s[6:7]
	s_mul_i32 s6, s13, 0xc8
	v_mul_f32_e32 v66, 0x43000000, v87
	v_mul_f32_e32 v64, 0x43000000, v79
	v_lshl_add_u64 v[44:45], v[132:133], 0, s[6:7]
	s_mul_i32 s6, s13, 0xcc
	v_med3_f32 v65, v66, s37, v149
	v_med3_f32 v64, v64, s37, v149
	v_lshl_add_u64 v[46:47], v[132:133], 0, s[6:7]
	v_cvt_pk_fp8_f32 v67, v65, v64 op_sel:[0,0,1]
	s_waitcnt vmcnt(19)
	v_mul_f32_e32 v116, 0x43000000, v116
	s_waitcnt vmcnt(18)
	v_mul_f32_e32 v120, 0x43000000, v120
	global_load_dwordx4 v[32:35], v[32:33], off nt
	s_nop 0
	global_load_dwordx4 v[36:39], v[36:37], off nt
	s_nop 0
	global_load_dwordx4 v[52:55], v[44:45], off nt
	s_nop 0
	global_load_dwordx4 v[44:47], v[46:47], off nt
	ds_write2_b32 v146, v150, v73 offset0:16 offset1:20
	ds_write2_b32 v146, v81, v69 offset0:49 offset1:53
	ds_write2_b32 v146, v80, v68 offset0:82 offset1:86
	ds_write2_b32 v146, v75, v67 offset0:115 offset1:119
	v_med3_f32 v116, v116, s37, v149
	v_med3_f32 v120, v120, s37, v149
	v_mov_b32_e32 v150, v129
	v_cvt_pk_fp8_f32 v150, v116, v120
	s_waitcnt vmcnt(21)
	v_mul_f32_e32 v124, 0x43000000, v124
	s_waitcnt vmcnt(20)
; #define LAS __attribute__((address_space(3)))
; #define LDS_WAIT() asm volatile("s_waitcnt lgkmcnt(0)" ::: "memory")
; #define CV_LOAD(qi, Q, D) do { _Pragma("unroll") for (int s_ = 0; s_ < 2; ++s_) _Pragma("unroll") for (int r_ = 0; r_ < 4; ++r_) Q.v[s_][r_] = *(const f32x4*)(D.src + (size_t)(16 * (2 * (qi) + s_) + r_) * D.N); asm volatile("" ::: "memory"); } while (0)
; #define CV_PROC(qi, Q) do { _Pragma("unroll") for (int s_ = 0; s_ < 2; ++s_) _Pragma("unroll") for (int c_ = 0; c_ < 4; ++c_) \
;         *(LAS unsigned*)(scr + (4 * nl + c_) * 132 + 16 * (2 * (qi) + s_) + 4 * kg) = pg8::pk4_fp8c(Q.v[s_][0][c_] * FP8_WSC, Q.v[s_][1][c_] * FP8_WSC, Q.v[s_][2][c_] * FP8_WSC, Q.v[s_][3][c_] * FP8_WSC); asm volatile("" ::: "memory"); } while (0)
; __device__ __forceinline__ void moe_conv_stream(const Args& a, ARGAS unsigned char* ws, LAS unsigned char* scr, int first, int cnt, int lane) {
;     ...
;     Qt A, B, C, D4;
;     ConvItem cur = moe_conv_desc(a, ws, first, lane);
;     CV_LOAD(0, A, cur); CV_LOAD(1, B, cur); CV_LOAD(2, C, cur);
; #pragma unroll 1
;     for (int i = 0; i < cnt; ++i) {
;         const ConvItem nxt = moe_conv_desc(a, ws, first + 8 * ((i + 1 < cnt) ? i + 1 : i), lane);
;         CV_LOAD(3, D4, cur); CV_PROC(0, A);
;         CV_LOAD(0, A, nxt);  CV_PROC(1, B);
;         CV_LOAD(1, B, nxt);  CV_PROC(2, C);
;         CV_LOAD(2, C, nxt);  CV_PROC(3, D4);
;         LDS_WAIT(); asm volatile("" ::: "memory");
;         const int n0 = cur.gu > 0 ? cur.gu - 1 : -cur.gu - 1;
; #pragma unroll
;         for (int j = 0; j < 8; ++j) { const int row = (lane >> 3) + 8 * j; const LAS unsigned* s = (const LAS unsigned*)(scr + row * 132 + 16 * c8);
;             u32x4 o; o.x = s[0]; o.y = s[1]; o.z = s[2]; o.w = s[3];
;             const int n = n0 + row, wr_ = cur.gu > 0 ? RmGu()(n) : n;
;             *(u32x4*)(cur.dst + (size_t)wr_ * cur.ldk + 16 * c8) = o; }
	v_mul_f32_e32 v112, 0x43000000, v112
	v_med3_f32 v116, v124, s37, v149
	v_med3_f32 v112, v112, s37, v149
	v_cvt_pk_fp8_f32 v150, v116, v112 op_sel:[0,0,1]
	v_mul_f32_e32 v112, 0x43000000, v117
	v_mul_f32_e32 v116, 0x43000000, v121
	v_med3_f32 v112, v112, s37, v149
	v_med3_f32 v116, v116, s37, v149
	v_mov_b32_e32 v120, v129
	v_cvt_pk_fp8_f32 v120, v112, v116
	v_mul_f32_e32 v117, 0x43000000, v125
	v_mul_f32_e32 v112, 0x43000000, v113
	v_med3_f32 v113, v117, s37, v149
	v_med3_f32 v112, v112, s37, v149
	v_cvt_pk_fp8_f32 v120, v113, v112 op_sel:[0,0,1]
	v_mul_f32_e32 v112, 0x43000000, v118
	v_mul_f32_e32 v113, 0x43000000, v122
	v_med3_f32 v112, v112, s37, v149
	v_med3_f32 v113, v113, s37, v149
	v_mov_b32_e32 v117, v129
	v_cvt_pk_fp8_f32 v117, v112, v113
	v_mul_f32_e32 v116, 0x43000000, v126
	v_mul_f32_e32 v112, 0x43000000, v114
	v_med3_f32 v113, v116, s37, v149
	v_med3_f32 v112, v112, s37, v149
	v_cvt_pk_fp8_f32 v117, v113, v112 op_sel:[0,0,1]
	v_mul_f32_e32 v112, 0x43000000, v119
	v_mul_f32_e32 v113, 0x43000000, v123
	v_med3_f32 v112, v112, s37, v149
	v_med3_f32 v113, v113, s37, v149
	v_mov_b32_e32 v116, v129
	v_cvt_pk_fp8_f32 v116, v112, v113
	v_mul_f32_e32 v114, 0x43000000, v127
	v_mul_f32_e32 v112, 0x43000000, v115
	v_med3_f32 v113, v114, s37, v149
	v_med3_f32 v112, v112, s37, v149
	s_waitcnt vmcnt(19)
	v_mul_f32_e32 v100, 0x43000000, v100
	s_waitcnt vmcnt(18)
	v_mul_f32_e32 v104, 0x43000000, v104
	v_cvt_pk_fp8_f32 v116, v113, v112 op_sel:[0,0,1]
	v_med3_f32 v100, v100, s37, v149
	v_med3_f32 v104, v104, s37, v149
	v_mov_b32_e32 v112, v129
	v_cvt_pk_fp8_f32 v112, v100, v104
	s_waitcnt vmcnt(17)
	v_mul_f32_e32 v108, 0x43000000, v108
	s_waitcnt vmcnt(16)
	v_mul_f32_e32 v96, 0x43000000, v96
	v_med3_f32 v100, v108, s37, v149
	v_med3_f32 v96, v96, s37, v149
	v_cvt_pk_fp8_f32 v112, v100, v96 op_sel:[0,0,1]
	v_mul_f32_e32 v96, 0x43000000, v101
	v_mul_f32_e32 v100, 0x43000000, v105
	v_med3_f32 v96, v96, s37, v149
	v_med3_f32 v100, v100, s37, v149
	v_mov_b32_e32 v104, v129
	v_cvt_pk_fp8_f32 v104, v96, v100
	v_mul_f32_e32 v101, 0x43000000, v109
	v_mul_f32_e32 v96, 0x43000000, v97
	v_med3_f32 v97, v101, s37, v149
	v_med3_f32 v96, v96, s37, v149
	s_lshl_b32 s6, s13, 8
	v_cvt_pk_fp8_f32 v104, v97, v96 op_sel:[0,0,1]
	v_mul_f32_e32 v96, 0x43000000, v102
	v_mul_f32_e32 v97, 0x43000000, v106
	v_lshl_add_u64 v[64:65], v[132:133], 0, s[6:7]
	s_mul_i32 s6, s13, 0x104
	v_med3_f32 v96, v96, s37, v149
	v_med3_f32 v97, v97, s37, v149
	v_mov_b32_e32 v101, v129
	v_lshl_add_u64 v[66:67], v[132:133], 0, s[6:7]
	s_mul_i32 s6, s13, 0x108
	v_cvt_pk_fp8_f32 v101, v96, v97
	global_load_dwordx4 v[72:75], v[64:65], off nt
	global_load_dwordx4 v[80:83], v[66:67], off nt
	v_lshl_add_u64 v[64:65], v[132:133], 0, s[6:7]
	s_mul_i32 s6, s13, 0x10c
	v_lshl_add_u64 v[66:67], v[132:133], 0, s[6:7]
	s_mul_i32 s6, s13, 0x140
	v_mul_f32_e32 v100, 0x43000000, v110
	v_mul_f32_e32 v96, 0x43000000, v98
	global_load_dwordx4 v[92:95], v[64:65], off nt
	global_load_dwordx4 v[88:91], v[66:67], off nt
	v_lshl_add_u64 v[64:65], v[132:133], 0, s[6:7]
	s_mul_i32 s6, s13, 0x144
	v_med3_f32 v97, v100, s37, v149
	v_med3_f32 v96, v96, s37, v149
	v_lshl_add_u64 v[68:69], v[132:133], 0, s[6:7]
	s_mul_i32 s6, s13, 0x148
	v_cvt_pk_fp8_f32 v101, v97, v96 op_sel:[0,0,1]
	v_mul_f32_e32 v96, 0x43000000, v103
	v_mul_f32_e32 v97, 0x43000000, v107
	v_lshl_add_u64 v[76:77], v[132:133], 0, s[6:7]
	s_mul_i32 s6, s13, 0x14c
	v_med3_f32 v96, v96, s37, v149
	v_med3_f32 v97, v97, s37, v149
	v_mov_b32_e32 v100, v129
	v_lshl_add_u64 v[78:79], v[132:133], 0, s[6:7]
	v_cvt_pk_fp8_f32 v100, v96, v97
	s_add_i32 s6, s40, -1
	s_not_b32 s12, s40
	s_cmp_gt_i32 s40, 0
	global_load_dwordx4 v[64:67], v[64:65], off nt
	s_nop 0
	global_load_dwordx4 v[68:71], v[68:69], off nt
	s_nop 0
	global_load_dwordx4 v[84:87], v[76:77], off nt
	s_nop 0
	global_load_dwordx4 v[76:79], v[78:79], off nt
	v_mul_f32_e32 v98, 0x43000000, v111
	v_mul_f32_e32 v96, 0x43000000, v99
	s_cselect_b64 vcc, -1, 0
	v_med3_f32 v97, v98, s37, v149
	v_med3_f32 v96, v96, s37, v149
	s_and_b64 s[14:15], vcc, exec
	v_cvt_pk_fp8_f32 v100, v97, v96 op_sel:[0,0,1]
	s_cselect_b32 s6, s6, s12
	ds_write2_b32 v146, v150, v112 offset0:24 offset1:28
	ds_write2_b32 v146, v120, v104 offset0:57 offset1:61
	ds_write2_b32 v146, v117, v101 offset0:90 offset1:94
	ds_write2_b32 v146, v116, v100 offset0:123 offset1:127
	v_add_u32_e32 v100, s6, v194
	v_lshlrev_b32_e32 v101, 1, v100
	v_ashrrev_i32_e32 v102, 3, v100
	s_waitcnt lgkmcnt(0)
; #define LAS __attribute__((address_space(3)))
; #define LDS_WAIT() asm volatile("s_waitcnt lgkmcnt(0)" ::: "memory")
; __device__ __forceinline__ void moe_conv_stream(const Args& a, ARGAS unsigned char* ws, LAS unsigned char* scr, int first, int cnt, int lane) {
;     ...
;         LDS_WAIT(); asm volatile("" ::: "memory");
;         const int n0 = cur.gu > 0 ? cur.gu - 1 : -cur.gu - 1;
; #pragma unroll
;         for (int j = 0; j < 8; ++j) { const int row = (lane >> 3) + 8 * j; const LAS unsigned* s = (const LAS unsigned*)(scr + row * 132 + 16 * c8);
;             u32x4 o; o.x = s[0]; o.y = s[1]; o.z = s[2]; o.w = s[3];
;             const int n = n0 + row, wr_ = cur.gu > 0 ? RmGu()(n) : n;
;             *(u32x4*)(cur.dst + (size_t)wr_ * cur.ldk + 16 * c8) = o; }
;         LDS_WAIT(); asm volatile("" ::: "memory");
;         cur = nxt;
	v_and_b32_e32 v101, 0x700, v101
	v_and_b32_e32 v102, 0xffffff80, v102
	v_add_u32_e32 v101, v101, v102
	ds_read2_b32 v[96:97], v147 offset1:1
	ds_read2_b32 v[98:99], v147 offset0:2 offset1:3
	v_and_or_b32 v101, v100, s38, v101
	v_cndmask_b32_e32 v100, v100, v101, vcc
	v_ashrrev_i32_e32 v101, 31, v100
	v_lshl_add_u64 v[104:105], s[8:9], 0, v[130:131]
	v_lshlrev_b64 v[100:101], 10, v[100:101]
	v_lshl_add_u64 v[106:107], v[104:105], 0, v[100:101]
	v_add_u32_e32 v100, 0x420, v147
	v_add_u32_e32 v102, 0x428, v147
	ds_read2_b32 v[100:101], v100 offset1:1
	ds_read2_b32 v[102:103], v102 offset1:1
	s_waitcnt lgkmcnt(2)
	global_store_dwordx4 v[106:107], v[96:99], off
	s_add_i32 s41, s41, 8
	s_cmpk_eq_i32 s41, 0x88
	v_add_u32_e32 v96, s6, v137
	v_lshlrev_b32_e32 v97, 1, v96
	v_ashrrev_i32_e32 v98, 3, v96
	v_and_b32_e32 v97, 0x700, v97
	v_and_b32_e32 v98, 0xffffff80, v98
	v_add_u32_e32 v97, v97, v98
	v_and_or_b32 v97, v96, s38, v97
	v_cndmask_b32_e32 v96, v96, v97, vcc
	v_ashrrev_i32_e32 v97, 31, v96
	v_lshlrev_b64 v[96:97], 10, v[96:97]
	v_lshl_add_u64 v[96:97], v[104:105], 0, v[96:97]
	s_waitcnt lgkmcnt(0)
	global_store_dwordx4 v[96:97], v[100:103], off
	v_add_u32_e32 v96, 0x840, v147
	v_add_u32_e32 v98, 0x848, v147
	v_add_u32_e32 v100, s6, v138
	v_lshlrev_b32_e32 v101, 1, v100
	v_ashrrev_i32_e32 v102, 3, v100
	v_and_b32_e32 v101, 0x700, v101
	v_and_b32_e32 v102, 0xffffff80, v102
	v_add_u32_e32 v101, v101, v102
	ds_read2_b32 v[96:97], v96 offset1:1
	ds_read2_b32 v[98:99], v98 offset1:1
	v_and_or_b32 v101, v100, s38, v101
	v_cndmask_b32_e32 v100, v100, v101, vcc
	v_ashrrev_i32_e32 v101, 31, v100
	v_lshlrev_b64 v[100:101], 10, v[100:101]
	v_lshl_add_u64 v[106:107], v[104:105], 0, v[100:101]
	v_add_u32_e32 v100, 0xc60, v147
	v_add_u32_e32 v102, 0xc68, v147
	ds_read2_b32 v[100:101], v100 offset1:1
	ds_read2_b32 v[102:103], v102 offset1:1
	s_waitcnt lgkmcnt(2)
	global_store_dwordx4 v[106:107], v[96:99], off
	s_mov_b32 s40, s42
	s_mov_b64 s[8:9], s[10:11]
	v_add_u32_e32 v96, s6, v139
	v_lshlrev_b32_e32 v97, 1, v96
	v_ashrrev_i32_e32 v98, 3, v96
	v_and_b32_e32 v97, 0x700, v97
	v_and_b32_e32 v98, 0xffffff80, v98
	v_add_u32_e32 v97, v97, v98
	v_and_or_b32 v97, v96, s38, v97
	v_cndmask_b32_e32 v96, v96, v97, vcc
	v_ashrrev_i32_e32 v97, 31, v96
	v_lshlrev_b64 v[96:97], 10, v[96:97]
	v_lshl_add_u64 v[96:97], v[104:105], 0, v[96:97]
	s_waitcnt lgkmcnt(0)
	global_store_dwordx4 v[96:97], v[100:103], off
	v_add_u32_e32 v96, 0x1080, v147
	v_add_u32_e32 v98, 0x1088, v147
	v_add_u32_e32 v100, s6, v140
	v_lshlrev_b32_e32 v101, 1, v100
	v_ashrrev_i32_e32 v102, 3, v100
	v_and_b32_e32 v101, 0x700, v101
	v_and_b32_e32 v102, 0xffffff80, v102
	v_add_u32_e32 v101, v101, v102
	ds_read2_b32 v[96:97], v96 offset1:1
	ds_read2_b32 v[98:99], v98 offset1:1
	v_and_or_b32 v101, v100, s38, v101
	v_cndmask_b32_e32 v100, v100, v101, vcc
	v_ashrrev_i32_e32 v101, 31, v100
	v_lshlrev_b64 v[100:101], 10, v[100:101]
	v_lshl_add_u64 v[106:107], v[104:105], 0, v[100:101]
	v_add_u32_e32 v100, 0x14a0, v147
	v_add_u32_e32 v102, 0x14a8, v147
	ds_read2_b32 v[100:101], v100 offset1:1
	ds_read2_b32 v[102:103], v102 offset1:1
	s_waitcnt lgkmcnt(2)
	global_store_dwordx4 v[106:107], v[96:99], off
	s_nop 1
	v_add_u32_e32 v96, s6, v141
	v_lshlrev_b32_e32 v97, 1, v96
	v_ashrrev_i32_e32 v98, 3, v96
	v_and_b32_e32 v97, 0x700, v97
	v_and_b32_e32 v98, 0xffffff80, v98
	v_add_u32_e32 v97, v97, v98
	v_and_or_b32 v97, v96, s38, v97
	v_cndmask_b32_e32 v96, v96, v97, vcc
	v_ashrrev_i32_e32 v97, 31, v96
	v_lshlrev_b64 v[96:97], 10, v[96:97]
	v_lshl_add_u64 v[96:97], v[104:105], 0, v[96:97]
	s_waitcnt lgkmcnt(0)
	global_store_dwordx4 v[96:97], v[100:103], off
	v_add_u32_e32 v96, 0x18c0, v147
	v_add_u32_e32 v98, 0x18c8, v147
	v_add_u32_e32 v100, s6, v142
	v_lshlrev_b32_e32 v101, 1, v100
	v_ashrrev_i32_e32 v102, 3, v100
	v_and_b32_e32 v101, 0x700, v101
	v_and_b32_e32 v102, 0xffffff80, v102
	v_add_u32_e32 v101, v101, v102
	ds_read2_b32 v[96:97], v96 offset1:1
	ds_read2_b32 v[98:99], v98 offset1:1
	v_and_or_b32 v101, v100, s38, v101
	v_cndmask_b32_e32 v100, v100, v101, vcc
	v_ashrrev_i32_e32 v101, 31, v100
	v_lshlrev_b64 v[100:101], 10, v[100:101]
	v_lshl_add_u64 v[106:107], v[104:105], 0, v[100:101]
	v_add_u32_e32 v100, 0x1ce0, v147
	v_add_u32_e32 v102, 0x1ce8, v147
	ds_read2_b32 v[100:101], v100 offset1:1
	ds_read2_b32 v[102:103], v102 offset1:1
	s_waitcnt lgkmcnt(2)
	global_store_dwordx4 v[106:107], v[96:99], off
	s_nop 1
	v_add_u32_e32 v96, s6, v143
	v_lshlrev_b32_e32 v97, 1, v96
	v_ashrrev_i32_e32 v98, 3, v96
	v_and_b32_e32 v97, 0x700, v97
	v_and_b32_e32 v98, 0xffffff80, v98
	v_add_u32_e32 v97, v97, v98
	v_and_or_b32 v97, v96, s38, v97
	v_cndmask_b32_e32 v96, v96, v97, vcc
	v_ashrrev_i32_e32 v97, 31, v96
	v_lshlrev_b64 v[96:97], 10, v[96:97]
	v_lshl_add_u64 v[96:97], v[104:105], 0, v[96:97]
	s_waitcnt lgkmcnt(0)
	global_store_dwordx4 v[96:97], v[100:103], off
	s_waitcnt lgkmcnt(0)
	s_mov_b32 s6, s13
	v_mov_b64_e32 v[96:97], v[132:133]
	s_cbranch_scc1 .LBB0_3115

; #define CV_LOAD(qi, Q, D) do { _Pragma("unroll") for (int s_ = 0; s_ < 2; ++s_) _Pragma("unroll") for (int r_ = 0; r_ < 4; ++r_) Q.v[s_][r_] = *(const f32x4*)(D.src + (size_t)(16 * (2 * (qi) + s_) + r_) * D.N); asm volatile("" ::: "memory"); } while (0)
; #define CV_PROC(qi, Q) do { _Pragma("unroll") for (int s_ = 0; s_ < 2; ++s_) _Pragma("unroll") for (int c_ = 0; c_ < 4; ++c_) \
;         *(LAS unsigned*)(scr + (4 * nl + c_) * 132 + 16 * (2 * (qi) + s_) + 4 * kg) = pg8::pk4_fp8c(Q.v[s_][0][c_] * FP8_WSC, Q.v[s_][1][c_] * FP8_WSC, Q.v[s_][2][c_] * FP8_WSC, Q.v[s_][3][c_] * FP8_WSC); asm volatile("" ::: "memory"); } while (0)
; __device__ __forceinline__ void moe_conv_stream(const Args& a, ARGAS unsigned char* ws, LAS unsigned char* scr, int first, int cnt, int lane) {
;     ...
;     Qt A, B, C, D4;
;     ConvItem cur = moe_conv_desc(a, ws, first, lane);
;     CV_LOAD(0, A, cur); CV_LOAD(1, B, cur); CV_LOAD(2, C, cur);
; #pragma unroll 1
;     for (int i = 0; i < cnt; ++i) {
;         const ConvItem nxt = moe_conv_desc(a, ws, first + 8 * ((i + 1 < cnt) ? i + 1 : i), lane);
;         CV_LOAD(3, D4, cur); CV_PROC(0, A);
.LBB0_3206:
	v_lshl_add_u64 v[96:97], v[0:1], 0, v[128:129]
	s_lshl_b32 s6, s11, 2
	v_lshl_add_u64 v[0:1], v[96:97], 0, s[6:7]
	s_lshl_b32 s6, s11, 3
	v_lshl_add_u64 v[2:3], v[96:97], 0, s[6:7]
	s_mul_i32 s6, s11, 12
	s_waitcnt vmcnt(26)
	v_lshl_add_u64 v[4:5], v[96:97], 0, s[6:7]
	s_lshl_b32 s6, s11, 6
	v_lshl_add_u64 v[6:7], v[96:97], 0, s[6:7]
	s_mul_i32 s6, s11, 0x44
	s_waitcnt vmcnt(24)
	v_lshl_add_u64 v[12:13], v[96:97], 0, s[6:7]
	s_mul_i32 s6, s11, 0x48
	v_lshl_add_u64 v[14:15], v[96:97], 0, s[6:7]
	s_mul_i32 s6, s11, 0x4c
	s_waitcnt vmcnt(19)
	v_lshl_add_u64 v[32:33], v[96:97], 0, s[6:7]
	s_lshl_b32 s6, s11, 7
	global_load_dwordx4 v[16:19], v[0:1], off nt
	global_load_dwordx4 v[20:23], v[2:3], off nt
	global_load_dwordx4 v[24:27], v[4:5], off nt
	s_nop 0
	global_load_dwordx4 v[0:3], v[6:7], off nt
	s_nop 0
	global_load_dwordx4 v[4:7], v[12:13], off nt
	global_load_dwordx4 v[8:11], v[14:15], off nt
	global_load_dwordx4 v[28:31], v[96:97], off nt
	s_nop 0
	global_load_dwordx4 v[12:15], v[32:33], off nt
	v_lshl_add_u64 v[32:33], v[96:97], 0, s[6:7]
	s_mul_i32 s6, s11, 0x84
	v_lshl_add_u64 v[34:35], v[96:97], 0, s[6:7]
	s_mul_i32 s6, s11, 0x88
	global_load_dwordx4 v[40:43], v[32:33], off nt
	global_load_dwordx4 v[48:51], v[34:35], off nt
	v_lshl_add_u64 v[32:33], v[96:97], 0, s[6:7]
	s_mul_i32 s6, s11, 0x8c
	v_lshl_add_u64 v[34:35], v[96:97], 0, s[6:7]
	s_mul_i32 s6, s11, 0xc0
	s_waitcnt vmcnt(26)
	v_lshl_add_u64 v[44:45], v[96:97], 0, s[6:7]
	s_mul_i32 s6, s11, 0xc4
	v_lshl_add_u64 v[46:47], v[96:97], 0, s[6:7]
	s_mul_i32 s6, s11, 0xc8
	s_waitcnt vmcnt(21)
	v_lshl_add_u64 v[64:65], v[96:97], 0, s[6:7]
	s_mul_i32 s6, s11, 0xcc
	v_lshl_add_u64 v[66:67], v[96:97], 0, s[6:7]
	s_lshl_b32 s6, s11, 8
	global_load_dwordx4 v[60:63], v[32:33], off nt
	global_load_dwordx4 v[56:59], v[34:35], off nt
	s_nop 0
	global_load_dwordx4 v[32:35], v[44:45], off nt
	global_load_dwordx4 v[36:39], v[46:47], off nt
	global_load_dwordx4 v[52:55], v[64:65], off nt
	s_nop 0
	global_load_dwordx4 v[44:47], v[66:67], off nt
	v_lshl_add_u64 v[64:65], v[96:97], 0, s[6:7]
	s_mul_i32 s6, s11, 0x104
	v_lshl_add_u64 v[66:67], v[96:97], 0, s[6:7]
	s_mul_i32 s6, s11, 0x108
	global_load_dwordx4 v[72:75], v[64:65], off nt
	global_load_dwordx4 v[80:83], v[66:67], off nt
	v_lshl_add_u64 v[64:65], v[96:97], 0, s[6:7]
	s_mul_i32 s6, s11, 0x10c
	v_lshl_add_u64 v[66:67], v[96:97], 0, s[6:7]
	s_mul_i32 s6, s11, 0x140
	s_waitcnt vmcnt(26)
	v_lshl_add_u64 v[76:77], v[96:97], 0, s[6:7]
	s_mul_i32 s6, s11, 0x144
	v_lshl_add_u64 v[78:79], v[96:97], 0, s[6:7]
	s_mul_i32 s6, s11, 0x148
	v_lshl_add_u64 v[98:99], v[96:97], 0, s[6:7]
	s_mul_i32 s6, s11, 0x14c
	global_load_dwordx4 v[92:95], v[64:65], off nt
	global_load_dwordx4 v[88:91], v[66:67], off nt
	s_nop 0
	global_load_dwordx4 v[64:67], v[76:77], off nt
	global_load_dwordx4 v[68:71], v[78:79], off nt
	v_lshl_add_u64 v[100:101], v[96:97], 0, s[6:7]
	global_load_dwordx4 v[84:87], v[98:99], off nt
	global_load_dwordx4 v[76:79], v[100:101], off nt
	s_mov_b32 s39, 8
	s_mov_b32 s6, s11
	s_branch .LBB0_3208
.LBB0_3207:
	s_waitcnt vmcnt(17)
	v_mul_f32_e32 v28, 0x43000000, v28
	v_mul_f32_e32 v16, 0x43000000, v16
	v_med3_f32 v28, v28, s27, v147
	v_med3_f32 v16, v16, s27, v147
	v_mov_b32_e32 v148, v129
	v_cvt_pk_fp8_f32 v148, v28, v16
	v_mul_f32_e32 v20, 0x43000000, v20
	v_mul_f32_e32 v16, 0x43000000, v24
	v_med3_f32 v20, v20, s27, v147
	v_med3_f32 v16, v16, s27, v147
	v_cvt_pk_fp8_f32 v148, v20, v16 op_sel:[0,0,1]
	v_mul_f32_e32 v16, 0x43000000, v29
	v_mul_f32_e32 v17, 0x43000000, v17
	v_mul_f32_e32 v20, 0x43000000, v21
	v_med3_f32 v16, v16, s27, v147
	v_med3_f32 v17, v17, s27, v147
	v_mov_b32_e32 v21, v129
	v_cvt_pk_fp8_f32 v21, v16, v17
	v_mul_f32_e32 v16, 0x43000000, v25
	v_med3_f32 v17, v20, s27, v147
	v_med3_f32 v16, v16, s27, v147
	v_cvt_pk_fp8_f32 v21, v17, v16 op_sel:[0,0,1]
	v_mul_f32_e32 v16, 0x43000000, v30
	v_mul_f32_e32 v17, 0x43000000, v18
	v_med3_f32 v16, v16, s27, v147
	v_med3_f32 v17, v17, s27, v147
	v_mov_b32_e32 v20, v129
	v_cvt_pk_fp8_f32 v20, v16, v17
	v_mul_f32_e32 v18, 0x43000000, v22
	v_mul_f32_e32 v16, 0x43000000, v26
	v_med3_f32 v17, v18, s27, v147
	v_med3_f32 v16, v16, s27, v147
	v_cvt_pk_fp8_f32 v20, v17, v16 op_sel:[0,0,1]
	v_mul_f32_e32 v16, 0x43000000, v31
	v_mul_f32_e32 v17, 0x43000000, v19
	v_med3_f32 v16, v16, s27, v147
	v_med3_f32 v17, v17, s27, v147
	v_mov_b32_e32 v19, v129
	v_cvt_pk_fp8_f32 v19, v16, v17
	v_mul_f32_e32 v18, 0x43000000, v23
	v_mul_f32_e32 v16, 0x43000000, v27
	v_med3_f32 v17, v18, s27, v147
	v_med3_f32 v16, v16, s27, v147
	v_mul_f32_e32 v0, 0x43000000, v0
	v_mul_f32_e32 v4, 0x43000000, v4
	v_cvt_pk_fp8_f32 v19, v17, v16 op_sel:[0,0,1]
	v_med3_f32 v0, v0, s27, v147
	v_med3_f32 v4, v4, s27, v147
	v_mov_b32_e32 v16, v129
	v_cvt_pk_fp8_f32 v16, v0, v4
	v_mul_f32_e32 v8, 0x43000000, v8
	s_waitcnt vmcnt(16)
; #define CV_LOAD(qi, Q, D) do { _Pragma("unroll") for (int s_ = 0; s_ < 2; ++s_) _Pragma("unroll") for (int r_ = 0; r_ < 4; ++r_) Q.v[s_][r_] = *(const f32x4*)(D.src + (size_t)(16 * (2 * (qi) + s_) + r_) * D.N); asm volatile("" ::: "memory"); } while (0)
; #define CV_PROC(qi, Q) do { _Pragma("unroll") for (int s_ = 0; s_ < 2; ++s_) _Pragma("unroll") for (int c_ = 0; c_ < 4; ++c_) \
;         *(LAS unsigned*)(scr + (4 * nl + c_) * 132 + 16 * (2 * (qi) + s_) + 4 * kg) = pg8::pk4_fp8c(Q.v[s_][0][c_] * FP8_WSC, Q.v[s_][1][c_] * FP8_WSC, Q.v[s_][2][c_] * FP8_WSC, Q.v[s_][3][c_] * FP8_WSC); asm volatile("" ::: "memory"); } while (0)
; __device__ __forceinline__ void moe_conv_stream(const Args& a, ARGAS unsigned char* ws, LAS unsigned char* scr, int first, int cnt, int lane) {
;     ...
;     Qt A, B, C, D4;
;     ConvItem cur = moe_conv_desc(a, ws, first, lane);
;     CV_LOAD(0, A, cur); CV_LOAD(1, B, cur); CV_LOAD(2, C, cur);
; #pragma unroll 1
;     for (int i = 0; i < cnt; ++i) {
;         const ConvItem nxt = moe_conv_desc(a, ws, first + 8 * ((i + 1 < cnt) ? i + 1 : i), lane);
;         CV_LOAD(3, D4, cur); CV_PROC(0, A);
;         CV_LOAD(0, A, nxt);  CV_PROC(1, B);
;         CV_LOAD(1, B, nxt);  CV_PROC(2, C);
;         CV_LOAD(2, C, nxt);  CV_PROC(3, D4);
	v_mul_f32_e32 v0, 0x43000000, v12
	v_med3_f32 v4, v8, s27, v147
	v_med3_f32 v0, v0, s27, v147
	v_cvt_pk_fp8_f32 v16, v4, v0 op_sel:[0,0,1]
	v_mul_f32_e32 v0, 0x43000000, v1
	v_mul_f32_e32 v1, 0x43000000, v5
	v_med3_f32 v0, v0, s27, v147
	v_med3_f32 v1, v1, s27, v147
	v_mov_b32_e32 v5, v129
	v_cvt_pk_fp8_f32 v5, v0, v1
	v_mul_f32_e32 v4, 0x43000000, v9
	v_mul_f32_e32 v0, 0x43000000, v13
	v_med3_f32 v1, v4, s27, v147
	v_med3_f32 v0, v0, s27, v147
	v_cvt_pk_fp8_f32 v5, v1, v0 op_sel:[0,0,1]
	v_mul_f32_e32 v0, 0x43000000, v2
	v_mul_f32_e32 v1, 0x43000000, v6
	v_med3_f32 v0, v0, s27, v147
	v_med3_f32 v1, v1, s27, v147
	v_mov_b32_e32 v4, v129
	v_cvt_pk_fp8_f32 v4, v0, v1
	v_mad_u64_u32 v[96:97], s[14:15], s6, v146, v[96:97]
	v_mul_f32_e32 v2, 0x43000000, v10
	v_mul_f32_e32 v0, 0x43000000, v14
	s_lshl_b64 s[14:15], s[6:7], 2
	v_med3_f32 v1, v2, s27, v147
	v_med3_f32 v0, v0, s27, v147
	v_lshl_add_u64 v[132:133], v[98:99], 0, v[128:129]
	v_lshl_add_u64 v[98:99], v[96:97], 0, s[14:15]
	v_cvt_pk_fp8_f32 v4, v1, v0 op_sel:[0,0,1]
	v_mul_f32_e32 v0, 0x43000000, v3
	v_mul_f32_e32 v1, 0x43000000, v7
	global_load_dwordx4 v[116:119], v[96:97], off nt
	global_load_dwordx4 v[120:123], v[98:99], off nt
	v_lshl_add_u64 v[96:97], v[98:99], 0, s[14:15]
	v_med3_f32 v0, v0, s27, v147
	v_med3_f32 v1, v1, s27, v147
	v_mov_b32_e32 v3, v129
	v_lshl_add_u64 v[98:99], v[96:97], 0, s[14:15]
	v_cvt_pk_fp8_f32 v3, v0, v1
	global_load_dwordx4 v[124:127], v[96:97], off nt
	global_load_dwordx4 v[112:115], v[98:99], off nt
	v_mad_u64_u32 v[96:97], s[42:43], s6, 52, v[98:99]
	v_lshl_add_u64 v[98:99], v[96:97], 0, s[14:15]
	v_mul_f32_e32 v2, 0x43000000, v11
	v_mul_f32_e32 v0, 0x43000000, v15
	global_load_dwordx4 v[100:103], v[96:97], off nt
	global_load_dwordx4 v[104:107], v[98:99], off nt
	v_lshl_add_u64 v[96:97], v[98:99], 0, s[14:15]
	v_med3_f32 v1, v2, s27, v147
	v_med3_f32 v0, v0, s27, v147
	v_lshl_add_u64 v[98:99], v[96:97], 0, s[14:15]
	v_cvt_pk_fp8_f32 v3, v1, v0 op_sel:[0,0,1]
	s_waitcnt vmcnt(21)
	v_mul_f32_e32 v40, 0x43000000, v40
	s_waitcnt vmcnt(20)
	v_mul_f32_e32 v48, 0x43000000, v48
	global_load_dwordx4 v[108:111], v[96:97], off nt
	s_nop 0
	global_load_dwordx4 v[96:99], v[98:99], off nt
	ds_write2_b32 v143, v148, v16 offset1:4
	ds_write2_b32 v143, v21, v5 offset0:33 offset1:37
	ds_write2_b32 v143, v20, v4 offset0:66 offset1:70
	ds_write2_b32 v143, v19, v3 offset0:99 offset1:103
	v_med3_f32 v40, v40, s27, v147
	v_med3_f32 v48, v48, s27, v147
	v_mov_b32_e32 v148, v129
	v_cvt_pk_fp8_f32 v148, v40, v48
	s_waitcnt vmcnt(21)
	v_mul_f32_e32 v60, 0x43000000, v60
	s_waitcnt vmcnt(20)
	v_mul_f32_e32 v40, 0x43000000, v56
	v_med3_f32 v48, v60, s27, v147
	v_med3_f32 v40, v40, s27, v147
	v_cvt_pk_fp8_f32 v148, v48, v40 op_sel:[0,0,1]
	v_mul_f32_e32 v40, 0x43000000, v41
	v_mul_f32_e32 v41, 0x43000000, v49
	v_med3_f32 v40, v40, s27, v147
	v_med3_f32 v41, v41, s27, v147
	v_mov_b32_e32 v49, v129
	v_cvt_pk_fp8_f32 v49, v40, v41
	v_mul_f32_e32 v48, 0x43000000, v61
	v_mul_f32_e32 v40, 0x43000000, v57
	v_med3_f32 v41, v48, s27, v147
	v_med3_f32 v40, v40, s27, v147
	v_cvt_pk_fp8_f32 v49, v41, v40 op_sel:[0,0,1]
	v_mul_f32_e32 v40, 0x43000000, v42
	v_mul_f32_e32 v41, 0x43000000, v50
	v_med3_f32 v40, v40, s27, v147
	v_med3_f32 v41, v41, s27, v147
	v_mov_b32_e32 v48, v129
	v_cvt_pk_fp8_f32 v48, v40, v41
	v_mul_f32_e32 v42, 0x43000000, v62
	v_mul_f32_e32 v40, 0x43000000, v58
	v_med3_f32 v41, v42, s27, v147
	v_med3_f32 v40, v40, s27, v147
	v_cvt_pk_fp8_f32 v48, v41, v40 op_sel:[0,0,1]
	v_mul_f32_e32 v40, 0x43000000, v43
	v_mul_f32_e32 v41, 0x43000000, v51
	v_med3_f32 v40, v40, s27, v147
	v_med3_f32 v41, v41, s27, v147
	v_mov_b32_e32 v43, v129
	v_cvt_pk_fp8_f32 v43, v40, v41
	v_mul_f32_e32 v42, 0x43000000, v63
	v_mul_f32_e32 v40, 0x43000000, v59
	v_med3_f32 v41, v42, s27, v147
	v_med3_f32 v40, v40, s27, v147
	s_waitcnt vmcnt(19)
	v_mul_f32_e32 v32, 0x43000000, v32
	s_waitcnt vmcnt(18)
	v_mul_f32_e32 v36, 0x43000000, v36
	v_cvt_pk_fp8_f32 v43, v41, v40 op_sel:[0,0,1]
	v_med3_f32 v32, v32, s27, v147
	v_med3_f32 v36, v36, s27, v147
	v_mov_b32_e32 v41, v129
	v_cvt_pk_fp8_f32 v41, v32, v36
	s_waitcnt vmcnt(17)
	v_mul_f32_e32 v40, 0x43000000, v52
	s_waitcnt vmcnt(16)
	v_mul_f32_e32 v32, 0x43000000, v44
	v_med3_f32 v36, v40, s27, v147
	v_med3_f32 v32, v32, s27, v147
	v_cvt_pk_fp8_f32 v41, v36, v32 op_sel:[0,0,1]
	v_mul_f32_e32 v32, 0x43000000, v33
	v_mul_f32_e32 v33, 0x43000000, v37
	v_med3_f32 v32, v32, s27, v147
	v_med3_f32 v33, v33, s27, v147
	v_mov_b32_e32 v37, v129
	v_cvt_pk_fp8_f32 v37, v32, v33
	v_mul_f32_e32 v36, 0x43000000, v53
	v_mul_f32_e32 v32, 0x43000000, v45
	v_med3_f32 v33, v36, s27, v147
	v_med3_f32 v32, v32, s27, v147
	v_cvt_pk_fp8_f32 v37, v33, v32 op_sel:[0,0,1]
	v_mul_f32_e32 v32, 0x43000000, v34
	v_mul_f32_e32 v33, 0x43000000, v38
	v_med3_f32 v32, v32, s27, v147
	v_med3_f32 v33, v33, s27, v147
	v_mov_b32_e32 v36, v129
	v_cvt_pk_fp8_f32 v36, v32, v33
	v_mul_f32_e32 v34, 0x43000000, v54
	v_mul_f32_e32 v32, 0x43000000, v46
	s_lshl_b32 s6, s13, 2
	v_med3_f32 v33, v34, s27, v147
	v_med3_f32 v32, v32, s27, v147
	v_lshl_add_u64 v[0:1], v[132:133], 0, s[6:7]
	s_lshl_b32 s6, s13, 3
	v_cvt_pk_fp8_f32 v36, v33, v32 op_sel:[0,0,1]
	v_mul_f32_e32 v32, 0x43000000, v35
	v_mul_f32_e32 v33, 0x43000000, v39
	global_load_dwordx4 v[28:31], v[132:133], off nt
	global_load_dwordx4 v[16:19], v[0:1], off nt
	v_lshl_add_u64 v[0:1], v[132:133], 0, s[6:7]
	s_mul_i32 s6, s13, 12
	v_med3_f32 v32, v32, s27, v147
	v_med3_f32 v33, v33, s27, v147
	v_mov_b32_e32 v35, v129
	v_lshl_add_u64 v[2:3], v[132:133], 0, s[6:7]
	s_lshl_b32 s6, s13, 6
	v_cvt_pk_fp8_f32 v35, v32, v33
	global_load_dwordx4 v[20:23], v[0:1], off nt
	global_load_dwordx4 v[24:27], v[2:3], off nt
	v_lshl_add_u64 v[0:1], v[132:133], 0, s[6:7]
	s_mul_i32 s6, s13, 0x44
	v_lshl_add_u64 v[4:5], v[132:133], 0, s[6:7]
	s_mul_i32 s6, s13, 0x48
	v_mul_f32_e32 v34, 0x43000000, v55
	v_mul_f32_e32 v32, 0x43000000, v47
	v_lshl_add_u64 v[8:9], v[132:133], 0, s[6:7]
	s_mul_i32 s6, s13, 0x4c
	v_med3_f32 v33, v34, s27, v147
	v_med3_f32 v32, v32, s27, v147
	v_lshl_add_u64 v[12:13], v[132:133], 0, s[6:7]
	v_cvt_pk_fp8_f32 v35, v33, v32 op_sel:[0,0,1]
	s_waitcnt vmcnt(19)
; #define CV_LOAD(qi, Q, D) do { _Pragma("unroll") for (int s_ = 0; s_ < 2; ++s_) _Pragma("unroll") for (int r_ = 0; r_ < 4; ++r_) Q.v[s_][r_] = *(const f32x4*)(D.src + (size_t)(16 * (2 * (qi) + s_) + r_) * D.N); asm volatile("" ::: "memory"); } while (0)
; #define CV_PROC(qi, Q) do { _Pragma("unroll") for (int s_ = 0; s_ < 2; ++s_) _Pragma("unroll") for (int c_ = 0; c_ < 4; ++c_) \
;         *(LAS unsigned*)(scr + (4 * nl + c_) * 132 + 16 * (2 * (qi) + s_) + 4 * kg) = pg8::pk4_fp8c(Q.v[s_][0][c_] * FP8_WSC, Q.v[s_][1][c_] * FP8_WSC, Q.v[s_][2][c_] * FP8_WSC, Q.v[s_][3][c_] * FP8_WSC); asm volatile("" ::: "memory"); } while (0)
; __device__ __forceinline__ void moe_conv_stream(const Args& a, ARGAS unsigned char* ws, LAS unsigned char* scr, int first, int cnt, int lane) {
;     ...
;     Qt A, B, C, D4;
;     ConvItem cur = moe_conv_desc(a, ws, first, lane);
;     CV_LOAD(0, A, cur); CV_LOAD(1, B, cur); CV_LOAD(2, C, cur);
; #pragma unroll 1
;     for (int i = 0; i < cnt; ++i) {
;         const ConvItem nxt = moe_conv_desc(a, ws, first + 8 * ((i + 1 < cnt) ? i + 1 : i), lane);
;         CV_LOAD(3, D4, cur); CV_PROC(0, A);
;         CV_LOAD(0, A, nxt);  CV_PROC(1, B);
;         CV_LOAD(1, B, nxt);  CV_PROC(2, C);
;         CV_LOAD(2, C, nxt);  CV_PROC(3, D4);
	v_mul_f32_e32 v72, 0x43000000, v72
	s_waitcnt vmcnt(18)
	v_mul_f32_e32 v80, 0x43000000, v80
	global_load_dwordx4 v[0:3], v[0:1], off nt
	s_nop 0
	global_load_dwordx4 v[4:7], v[4:5], off nt
	s_nop 0
	global_load_dwordx4 v[8:11], v[8:9], off nt
	s_nop 0
	global_load_dwordx4 v[12:15], v[12:13], off nt
	ds_write2_b32 v144, v148, v41 offset0:8 offset1:12
	ds_write2_b32 v144, v49, v37 offset0:41 offset1:45
	ds_write2_b32 v144, v48, v36 offset0:74 offset1:78
	ds_write2_b32 v144, v43, v35 offset0:107 offset1:111
	v_med3_f32 v72, v72, s27, v147
	v_med3_f32 v80, v80, s27, v147
	v_mov_b32_e32 v148, v129
	v_cvt_pk_fp8_f32 v148, v72, v80
	s_waitcnt vmcnt(21)
	v_mul_f32_e32 v92, 0x43000000, v92
	s_waitcnt vmcnt(20)
	v_mul_f32_e32 v72, 0x43000000, v88
	v_med3_f32 v80, v92, s27, v147
	v_med3_f32 v72, v72, s27, v147
	v_cvt_pk_fp8_f32 v148, v80, v72 op_sel:[0,0,1]
	v_mul_f32_e32 v72, 0x43000000, v73
	v_mul_f32_e32 v73, 0x43000000, v81
	v_med3_f32 v72, v72, s27, v147
	v_med3_f32 v73, v73, s27, v147
	v_mov_b32_e32 v81, v129
	v_cvt_pk_fp8_f32 v81, v72, v73
	v_mul_f32_e32 v80, 0x43000000, v93
	v_mul_f32_e32 v72, 0x43000000, v89
	v_med3_f32 v73, v80, s27, v147
	v_med3_f32 v72, v72, s27, v147
	v_cvt_pk_fp8_f32 v81, v73, v72 op_sel:[0,0,1]
	v_mul_f32_e32 v72, 0x43000000, v74
	v_mul_f32_e32 v73, 0x43000000, v82
	v_med3_f32 v72, v72, s27, v147
	v_med3_f32 v73, v73, s27, v147
	v_mov_b32_e32 v80, v129
	v_cvt_pk_fp8_f32 v80, v72, v73
	v_mul_f32_e32 v74, 0x43000000, v94
	v_mul_f32_e32 v72, 0x43000000, v90
	v_med3_f32 v73, v74, s27, v147
	v_med3_f32 v72, v72, s27, v147
	v_cvt_pk_fp8_f32 v80, v73, v72 op_sel:[0,0,1]
	v_mul_f32_e32 v72, 0x43000000, v75
	v_mul_f32_e32 v73, 0x43000000, v83
	v_med3_f32 v72, v72, s27, v147
	v_med3_f32 v73, v73, s27, v147
	v_mov_b32_e32 v75, v129
	v_cvt_pk_fp8_f32 v75, v72, v73
	v_mul_f32_e32 v74, 0x43000000, v95
	v_mul_f32_e32 v72, 0x43000000, v91
	v_med3_f32 v73, v74, s27, v147
	v_med3_f32 v72, v72, s27, v147
	s_waitcnt vmcnt(19)
	v_mul_f32_e32 v64, 0x43000000, v64
	s_waitcnt vmcnt(18)
	v_mul_f32_e32 v68, 0x43000000, v68
	v_cvt_pk_fp8_f32 v75, v73, v72 op_sel:[0,0,1]
	v_med3_f32 v64, v64, s27, v147
	v_med3_f32 v68, v68, s27, v147
	v_mov_b32_e32 v73, v129
	v_cvt_pk_fp8_f32 v73, v64, v68
	s_waitcnt vmcnt(17)
	v_mul_f32_e32 v72, 0x43000000, v84
	s_waitcnt vmcnt(16)
	v_mul_f32_e32 v64, 0x43000000, v76
	v_med3_f32 v68, v72, s27, v147
	v_med3_f32 v64, v64, s27, v147
	v_cvt_pk_fp8_f32 v73, v68, v64 op_sel:[0,0,1]
	v_mul_f32_e32 v64, 0x43000000, v65
	v_mul_f32_e32 v65, 0x43000000, v69
	v_med3_f32 v64, v64, s27, v147
	v_med3_f32 v65, v65, s27, v147
	v_mov_b32_e32 v69, v129
	v_cvt_pk_fp8_f32 v69, v64, v65
	v_mul_f32_e32 v68, 0x43000000, v85
	v_mul_f32_e32 v64, 0x43000000, v77
	v_med3_f32 v65, v68, s27, v147
	v_med3_f32 v64, v64, s27, v147
	v_cvt_pk_fp8_f32 v69, v65, v64 op_sel:[0,0,1]
	v_mul_f32_e32 v64, 0x43000000, v66
	v_mul_f32_e32 v65, 0x43000000, v70
	v_med3_f32 v64, v64, s27, v147
	v_med3_f32 v65, v65, s27, v147
	v_mov_b32_e32 v68, v129
	v_cvt_pk_fp8_f32 v68, v64, v65
	s_lshl_b32 s6, s13, 7
	v_mul_f32_e32 v66, 0x43000000, v86
	v_mul_f32_e32 v64, 0x43000000, v78
	v_lshl_add_u64 v[32:33], v[132:133], 0, s[6:7]
	s_mul_i32 s6, s13, 0x84
	v_med3_f32 v65, v66, s27, v147
	v_med3_f32 v64, v64, s27, v147
	v_lshl_add_u64 v[34:35], v[132:133], 0, s[6:7]
	s_mul_i32 s6, s13, 0x88
	v_cvt_pk_fp8_f32 v68, v65, v64 op_sel:[0,0,1]
	v_mul_f32_e32 v64, 0x43000000, v67
	v_mul_f32_e32 v65, 0x43000000, v71
	global_load_dwordx4 v[40:43], v[32:33], off nt
	global_load_dwordx4 v[48:51], v[34:35], off nt
	v_lshl_add_u64 v[32:33], v[132:133], 0, s[6:7]
	s_mul_i32 s6, s13, 0x8c
	v_med3_f32 v64, v64, s27, v147
	v_med3_f32 v65, v65, s27, v147
	v_mov_b32_e32 v67, v129
	v_lshl_add_u64 v[34:35], v[132:133], 0, s[6:7]
	s_mul_i32 s6, s13, 0xc0
	v_cvt_pk_fp8_f32 v67, v64, v65
	global_load_dwordx4 v[60:63], v[32:33], off nt
	global_load_dwordx4 v[56:59], v[34:35], off nt
	v_lshl_add_u64 v[32:33], v[132:133], 0, s[6:7]
	s_mul_i32 s6, s13, 0xc4
	v_lshl_add_u64 v[36:37], v[132:133], 0, s[6:7]
	s_mul_i32 s6, s13, 0xc8
	v_mul_f32_e32 v66, 0x43000000, v87
	v_mul_f32_e32 v64, 0x43000000, v79
	v_lshl_add_u64 v[44:45], v[132:133], 0, s[6:7]
	s_mul_i32 s6, s13, 0xcc
	v_med3_f32 v65, v66, s27, v147
	v_med3_f32 v64, v64, s27, v147
	v_lshl_add_u64 v[46:47], v[132:133], 0, s[6:7]
	v_cvt_pk_fp8_f32 v67, v65, v64 op_sel:[0,0,1]
	s_waitcnt vmcnt(19)
	v_mul_f32_e32 v116, 0x43000000, v116
	s_waitcnt vmcnt(18)
	v_mul_f32_e32 v120, 0x43000000, v120
	global_load_dwordx4 v[32:35], v[32:33], off nt
	s_nop 0
	global_load_dwordx4 v[36:39], v[36:37], off nt
	s_nop 0
	global_load_dwordx4 v[52:55], v[44:45], off nt
	s_nop 0
	global_load_dwordx4 v[44:47], v[46:47], off nt
	ds_write2_b32 v144, v148, v73 offset0:16 offset1:20
	ds_write2_b32 v144, v81, v69 offset0:49 offset1:53
	ds_write2_b32 v144, v80, v68 offset0:82 offset1:86
	ds_write2_b32 v144, v75, v67 offset0:115 offset1:119
	v_med3_f32 v116, v116, s27, v147
	v_med3_f32 v120, v120, s27, v147
	v_mov_b32_e32 v148, v129
	v_cvt_pk_fp8_f32 v148, v116, v120
	s_waitcnt vmcnt(21)
	v_mul_f32_e32 v124, 0x43000000, v124
	s_waitcnt vmcnt(20)
; #define LDS_WAIT() asm volatile("s_waitcnt lgkmcnt(0)" ::: "memory")
; #define CV_LOAD(qi, Q, D) do { _Pragma("unroll") for (int s_ = 0; s_ < 2; ++s_) _Pragma("unroll") for (int r_ = 0; r_ < 4; ++r_) Q.v[s_][r_] = *(const f32x4*)(D.src + (size_t)(16 * (2 * (qi) + s_) + r_) * D.N); asm volatile("" ::: "memory"); } while (0)
; #define CV_PROC(qi, Q) do { _Pragma("unroll") for (int s_ = 0; s_ < 2; ++s_) _Pragma("unroll") for (int c_ = 0; c_ < 4; ++c_) \
;         *(LAS unsigned*)(scr + (4 * nl + c_) * 132 + 16 * (2 * (qi) + s_) + 4 * kg) = pg8::pk4_fp8c(Q.v[s_][0][c_] * FP8_WSC, Q.v[s_][1][c_] * FP8_WSC, Q.v[s_][2][c_] * FP8_WSC, Q.v[s_][3][c_] * FP8_WSC); asm volatile("" ::: "memory"); } while (0)
; __device__ __forceinline__ void moe_conv_stream(const Args& a, ARGAS unsigned char* ws, LAS unsigned char* scr, int first, int cnt, int lane) {
;     ...
;     Qt A, B, C, D4;
;     ConvItem cur = moe_conv_desc(a, ws, first, lane);
;     CV_LOAD(0, A, cur); CV_LOAD(1, B, cur); CV_LOAD(2, C, cur);
; #pragma unroll 1
;     for (int i = 0; i < cnt; ++i) {
;         const ConvItem nxt = moe_conv_desc(a, ws, first + 8 * ((i + 1 < cnt) ? i + 1 : i), lane);
;         CV_LOAD(3, D4, cur); CV_PROC(0, A);
;         CV_LOAD(0, A, nxt);  CV_PROC(1, B);
;         CV_LOAD(1, B, nxt);  CV_PROC(2, C);
;         CV_LOAD(2, C, nxt);  CV_PROC(3, D4);
;         LDS_WAIT(); asm volatile("" ::: "memory");
;         const int n0 = cur.gu > 0 ? cur.gu - 1 : -cur.gu - 1;
	v_mul_f32_e32 v112, 0x43000000, v112
	v_med3_f32 v116, v124, s27, v147
	v_med3_f32 v112, v112, s27, v147
	v_cvt_pk_fp8_f32 v148, v116, v112 op_sel:[0,0,1]
	v_mul_f32_e32 v112, 0x43000000, v117
	v_mul_f32_e32 v116, 0x43000000, v121
	v_med3_f32 v112, v112, s27, v147
	v_med3_f32 v116, v116, s27, v147
	v_mov_b32_e32 v120, v129
	v_cvt_pk_fp8_f32 v120, v112, v116
	v_mul_f32_e32 v117, 0x43000000, v125
	v_mul_f32_e32 v112, 0x43000000, v113
	v_med3_f32 v113, v117, s27, v147
	v_med3_f32 v112, v112, s27, v147
	v_cvt_pk_fp8_f32 v120, v113, v112 op_sel:[0,0,1]
	v_mul_f32_e32 v112, 0x43000000, v118
	v_mul_f32_e32 v113, 0x43000000, v122
	v_med3_f32 v112, v112, s27, v147
	v_med3_f32 v113, v113, s27, v147
	v_mov_b32_e32 v117, v129
	v_cvt_pk_fp8_f32 v117, v112, v113
	v_mul_f32_e32 v116, 0x43000000, v126
	v_mul_f32_e32 v112, 0x43000000, v114
	v_med3_f32 v113, v116, s27, v147
	v_med3_f32 v112, v112, s27, v147
	v_cvt_pk_fp8_f32 v117, v113, v112 op_sel:[0,0,1]
	v_mul_f32_e32 v112, 0x43000000, v119
	v_mul_f32_e32 v113, 0x43000000, v123
	v_med3_f32 v112, v112, s27, v147
	v_med3_f32 v113, v113, s27, v147
	v_mov_b32_e32 v116, v129
	v_cvt_pk_fp8_f32 v116, v112, v113
	v_mul_f32_e32 v114, 0x43000000, v127
	v_mul_f32_e32 v112, 0x43000000, v115
	v_med3_f32 v113, v114, s27, v147
	v_med3_f32 v112, v112, s27, v147
	s_waitcnt vmcnt(19)
	v_mul_f32_e32 v100, 0x43000000, v100
	s_waitcnt vmcnt(18)
	v_mul_f32_e32 v104, 0x43000000, v104
	v_cvt_pk_fp8_f32 v116, v113, v112 op_sel:[0,0,1]
	v_med3_f32 v100, v100, s27, v147
	v_med3_f32 v104, v104, s27, v147
	v_mov_b32_e32 v112, v129
	v_cvt_pk_fp8_f32 v112, v100, v104
	s_waitcnt vmcnt(17)
	v_mul_f32_e32 v108, 0x43000000, v108
	s_waitcnt vmcnt(16)
	v_mul_f32_e32 v96, 0x43000000, v96
	v_med3_f32 v100, v108, s27, v147
	v_med3_f32 v96, v96, s27, v147
	v_cvt_pk_fp8_f32 v112, v100, v96 op_sel:[0,0,1]
	v_mul_f32_e32 v96, 0x43000000, v101
	v_mul_f32_e32 v100, 0x43000000, v105
	v_med3_f32 v96, v96, s27, v147
	v_med3_f32 v100, v100, s27, v147
	v_mov_b32_e32 v104, v129
	v_cvt_pk_fp8_f32 v104, v96, v100
	v_mul_f32_e32 v101, 0x43000000, v109
	v_mul_f32_e32 v96, 0x43000000, v97
	v_med3_f32 v97, v101, s27, v147
	v_med3_f32 v96, v96, s27, v147
	s_lshl_b32 s6, s13, 8
	v_cvt_pk_fp8_f32 v104, v97, v96 op_sel:[0,0,1]
	v_mul_f32_e32 v96, 0x43000000, v102
	v_mul_f32_e32 v97, 0x43000000, v106
	v_lshl_add_u64 v[64:65], v[132:133], 0, s[6:7]
	s_mul_i32 s6, s13, 0x104
	v_med3_f32 v96, v96, s27, v147
	v_med3_f32 v97, v97, s27, v147
	v_mov_b32_e32 v101, v129
	v_lshl_add_u64 v[66:67], v[132:133], 0, s[6:7]
	s_mul_i32 s6, s13, 0x108
	v_cvt_pk_fp8_f32 v101, v96, v97
	global_load_dwordx4 v[72:75], v[64:65], off nt
	global_load_dwordx4 v[80:83], v[66:67], off nt
	v_lshl_add_u64 v[64:65], v[132:133], 0, s[6:7]
	s_mul_i32 s6, s13, 0x10c
	v_lshl_add_u64 v[66:67], v[132:133], 0, s[6:7]
	s_mul_i32 s6, s13, 0x140
	v_mul_f32_e32 v100, 0x43000000, v110
	v_mul_f32_e32 v96, 0x43000000, v98
	global_load_dwordx4 v[92:95], v[64:65], off nt
	global_load_dwordx4 v[88:91], v[66:67], off nt
	v_lshl_add_u64 v[64:65], v[132:133], 0, s[6:7]
	s_mul_i32 s6, s13, 0x144
	v_med3_f32 v97, v100, s27, v147
	v_med3_f32 v96, v96, s27, v147
	v_lshl_add_u64 v[68:69], v[132:133], 0, s[6:7]
	s_mul_i32 s6, s13, 0x148
	v_cvt_pk_fp8_f32 v101, v97, v96 op_sel:[0,0,1]
	v_mul_f32_e32 v96, 0x43000000, v103
	v_mul_f32_e32 v97, 0x43000000, v107
	v_lshl_add_u64 v[76:77], v[132:133], 0, s[6:7]
	s_mul_i32 s6, s13, 0x14c
	v_med3_f32 v96, v96, s27, v147
	v_med3_f32 v97, v97, s27, v147
	v_mov_b32_e32 v100, v129
	v_lshl_add_u64 v[78:79], v[132:133], 0, s[6:7]
	v_cvt_pk_fp8_f32 v100, v96, v97
	s_add_i32 s6, s38, -1
	s_not_b32 s12, s38
	s_cmp_gt_i32 s38, 0
	global_load_dwordx4 v[64:67], v[64:65], off nt
	s_nop 0
	global_load_dwordx4 v[68:71], v[68:69], off nt
	s_nop 0
	global_load_dwordx4 v[84:87], v[76:77], off nt
	s_nop 0
	global_load_dwordx4 v[76:79], v[78:79], off nt
	v_mul_f32_e32 v98, 0x43000000, v111
	v_mul_f32_e32 v96, 0x43000000, v99
	s_cselect_b64 vcc, -1, 0
	v_med3_f32 v97, v98, s27, v147
	v_med3_f32 v96, v96, s27, v147
	s_and_b64 s[14:15], vcc, exec
	v_cvt_pk_fp8_f32 v100, v97, v96 op_sel:[0,0,1]
	s_cselect_b32 s6, s6, s12
	ds_write2_b32 v144, v148, v112 offset0:24 offset1:28
	ds_write2_b32 v144, v120, v104 offset0:57 offset1:61
	ds_write2_b32 v144, v117, v101 offset0:90 offset1:94
	ds_write2_b32 v144, v116, v100 offset0:123 offset1:127
	v_add_u32_e32 v100, s6, v194
	v_lshlrev_b32_e32 v101, 1, v100
	v_ashrrev_i32_e32 v102, 3, v100
	s_waitcnt lgkmcnt(0)
; #define LAS __attribute__((address_space(3)))
; #define LDS_WAIT() asm volatile("s_waitcnt lgkmcnt(0)" ::: "memory")
; __device__ __forceinline__ void moe_conv_stream(const Args& a, ARGAS unsigned char* ws, LAS unsigned char* scr, int first, int cnt, int lane) {
;     ...
;         LDS_WAIT(); asm volatile("" ::: "memory");
;         const int n0 = cur.gu > 0 ? cur.gu - 1 : -cur.gu - 1;
; #pragma unroll
;         for (int j = 0; j < 8; ++j) { const int row = (lane >> 3) + 8 * j; const LAS unsigned* s = (const LAS unsigned*)(scr + row * 132 + 16 * c8);
;             u32x4 o; o.x = s[0]; o.y = s[1]; o.z = s[2]; o.w = s[3];
;             const int n = n0 + row, wr_ = cur.gu > 0 ? RmGu()(n) : n;
;             *(u32x4*)(cur.dst + (size_t)wr_ * cur.ldk + 16 * c8) = o; }
;         LDS_WAIT(); asm volatile("" ::: "memory");
;         cur = nxt;
	v_and_b32_e32 v101, 0x700, v101
	v_and_b32_e32 v102, 0xffffff80, v102
	v_add_u32_e32 v101, v101, v102
	ds_read2_b32 v[96:97], v145 offset1:1
	ds_read2_b32 v[98:99], v145 offset0:2 offset1:3
	v_and_or_b32 v101, v100, s36, v101
	v_cndmask_b32_e32 v100, v100, v101, vcc
	v_ashrrev_i32_e32 v101, 31, v100
	v_lshl_add_u64 v[104:105], s[8:9], 0, v[130:131]
	v_lshlrev_b64 v[100:101], 10, v[100:101]
	v_lshl_add_u64 v[106:107], v[104:105], 0, v[100:101]
	v_add_u32_e32 v100, 0x420, v145
	v_add_u32_e32 v102, 0x428, v145
	ds_read2_b32 v[100:101], v100 offset1:1
	ds_read2_b32 v[102:103], v102 offset1:1
	s_waitcnt lgkmcnt(2)
	global_store_dwordx4 v[106:107], v[96:99], off
	s_add_i32 s39, s39, 8
	s_cmpk_eq_i32 s39, 0x88
	v_add_u32_e32 v96, s6, v135
	v_lshlrev_b32_e32 v97, 1, v96
	v_ashrrev_i32_e32 v98, 3, v96
	v_and_b32_e32 v97, 0x700, v97
	v_and_b32_e32 v98, 0xffffff80, v98
	v_add_u32_e32 v97, v97, v98
	v_and_or_b32 v97, v96, s36, v97
	v_cndmask_b32_e32 v96, v96, v97, vcc
	v_ashrrev_i32_e32 v97, 31, v96
	v_lshlrev_b64 v[96:97], 10, v[96:97]
	v_lshl_add_u64 v[96:97], v[104:105], 0, v[96:97]
	s_waitcnt lgkmcnt(0)
	global_store_dwordx4 v[96:97], v[100:103], off
	v_add_u32_e32 v96, 0x840, v145
	v_add_u32_e32 v98, 0x848, v145
	v_add_u32_e32 v100, s6, v136
	v_lshlrev_b32_e32 v101, 1, v100
	v_ashrrev_i32_e32 v102, 3, v100
	v_and_b32_e32 v101, 0x700, v101
	v_and_b32_e32 v102, 0xffffff80, v102
	v_add_u32_e32 v101, v101, v102
	ds_read2_b32 v[96:97], v96 offset1:1
	ds_read2_b32 v[98:99], v98 offset1:1
	v_and_or_b32 v101, v100, s36, v101
	v_cndmask_b32_e32 v100, v100, v101, vcc
	v_ashrrev_i32_e32 v101, 31, v100
	v_lshlrev_b64 v[100:101], 10, v[100:101]
	v_lshl_add_u64 v[106:107], v[104:105], 0, v[100:101]
	v_add_u32_e32 v100, 0xc60, v145
	v_add_u32_e32 v102, 0xc68, v145
	ds_read2_b32 v[100:101], v100 offset1:1
	ds_read2_b32 v[102:103], v102 offset1:1
	s_waitcnt lgkmcnt(2)
	global_store_dwordx4 v[106:107], v[96:99], off
	s_mov_b32 s38, s40
	s_mov_b64 s[8:9], s[10:11]
	v_add_u32_e32 v96, s6, v137
	v_lshlrev_b32_e32 v97, 1, v96
	v_ashrrev_i32_e32 v98, 3, v96
	v_and_b32_e32 v97, 0x700, v97
	v_and_b32_e32 v98, 0xffffff80, v98
	v_add_u32_e32 v97, v97, v98
	v_and_or_b32 v97, v96, s36, v97
	v_cndmask_b32_e32 v96, v96, v97, vcc
	v_ashrrev_i32_e32 v97, 31, v96
	v_lshlrev_b64 v[96:97], 10, v[96:97]
	v_lshl_add_u64 v[96:97], v[104:105], 0, v[96:97]
	s_waitcnt lgkmcnt(0)
	global_store_dwordx4 v[96:97], v[100:103], off
	v_add_u32_e32 v96, 0x1080, v145
	v_add_u32_e32 v98, 0x1088, v145
	v_add_u32_e32 v100, s6, v138
	v_lshlrev_b32_e32 v101, 1, v100
	v_ashrrev_i32_e32 v102, 3, v100
	v_and_b32_e32 v101, 0x700, v101
	v_and_b32_e32 v102, 0xffffff80, v102
	v_add_u32_e32 v101, v101, v102
	ds_read2_b32 v[96:97], v96 offset1:1
	ds_read2_b32 v[98:99], v98 offset1:1
	v_and_or_b32 v101, v100, s36, v101
	v_cndmask_b32_e32 v100, v100, v101, vcc
	v_ashrrev_i32_e32 v101, 31, v100
	v_lshlrev_b64 v[100:101], 10, v[100:101]
	v_lshl_add_u64 v[106:107], v[104:105], 0, v[100:101]
	v_add_u32_e32 v100, 0x14a0, v145
	v_add_u32_e32 v102, 0x14a8, v145
	ds_read2_b32 v[100:101], v100 offset1:1
	ds_read2_b32 v[102:103], v102 offset1:1
	s_waitcnt lgkmcnt(2)
	global_store_dwordx4 v[106:107], v[96:99], off
	s_nop 1
	v_add_u32_e32 v96, s6, v139
	v_lshlrev_b32_e32 v97, 1, v96
	v_ashrrev_i32_e32 v98, 3, v96
	v_and_b32_e32 v97, 0x700, v97
	v_and_b32_e32 v98, 0xffffff80, v98
	v_add_u32_e32 v97, v97, v98
	v_and_or_b32 v97, v96, s36, v97
	v_cndmask_b32_e32 v96, v96, v97, vcc
	v_ashrrev_i32_e32 v97, 31, v96
	v_lshlrev_b64 v[96:97], 10, v[96:97]
	v_lshl_add_u64 v[96:97], v[104:105], 0, v[96:97]
	s_waitcnt lgkmcnt(0)
	global_store_dwordx4 v[96:97], v[100:103], off
	v_add_u32_e32 v96, 0x18c0, v145
	v_add_u32_e32 v98, 0x18c8, v145
	v_add_u32_e32 v100, s6, v140
	v_lshlrev_b32_e32 v101, 1, v100
	v_ashrrev_i32_e32 v102, 3, v100
	v_and_b32_e32 v101, 0x700, v101
	v_and_b32_e32 v102, 0xffffff80, v102
	v_add_u32_e32 v101, v101, v102
	ds_read2_b32 v[96:97], v96 offset1:1
	ds_read2_b32 v[98:99], v98 offset1:1
	v_and_or_b32 v101, v100, s36, v101
	v_cndmask_b32_e32 v100, v100, v101, vcc
	v_ashrrev_i32_e32 v101, 31, v100
	v_lshlrev_b64 v[100:101], 10, v[100:101]
	v_lshl_add_u64 v[106:107], v[104:105], 0, v[100:101]
	v_add_u32_e32 v100, 0x1ce0, v145
	v_add_u32_e32 v102, 0x1ce8, v145
	ds_read2_b32 v[100:101], v100 offset1:1
	ds_read2_b32 v[102:103], v102 offset1:1
	s_waitcnt lgkmcnt(2)
	global_store_dwordx4 v[106:107], v[96:99], off
	s_nop 1
	v_add_u32_e32 v96, s6, v141
	v_lshlrev_b32_e32 v97, 1, v96
	v_ashrrev_i32_e32 v98, 3, v96
	v_and_b32_e32 v97, 0x700, v97
	v_and_b32_e32 v98, 0xffffff80, v98
	v_add_u32_e32 v97, v97, v98
	v_and_or_b32 v97, v96, s36, v97
	v_cndmask_b32_e32 v96, v96, v97, vcc
	v_ashrrev_i32_e32 v97, 31, v96
	v_lshlrev_b64 v[96:97], 10, v[96:97]
	v_lshl_add_u64 v[96:97], v[104:105], 0, v[96:97]
	s_waitcnt lgkmcnt(0)
	global_store_dwordx4 v[96:97], v[100:103], off
	s_waitcnt lgkmcnt(0)
	s_mov_b32 s6, s13
	v_mov_b64_e32 v[96:97], v[132:133]
	s_cbranch_scc1 .LBB0_3195
